# stack: mix_post software-pipelined (next group loads issued per item), kmean unroll, split read-back batch, final te/tp/tw preload
# speedup vs baseline: 1.0005x; 1.0005x over previous
.LBB0_783:
	s_or_b64 exec, exec, s[4:5]
	v_mov_b32_e32 v1, s2
	s_waitcnt lgkmcnt(0)
	s_barrier
	v_mbcnt_lo_u32_b32 v0, -1, 0
	v_mbcnt_hi_u32_b32 v0, -1, v0
	s_nop 0
	v_readfirstlane_b32 s16, v1
	v_mov_b32_e32 v1, 0
	s_load_dwordx2 s[4:5], s[52:53], 0x188
	s_lshl_b32 s0, s16, 3
	s_add_i32 s18, s0, s66
	s_cmpk_gt_i32 s18, 0x7fff
	v_readfirstlane_b32 s6, v1
	s_cbranch_scc1 .LBB0_787
	s_ashr_i32 s0, s6, 31
	s_waitcnt lgkmcnt(0)
	s_add_u32 s1, s4, s6
	s_addc_u32 s0, s5, s0
	s_add_u32 s6, s1, 0x4c480000
	s_addc_u32 s7, s0, 0
	s_add_u32 s12, s1, 0x48480000
	s_addc_u32 s13, s0, 0
	s_add_u32 s14, s1, 0x4a480000
	s_addc_u32 s15, s0, 0
	s_load_dwordx4 s[8:11], s[52:53], 0x78
	s_add_u32 s19, s1, 0x4c0000
	s_addc_u32 s20, s0, 0
	s_add_u32 s21, s1, 0x35c80000
	s_addc_u32 s22, s0, 0
	s_lshl_b32 s0, s16, 11
	s_lshl_b32 s1, s66, 8
	v_lshlrev_b32_e32 v0, 2, v0
	s_add_i32 s23, s0, s1
	v_mov_b32_e32 v1, 0x3a27c5ac
	s_mov_b32 s24, 0xf800000
	v_mov_b32_e32 v2, 0x260
	s_waitcnt lgkmcnt(0)
	s_and_b32 s0, s23, 0x300
	v_add_u32_e32 v130, s0, v0
	v_lshlrev_b32_e32 v130, 2, v130
	global_load_dwordx4 v[134:137], v130, s[10:11]
	global_load_dwordx4 v[130:133], v130, s[8:9]
	s_ashr_i32 s4, s18, 2
	s_and_b32 s0, s23, 0x300
	v_add_u32_e32 v16, s0, v0
	s_ashr_i32 s5, s4, 31
	s_lshl_b64 s[16:17], s[4:5], 10
	v_ashrrev_i32_e32 v17, 31, v16
	v_lshl_add_u64 v[4:5], s[16:17], 0, v[16:17]
	v_lshl_add_u64 v[8:9], v[4:5], 2, s[6:7]
	v_lshlrev_b64 v[10:11], 1, v[4:5]
	s_waitcnt lgkmcnt(0)
	global_load_dwordx4 v[4:7], v[8:9], off
	s_lshl_b64 s[26:27], s[4:5], 6
	v_ashrrev_i32_e32 v18, 6, v16
	s_add_u32 s16, s19, s26
	v_ashrrev_i32_e32 v19, 31, v18
	s_addc_u32 s17, s20, s27
	v_lshl_add_u64 v[20:21], s[12:13], 0, v[10:11]
	v_lshl_add_u64 v[22:23], s[14:15], 0, v[10:11]
	s_nop 0
	v_lshl_add_u64 v[18:19], v[18:19], 2, s[16:17]
	global_load_dwordx2 v[20:21], v[20:21], off
	s_nop 0
	global_load_dwordx2 v[22:23], v[22:23], off
	s_nop 0
	global_load_dword v18, v[18:19], off
	s_lshl_b64 s[4:5], s[4:5], 12
	s_add_u32 s4, s21, s4
	s_addc_u32 s5, s22, s5
	v_lshl_add_u64 v[16:17], v[16:17], 1, s[4:5]
	s_add_i32 s0, s18, 0x800
	s_add_i32 s23, s23, 0x80000
	s_cmpk_lt_i32 s18, 0x7800
	s_mov_b32 s18, s0
	s_ashr_i32 s4, s18, 2
	s_and_b32 s0, s23, 0x300
	v_add_u32_e32 v48, s0, v0
	s_ashr_i32 s5, s4, 31
	s_lshl_b64 s[16:17], s[4:5], 10
	v_ashrrev_i32_e32 v49, 31, v48
	v_lshl_add_u64 v[36:37], s[16:17], 0, v[48:49]
	v_lshl_add_u64 v[40:41], v[36:37], 2, s[6:7]
	v_lshlrev_b64 v[42:43], 1, v[36:37]
	s_waitcnt lgkmcnt(0)
	global_load_dwordx4 v[36:39], v[40:41], off
	s_lshl_b64 s[26:27], s[4:5], 6
	v_ashrrev_i32_e32 v50, 6, v48
	s_add_u32 s16, s19, s26
	v_ashrrev_i32_e32 v51, 31, v50
	s_addc_u32 s17, s20, s27
	v_lshl_add_u64 v[52:53], s[12:13], 0, v[42:43]
	v_lshl_add_u64 v[54:55], s[14:15], 0, v[42:43]
	s_nop 0
	v_lshl_add_u64 v[50:51], v[50:51], 2, s[16:17]
	global_load_dwordx2 v[52:53], v[52:53], off
	s_nop 0
	global_load_dwordx2 v[54:55], v[54:55], off
	s_nop 0
	global_load_dword v50, v[50:51], off
	s_lshl_b64 s[4:5], s[4:5], 12
	s_add_u32 s4, s21, s4
	s_addc_u32 s5, s22, s5
	v_lshl_add_u64 v[48:49], v[48:49], 1, s[4:5]
	s_add_i32 s0, s18, 0x800
	s_add_i32 s23, s23, 0x80000
	s_cmpk_lt_i32 s18, 0x7800
	s_mov_b32 s18, s0
	s_ashr_i32 s4, s18, 2
	s_and_b32 s0, s23, 0x300
	v_add_u32_e32 v80, s0, v0
	s_ashr_i32 s5, s4, 31
	s_lshl_b64 s[16:17], s[4:5], 10
	v_ashrrev_i32_e32 v81, 31, v80
	v_lshl_add_u64 v[68:69], s[16:17], 0, v[80:81]
	v_lshl_add_u64 v[72:73], v[68:69], 2, s[6:7]
	v_lshlrev_b64 v[74:75], 1, v[68:69]
	s_waitcnt lgkmcnt(0)
	global_load_dwordx4 v[68:71], v[72:73], off
	s_lshl_b64 s[26:27], s[4:5], 6
	v_ashrrev_i32_e32 v82, 6, v80
	s_add_u32 s16, s19, s26
	v_ashrrev_i32_e32 v83, 31, v82
	s_addc_u32 s17, s20, s27
	v_lshl_add_u64 v[84:85], s[12:13], 0, v[74:75]
	v_lshl_add_u64 v[86:87], s[14:15], 0, v[74:75]
	s_nop 0
	v_lshl_add_u64 v[82:83], v[82:83], 2, s[16:17]
	global_load_dwordx2 v[84:85], v[84:85], off
	s_nop 0
	global_load_dwordx2 v[86:87], v[86:87], off
	s_nop 0
	global_load_dword v82, v[82:83], off
	s_lshl_b64 s[4:5], s[4:5], 12
	s_add_u32 s4, s21, s4
	s_addc_u32 s5, s22, s5
	v_lshl_add_u64 v[80:81], v[80:81], 1, s[4:5]
	s_add_i32 s0, s18, 0x800
	s_add_i32 s23, s23, 0x80000
	s_cmpk_lt_i32 s18, 0x7800
	s_mov_b32 s18, s0
	s_ashr_i32 s4, s18, 2
	s_and_b32 s0, s23, 0x300
	v_add_u32_e32 v112, s0, v0
	s_ashr_i32 s5, s4, 31
	s_lshl_b64 s[16:17], s[4:5], 10
	v_ashrrev_i32_e32 v113, 31, v112
	v_lshl_add_u64 v[100:101], s[16:17], 0, v[112:113]
	v_lshl_add_u64 v[104:105], v[100:101], 2, s[6:7]
	v_lshlrev_b64 v[106:107], 1, v[100:101]
	s_waitcnt lgkmcnt(0)
	global_load_dwordx4 v[100:103], v[104:105], off
	s_lshl_b64 s[26:27], s[4:5], 6
	v_ashrrev_i32_e32 v114, 6, v112
	s_add_u32 s16, s19, s26
	v_ashrrev_i32_e32 v115, 31, v114
	s_addc_u32 s17, s20, s27
	v_lshl_add_u64 v[116:117], s[12:13], 0, v[106:107]
	v_lshl_add_u64 v[118:119], s[14:15], 0, v[106:107]
	s_nop 0
	v_lshl_add_u64 v[114:115], v[114:115], 2, s[16:17]
	global_load_dwordx2 v[116:117], v[116:117], off
	s_nop 0
	global_load_dwordx2 v[118:119], v[118:119], off
	s_nop 0
	global_load_dword v114, v[114:115], off
	s_lshl_b64 s[4:5], s[4:5], 12
	s_add_u32 s4, s21, s4
	s_addc_u32 s5, s22, s5
	v_lshl_add_u64 v[112:113], v[112:113], 1, s[4:5]
	s_add_i32 s0, s18, 0x800
	s_add_i32 s23, s23, 0x80000
	s_cmpk_lt_i32 s18, 0x7800
	s_mov_b32 s18, s0
	s_waitcnt vmcnt(15)
	v_mov_b32_e32 v24, v5
	v_mov_b32_e32 v25, v6
	v_mov_b32_e32 v26, v4
	v_mov_b32_e32 v27, v7
	v_pk_add_f32 v[24:25], v[24:25], v[26:27]
	s_waitcnt vmcnt(14)
	v_lshlrev_b32_e32 v26, 16, v20
	v_add_f32_e32 v3, v24, v25
	v_and_b32_e32 v27, 0xffff0000, v20
	v_lshlrev_b32_e32 v20, 16, v21
	v_add_f32_dpp v3, v3, v3 quad_perm:[1,0,3,2] row_mask:0xf bank_mask:0xf bound_ctrl:1
	v_and_b32_e32 v21, 0xffff0000, v21
	s_waitcnt vmcnt(13)
	v_lshlrev_b32_e32 v28, 16, v22
	v_add_f32_dpp v3, v3, v3 quad_perm:[2,3,0,1] row_mask:0xf bank_mask:0xf bound_ctrl:1
	v_and_b32_e32 v29, 0xffff0000, v22
	v_lshlrev_b32_e32 v22, 16, v23
	v_add_f32_dpp v3, v3, v3 row_half_mirror row_mask:0xf bank_mask:0xf bound_ctrl:1
	v_and_b32_e32 v23, 0xffff0000, v23
	s_nop 0
	v_add_f32_dpp v3, v3, v3 row_mirror row_mask:0xf bank_mask:0xf bound_ctrl:1
	v_fmamk_f32 v5, v3, 0xbc800000, v5
	v_fmamk_f32 v4, v3, 0xbc800000, v4
	v_fmamk_f32 v7, v3, 0xbc800000, v7
	v_fmac_f32_e32 v6, 0xbc800000, v3
	v_pk_mul_f32 v[24:25], v[6:7], v[6:7]
	v_pk_mul_f32 v[30:31], v[4:5], v[4:5]
	s_nop 0
	v_pk_mov_b32 v[32:33], v[30:31], v[24:25] op_sel:[1,0]
	v_mov_b32_e32 v31, v25
	v_pk_add_f32 v[24:25], v[32:33], v[30:31]
	s_nop 0
	v_add_f32_e32 v3, v24, v25
	s_nop 1
	v_add_f32_dpp v3, v3, v3 quad_perm:[1,0,3,2] row_mask:0xf bank_mask:0xf bound_ctrl:1
	s_nop 1
	v_add_f32_dpp v3, v3, v3 quad_perm:[2,3,0,1] row_mask:0xf bank_mask:0xf bound_ctrl:1
	s_nop 1
	v_add_f32_dpp v3, v3, v3 row_half_mirror row_mask:0xf bank_mask:0xf bound_ctrl:1
	s_nop 1
	v_add_f32_dpp v3, v3, v3 row_mirror row_mask:0xf bank_mask:0xf bound_ctrl:1
	v_fmamk_f32 v3, v3, 0x3c800000, v1
	v_mul_f32_e32 v19, 0x4f800000, v3
	v_cmp_gt_f32_e32 vcc, s24, v3
	s_nop 1
	v_cndmask_b32_e32 v3, v3, v19, vcc
	v_sqrt_f32_e32 v19, v3
	s_nop 0
	v_add_u32_e32 v24, -1, v19
	v_add_u32_e32 v25, 1, v19
	v_fma_f32 v30, -v24, v19, v3
	v_fma_f32 v31, -v25, v19, v3
	v_cmp_ge_f32_e64 s[4:5], 0, v30
	s_nop 1
	v_cndmask_b32_e64 v19, v19, v24, s[4:5]
	v_cmp_lt_f32_e64 s[4:5], 0, v31
	s_nop 1
	v_cndmask_b32_e64 v19, v19, v25, s[4:5]
	v_mul_f32_e32 v24, 0x37800000, v19
	v_cndmask_b32_e32 v19, v19, v24, vcc
	v_cmp_class_f32_e32 vcc, v3, v2
	s_nop 1
	v_cndmask_b32_e32 v3, v19, v3, vcc
	v_div_scale_f32 v19, s[4:5], v3, v3, 1.0
	v_rcp_f32_e32 v25, v19
	v_div_scale_f32 v24, vcc, 1.0, v3, 1.0
	v_fma_f32 v30, -v19, v25, 1.0
	v_fmac_f32_e32 v25, v30, v25
	v_mul_f32_e32 v30, v24, v25
	v_fma_f32 v31, -v19, v30, v24
	v_fmac_f32_e32 v30, v31, v25
	v_fma_f32 v19, -v19, v30, v24
	v_div_fmas_f32 v19, v19, v25, v30
	v_div_fixup_f32 v24, v19, v3, 1.0
	v_pk_mul_f32 v[4:5], v[4:5], v[24:25] op_sel_hi:[1,0]
	v_pk_mul_f32 v[6:7], v[6:7], v[24:25] op_sel_hi:[1,0]
	v_pk_fma_f32 v[4:5], v[130:131], v[4:5], v[134:135]
	v_pk_fma_f32 v[6:7], v[132:133], v[6:7], v[136:137]
	s_waitcnt vmcnt(12)
	v_pk_fma_f32 v[4:5], v[18:19], v[26:27], v[4:5] op_sel_hi:[0,1,1]
	v_pk_fma_f32 v[6:7], v[18:19], v[20:21], v[6:7] op_sel_hi:[0,1,1]
	v_pk_mul_f32 v[6:7], v[6:7], v[22:23]
	v_pk_mul_f32 v[4:5], v[4:5], v[28:29]
	s_nop 0
	v_cvt_pk_bf16_f32 v4, v4, v5
	v_cvt_pk_bf16_f32 v5, v6, v7
	global_store_dwordx2 v[16:17], v[4:5], off
	s_ashr_i32 s4, s18, 2
	s_and_b32 s0, s23, 0x300
	v_add_u32_e32 v16, s0, v0
	s_ashr_i32 s5, s4, 31
	s_lshl_b64 s[16:17], s[4:5], 10
	v_ashrrev_i32_e32 v17, 31, v16
	v_lshl_add_u64 v[4:5], s[16:17], 0, v[16:17]
	v_lshl_add_u64 v[8:9], v[4:5], 2, s[6:7]
	v_lshlrev_b64 v[10:11], 1, v[4:5]
	s_waitcnt lgkmcnt(0)
	global_load_dwordx4 v[4:7], v[8:9], off
	s_lshl_b64 s[26:27], s[4:5], 6
	v_ashrrev_i32_e32 v18, 6, v16
	s_add_u32 s16, s19, s26
	v_ashrrev_i32_e32 v19, 31, v18
	s_addc_u32 s17, s20, s27
	v_lshl_add_u64 v[20:21], s[12:13], 0, v[10:11]
	v_lshl_add_u64 v[22:23], s[14:15], 0, v[10:11]
	s_nop 0
	v_lshl_add_u64 v[18:19], v[18:19], 2, s[16:17]
	global_load_dwordx2 v[20:21], v[20:21], off
	s_nop 0
	global_load_dwordx2 v[22:23], v[22:23], off
	s_nop 0
	global_load_dword v18, v[18:19], off
	s_lshl_b64 s[4:5], s[4:5], 12
	s_add_u32 s4, s21, s4
	s_addc_u32 s5, s22, s5
	v_lshl_add_u64 v[16:17], v[16:17], 1, s[4:5]
	s_add_i32 s0, s18, 0x800
	s_add_i32 s23, s23, 0x80000
	s_cmpk_lt_i32 s18, 0x7800
	s_mov_b32 s18, s0
	s_waitcnt vmcnt(16)
	v_mov_b32_e32 v56, v37
	v_mov_b32_e32 v57, v38
	v_mov_b32_e32 v58, v36
	v_mov_b32_e32 v59, v39
	v_pk_add_f32 v[56:57], v[56:57], v[58:59]
	s_waitcnt vmcnt(15)
	v_lshlrev_b32_e32 v58, 16, v52
	v_add_f32_e32 v35, v56, v57
	v_and_b32_e32 v59, 0xffff0000, v52
	v_lshlrev_b32_e32 v52, 16, v53
	v_add_f32_dpp v35, v35, v35 quad_perm:[1,0,3,2] row_mask:0xf bank_mask:0xf bound_ctrl:1
	v_and_b32_e32 v53, 0xffff0000, v53
	s_waitcnt vmcnt(14)
	v_lshlrev_b32_e32 v60, 16, v54
	v_add_f32_dpp v35, v35, v35 quad_perm:[2,3,0,1] row_mask:0xf bank_mask:0xf bound_ctrl:1
	v_and_b32_e32 v61, 0xffff0000, v54
	v_lshlrev_b32_e32 v54, 16, v55
	v_add_f32_dpp v35, v35, v35 row_half_mirror row_mask:0xf bank_mask:0xf bound_ctrl:1
	v_and_b32_e32 v55, 0xffff0000, v55
	s_nop 0
	v_add_f32_dpp v35, v35, v35 row_mirror row_mask:0xf bank_mask:0xf bound_ctrl:1
	v_fmamk_f32 v37, v35, 0xbc800000, v37
	v_fmamk_f32 v36, v35, 0xbc800000, v36
	v_fmamk_f32 v39, v35, 0xbc800000, v39
	v_fmac_f32_e32 v38, 0xbc800000, v35
	v_pk_mul_f32 v[56:57], v[38:39], v[38:39]
	v_pk_mul_f32 v[62:63], v[36:37], v[36:37]
	s_nop 0
	v_pk_mov_b32 v[64:65], v[62:63], v[56:57] op_sel:[1,0]
	v_mov_b32_e32 v63, v57
	v_pk_add_f32 v[56:57], v[64:65], v[62:63]
	s_nop 0
	v_add_f32_e32 v35, v56, v57
	s_nop 1
	v_add_f32_dpp v35, v35, v35 quad_perm:[1,0,3,2] row_mask:0xf bank_mask:0xf bound_ctrl:1
	s_nop 1
	v_add_f32_dpp v35, v35, v35 quad_perm:[2,3,0,1] row_mask:0xf bank_mask:0xf bound_ctrl:1
	s_nop 1
	v_add_f32_dpp v35, v35, v35 row_half_mirror row_mask:0xf bank_mask:0xf bound_ctrl:1
	s_nop 1
	v_add_f32_dpp v35, v35, v35 row_mirror row_mask:0xf bank_mask:0xf bound_ctrl:1
	v_fmamk_f32 v35, v35, 0x3c800000, v1
	v_mul_f32_e32 v51, 0x4f800000, v35
	v_cmp_gt_f32_e32 vcc, s24, v35
	s_nop 1
	v_cndmask_b32_e32 v35, v35, v51, vcc
	v_sqrt_f32_e32 v51, v35
	s_nop 0
	v_add_u32_e32 v56, -1, v51
	v_add_u32_e32 v57, 1, v51
	v_fma_f32 v62, -v56, v51, v35
	v_fma_f32 v63, -v57, v51, v35
	v_cmp_ge_f32_e64 s[4:5], 0, v62
	s_nop 1
	v_cndmask_b32_e64 v51, v51, v56, s[4:5]
	v_cmp_lt_f32_e64 s[4:5], 0, v63
	s_nop 1
	v_cndmask_b32_e64 v51, v51, v57, s[4:5]
	v_mul_f32_e32 v56, 0x37800000, v51
	v_cndmask_b32_e32 v51, v51, v56, vcc
	v_cmp_class_f32_e32 vcc, v35, v2
	s_nop 1
	v_cndmask_b32_e32 v35, v51, v35, vcc
	v_div_scale_f32 v51, s[4:5], v35, v35, 1.0
	v_rcp_f32_e32 v57, v51
	v_div_scale_f32 v56, vcc, 1.0, v35, 1.0
	v_fma_f32 v62, -v51, v57, 1.0
	v_fmac_f32_e32 v57, v62, v57
	v_mul_f32_e32 v62, v56, v57
	v_fma_f32 v63, -v51, v62, v56
	v_fmac_f32_e32 v62, v63, v57
	v_fma_f32 v51, -v51, v62, v56
	v_div_fmas_f32 v51, v51, v57, v62
	v_div_fixup_f32 v56, v51, v35, 1.0
	v_pk_mul_f32 v[36:37], v[36:37], v[56:57] op_sel_hi:[1,0]
	v_pk_mul_f32 v[38:39], v[38:39], v[56:57] op_sel_hi:[1,0]
	v_pk_fma_f32 v[36:37], v[130:131], v[36:37], v[134:135]
	v_pk_fma_f32 v[38:39], v[132:133], v[38:39], v[136:137]
	s_waitcnt vmcnt(13)
	v_pk_fma_f32 v[36:37], v[50:51], v[58:59], v[36:37] op_sel_hi:[0,1,1]
	v_pk_fma_f32 v[38:39], v[50:51], v[52:53], v[38:39] op_sel_hi:[0,1,1]
	v_pk_mul_f32 v[38:39], v[38:39], v[54:55]
	v_pk_mul_f32 v[36:37], v[36:37], v[60:61]
	s_nop 0
	v_cvt_pk_bf16_f32 v36, v36, v37
	v_cvt_pk_bf16_f32 v37, v38, v39
	global_store_dwordx2 v[48:49], v[36:37], off
	s_ashr_i32 s4, s18, 2
	s_and_b32 s0, s23, 0x300
	v_add_u32_e32 v48, s0, v0
	s_ashr_i32 s5, s4, 31
	s_lshl_b64 s[16:17], s[4:5], 10
	v_ashrrev_i32_e32 v49, 31, v48
	v_lshl_add_u64 v[36:37], s[16:17], 0, v[48:49]
	v_lshl_add_u64 v[40:41], v[36:37], 2, s[6:7]
	v_lshlrev_b64 v[42:43], 1, v[36:37]
	s_waitcnt lgkmcnt(0)
	global_load_dwordx4 v[36:39], v[40:41], off
	s_lshl_b64 s[26:27], s[4:5], 6
	v_ashrrev_i32_e32 v50, 6, v48
	s_add_u32 s16, s19, s26
	v_ashrrev_i32_e32 v51, 31, v50
	s_addc_u32 s17, s20, s27
	v_lshl_add_u64 v[52:53], s[12:13], 0, v[42:43]
	v_lshl_add_u64 v[54:55], s[14:15], 0, v[42:43]
	s_nop 0
	v_lshl_add_u64 v[50:51], v[50:51], 2, s[16:17]
	global_load_dwordx2 v[52:53], v[52:53], off
	s_nop 0
	global_load_dwordx2 v[54:55], v[54:55], off
	s_nop 0
	global_load_dword v50, v[50:51], off
	s_lshl_b64 s[4:5], s[4:5], 12
	s_add_u32 s4, s21, s4
	s_addc_u32 s5, s22, s5
	v_lshl_add_u64 v[48:49], v[48:49], 1, s[4:5]
	s_add_i32 s0, s18, 0x800
	s_add_i32 s23, s23, 0x80000
	s_cmpk_lt_i32 s18, 0x7800
	s_mov_b32 s18, s0
	s_waitcnt vmcnt(17)
	v_mov_b32_e32 v88, v69
	v_mov_b32_e32 v89, v70
	v_mov_b32_e32 v90, v68
	v_mov_b32_e32 v91, v71
	v_pk_add_f32 v[88:89], v[88:89], v[90:91]
	s_waitcnt vmcnt(16)
	v_lshlrev_b32_e32 v90, 16, v84
	v_add_f32_e32 v67, v88, v89
	v_and_b32_e32 v91, 0xffff0000, v84
	v_lshlrev_b32_e32 v84, 16, v85
	v_add_f32_dpp v67, v67, v67 quad_perm:[1,0,3,2] row_mask:0xf bank_mask:0xf bound_ctrl:1
	v_and_b32_e32 v85, 0xffff0000, v85
	s_waitcnt vmcnt(15)
	v_lshlrev_b32_e32 v92, 16, v86
	v_add_f32_dpp v67, v67, v67 quad_perm:[2,3,0,1] row_mask:0xf bank_mask:0xf bound_ctrl:1
	v_and_b32_e32 v93, 0xffff0000, v86
	v_lshlrev_b32_e32 v86, 16, v87
	v_add_f32_dpp v67, v67, v67 row_half_mirror row_mask:0xf bank_mask:0xf bound_ctrl:1
	v_and_b32_e32 v87, 0xffff0000, v87
	s_nop 0
	v_add_f32_dpp v67, v67, v67 row_mirror row_mask:0xf bank_mask:0xf bound_ctrl:1
	v_fmamk_f32 v69, v67, 0xbc800000, v69
	v_fmamk_f32 v68, v67, 0xbc800000, v68
	v_fmamk_f32 v71, v67, 0xbc800000, v71
	v_fmac_f32_e32 v70, 0xbc800000, v67
	v_pk_mul_f32 v[88:89], v[70:71], v[70:71]
	v_pk_mul_f32 v[94:95], v[68:69], v[68:69]
	s_nop 0
	v_pk_mov_b32 v[96:97], v[94:95], v[88:89] op_sel:[1,0]
	v_mov_b32_e32 v95, v89
	v_pk_add_f32 v[88:89], v[96:97], v[94:95]
	s_nop 0
	v_add_f32_e32 v67, v88, v89
	s_nop 1
	v_add_f32_dpp v67, v67, v67 quad_perm:[1,0,3,2] row_mask:0xf bank_mask:0xf bound_ctrl:1
	s_nop 1
	v_add_f32_dpp v67, v67, v67 quad_perm:[2,3,0,1] row_mask:0xf bank_mask:0xf bound_ctrl:1
	s_nop 1
	v_add_f32_dpp v67, v67, v67 row_half_mirror row_mask:0xf bank_mask:0xf bound_ctrl:1
	s_nop 1
	v_add_f32_dpp v67, v67, v67 row_mirror row_mask:0xf bank_mask:0xf bound_ctrl:1
	v_fmamk_f32 v67, v67, 0x3c800000, v1
	v_mul_f32_e32 v83, 0x4f800000, v67
	v_cmp_gt_f32_e32 vcc, s24, v67
	s_nop 1
	v_cndmask_b32_e32 v67, v67, v83, vcc
	v_sqrt_f32_e32 v83, v67
	s_nop 0
	v_add_u32_e32 v88, -1, v83
	v_add_u32_e32 v89, 1, v83
	v_fma_f32 v94, -v88, v83, v67
	v_fma_f32 v95, -v89, v83, v67
	v_cmp_ge_f32_e64 s[4:5], 0, v94
	s_nop 1
	v_cndmask_b32_e64 v83, v83, v88, s[4:5]
	v_cmp_lt_f32_e64 s[4:5], 0, v95
	s_nop 1
	v_cndmask_b32_e64 v83, v83, v89, s[4:5]
	v_mul_f32_e32 v88, 0x37800000, v83
	v_cndmask_b32_e32 v83, v83, v88, vcc
	v_cmp_class_f32_e32 vcc, v67, v2
	s_nop 1
	v_cndmask_b32_e32 v67, v83, v67, vcc
	v_div_scale_f32 v83, s[4:5], v67, v67, 1.0
	v_rcp_f32_e32 v89, v83
	v_div_scale_f32 v88, vcc, 1.0, v67, 1.0
	v_fma_f32 v94, -v83, v89, 1.0
	v_fmac_f32_e32 v89, v94, v89
	v_mul_f32_e32 v94, v88, v89
	v_fma_f32 v95, -v83, v94, v88
	v_fmac_f32_e32 v94, v95, v89
	v_fma_f32 v83, -v83, v94, v88
	v_div_fmas_f32 v83, v83, v89, v94
	v_div_fixup_f32 v88, v83, v67, 1.0
	v_pk_mul_f32 v[68:69], v[68:69], v[88:89] op_sel_hi:[1,0]
	v_pk_mul_f32 v[70:71], v[70:71], v[88:89] op_sel_hi:[1,0]
	v_pk_fma_f32 v[68:69], v[130:131], v[68:69], v[134:135]
	v_pk_fma_f32 v[70:71], v[132:133], v[70:71], v[136:137]
	s_waitcnt vmcnt(14)
	v_pk_fma_f32 v[68:69], v[82:83], v[90:91], v[68:69] op_sel_hi:[0,1,1]
	v_pk_fma_f32 v[70:71], v[82:83], v[84:85], v[70:71] op_sel_hi:[0,1,1]
	v_pk_mul_f32 v[70:71], v[70:71], v[86:87]
	v_pk_mul_f32 v[68:69], v[68:69], v[92:93]
	s_nop 0
	v_cvt_pk_bf16_f32 v68, v68, v69
	v_cvt_pk_bf16_f32 v69, v70, v71
	global_store_dwordx2 v[80:81], v[68:69], off
	s_ashr_i32 s4, s18, 2
	s_and_b32 s0, s23, 0x300
	v_add_u32_e32 v80, s0, v0
	s_ashr_i32 s5, s4, 31
	s_lshl_b64 s[16:17], s[4:5], 10
	v_ashrrev_i32_e32 v81, 31, v80
	v_lshl_add_u64 v[68:69], s[16:17], 0, v[80:81]
	v_lshl_add_u64 v[72:73], v[68:69], 2, s[6:7]
	v_lshlrev_b64 v[74:75], 1, v[68:69]
	s_waitcnt lgkmcnt(0)
	global_load_dwordx4 v[68:71], v[72:73], off
	s_lshl_b64 s[26:27], s[4:5], 6
	v_ashrrev_i32_e32 v82, 6, v80
	s_add_u32 s16, s19, s26
	v_ashrrev_i32_e32 v83, 31, v82
	s_addc_u32 s17, s20, s27
	v_lshl_add_u64 v[84:85], s[12:13], 0, v[74:75]
	v_lshl_add_u64 v[86:87], s[14:15], 0, v[74:75]
	s_nop 0
	v_lshl_add_u64 v[82:83], v[82:83], 2, s[16:17]
	global_load_dwordx2 v[84:85], v[84:85], off
	s_nop 0
	global_load_dwordx2 v[86:87], v[86:87], off
	s_nop 0
	global_load_dword v82, v[82:83], off
	s_lshl_b64 s[4:5], s[4:5], 12
	s_add_u32 s4, s21, s4
	s_addc_u32 s5, s22, s5
	v_lshl_add_u64 v[80:81], v[80:81], 1, s[4:5]
	s_add_i32 s0, s18, 0x800
	s_add_i32 s23, s23, 0x80000
	s_cmpk_lt_i32 s18, 0x7800
	s_mov_b32 s18, s0
	s_waitcnt vmcnt(18)
	v_mov_b32_e32 v120, v101
	v_mov_b32_e32 v121, v102
	v_mov_b32_e32 v122, v100
	v_mov_b32_e32 v123, v103
	v_pk_add_f32 v[120:121], v[120:121], v[122:123]
	s_waitcnt vmcnt(17)
	v_lshlrev_b32_e32 v122, 16, v116
	v_add_f32_e32 v99, v120, v121
	v_and_b32_e32 v123, 0xffff0000, v116
	v_lshlrev_b32_e32 v116, 16, v117
	v_add_f32_dpp v99, v99, v99 quad_perm:[1,0,3,2] row_mask:0xf bank_mask:0xf bound_ctrl:1
	v_and_b32_e32 v117, 0xffff0000, v117
	s_waitcnt vmcnt(16)
	v_lshlrev_b32_e32 v124, 16, v118
	v_add_f32_dpp v99, v99, v99 quad_perm:[2,3,0,1] row_mask:0xf bank_mask:0xf bound_ctrl:1
	v_and_b32_e32 v125, 0xffff0000, v118
	v_lshlrev_b32_e32 v118, 16, v119
	v_add_f32_dpp v99, v99, v99 row_half_mirror row_mask:0xf bank_mask:0xf bound_ctrl:1
	v_and_b32_e32 v119, 0xffff0000, v119
	s_nop 0
	v_add_f32_dpp v99, v99, v99 row_mirror row_mask:0xf bank_mask:0xf bound_ctrl:1
	v_fmamk_f32 v101, v99, 0xbc800000, v101
	v_fmamk_f32 v100, v99, 0xbc800000, v100
	v_fmamk_f32 v103, v99, 0xbc800000, v103
	v_fmac_f32_e32 v102, 0xbc800000, v99
	v_pk_mul_f32 v[120:121], v[102:103], v[102:103]
	v_pk_mul_f32 v[126:127], v[100:101], v[100:101]
	s_nop 0
	v_pk_mov_b32 v[128:129], v[126:127], v[120:121] op_sel:[1,0]
	v_mov_b32_e32 v127, v121
	v_pk_add_f32 v[120:121], v[128:129], v[126:127]
	s_nop 0
	v_add_f32_e32 v99, v120, v121
	s_nop 1
	v_add_f32_dpp v99, v99, v99 quad_perm:[1,0,3,2] row_mask:0xf bank_mask:0xf bound_ctrl:1
	s_nop 1
	v_add_f32_dpp v99, v99, v99 quad_perm:[2,3,0,1] row_mask:0xf bank_mask:0xf bound_ctrl:1
	s_nop 1
	v_add_f32_dpp v99, v99, v99 row_half_mirror row_mask:0xf bank_mask:0xf bound_ctrl:1
	s_nop 1
	v_add_f32_dpp v99, v99, v99 row_mirror row_mask:0xf bank_mask:0xf bound_ctrl:1
	v_fmamk_f32 v99, v99, 0x3c800000, v1
	v_mul_f32_e32 v115, 0x4f800000, v99
	v_cmp_gt_f32_e32 vcc, s24, v99
	s_nop 1
	v_cndmask_b32_e32 v99, v99, v115, vcc
	v_sqrt_f32_e32 v115, v99
	s_nop 0
	v_add_u32_e32 v120, -1, v115
	v_add_u32_e32 v121, 1, v115
	v_fma_f32 v126, -v120, v115, v99
	v_fma_f32 v127, -v121, v115, v99
	v_cmp_ge_f32_e64 s[4:5], 0, v126
	s_nop 1
	v_cndmask_b32_e64 v115, v115, v120, s[4:5]
	v_cmp_lt_f32_e64 s[4:5], 0, v127
	s_nop 1
	v_cndmask_b32_e64 v115, v115, v121, s[4:5]
	v_mul_f32_e32 v120, 0x37800000, v115
	v_cndmask_b32_e32 v115, v115, v120, vcc
	v_cmp_class_f32_e32 vcc, v99, v2
	s_nop 1
	v_cndmask_b32_e32 v99, v115, v99, vcc
	v_div_scale_f32 v115, s[4:5], v99, v99, 1.0
	v_rcp_f32_e32 v121, v115
	v_div_scale_f32 v120, vcc, 1.0, v99, 1.0
	v_fma_f32 v126, -v115, v121, 1.0
	v_fmac_f32_e32 v121, v126, v121
	v_mul_f32_e32 v126, v120, v121
	v_fma_f32 v127, -v115, v126, v120
	v_fmac_f32_e32 v126, v127, v121
	v_fma_f32 v115, -v115, v126, v120
	v_div_fmas_f32 v115, v115, v121, v126
	v_div_fixup_f32 v120, v115, v99, 1.0
	v_pk_mul_f32 v[100:101], v[100:101], v[120:121] op_sel_hi:[1,0]
	v_pk_mul_f32 v[102:103], v[102:103], v[120:121] op_sel_hi:[1,0]
	v_pk_fma_f32 v[100:101], v[130:131], v[100:101], v[134:135]
	v_pk_fma_f32 v[102:103], v[132:133], v[102:103], v[136:137]
	s_waitcnt vmcnt(15)
	v_pk_fma_f32 v[100:101], v[114:115], v[122:123], v[100:101] op_sel_hi:[0,1,1]
	v_pk_fma_f32 v[102:103], v[114:115], v[116:117], v[102:103] op_sel_hi:[0,1,1]
	v_pk_mul_f32 v[102:103], v[102:103], v[118:119]
	v_pk_mul_f32 v[100:101], v[100:101], v[124:125]
	s_nop 0
	v_cvt_pk_bf16_f32 v100, v100, v101
	v_cvt_pk_bf16_f32 v101, v102, v103
	global_store_dwordx2 v[112:113], v[100:101], off
	s_ashr_i32 s4, s18, 2
	s_and_b32 s0, s23, 0x300
	v_add_u32_e32 v112, s0, v0
	s_ashr_i32 s5, s4, 31
	s_lshl_b64 s[16:17], s[4:5], 10
	v_ashrrev_i32_e32 v113, 31, v112
	v_lshl_add_u64 v[100:101], s[16:17], 0, v[112:113]
	v_lshl_add_u64 v[104:105], v[100:101], 2, s[6:7]
	v_lshlrev_b64 v[106:107], 1, v[100:101]
	s_waitcnt lgkmcnt(0)
	global_load_dwordx4 v[100:103], v[104:105], off
	s_lshl_b64 s[26:27], s[4:5], 6
	v_ashrrev_i32_e32 v114, 6, v112
	s_add_u32 s16, s19, s26
	v_ashrrev_i32_e32 v115, 31, v114
	s_addc_u32 s17, s20, s27
	v_lshl_add_u64 v[116:117], s[12:13], 0, v[106:107]
	v_lshl_add_u64 v[118:119], s[14:15], 0, v[106:107]
	s_nop 0
	v_lshl_add_u64 v[114:115], v[114:115], 2, s[16:17]
	global_load_dwordx2 v[116:117], v[116:117], off
	s_nop 0
	global_load_dwordx2 v[118:119], v[118:119], off
	s_nop 0
	global_load_dword v114, v[114:115], off
	s_lshl_b64 s[4:5], s[4:5], 12
	s_add_u32 s4, s21, s4
	s_addc_u32 s5, s22, s5
	v_lshl_add_u64 v[112:113], v[112:113], 1, s[4:5]
	s_add_i32 s0, s18, 0x800
	s_add_i32 s23, s23, 0x80000
	s_cmpk_lt_i32 s18, 0x7800
	s_mov_b32 s18, s0
.LBB0_785:
	s_waitcnt vmcnt(18)
	v_mov_b32_e32 v24, v5
	v_mov_b32_e32 v25, v6
	v_mov_b32_e32 v26, v4
	v_mov_b32_e32 v27, v7
	v_pk_add_f32 v[24:25], v[24:25], v[26:27]
	s_waitcnt vmcnt(17)
	v_lshlrev_b32_e32 v26, 16, v20
	v_add_f32_e32 v3, v24, v25
	v_and_b32_e32 v27, 0xffff0000, v20
	v_lshlrev_b32_e32 v20, 16, v21
	v_add_f32_dpp v3, v3, v3 quad_perm:[1,0,3,2] row_mask:0xf bank_mask:0xf bound_ctrl:1
	v_and_b32_e32 v21, 0xffff0000, v21
	s_waitcnt vmcnt(16)
	v_lshlrev_b32_e32 v28, 16, v22
	v_add_f32_dpp v3, v3, v3 quad_perm:[2,3,0,1] row_mask:0xf bank_mask:0xf bound_ctrl:1
	v_and_b32_e32 v29, 0xffff0000, v22
	v_lshlrev_b32_e32 v22, 16, v23
	v_add_f32_dpp v3, v3, v3 row_half_mirror row_mask:0xf bank_mask:0xf bound_ctrl:1
	v_and_b32_e32 v23, 0xffff0000, v23
	s_nop 0
	v_add_f32_dpp v3, v3, v3 row_mirror row_mask:0xf bank_mask:0xf bound_ctrl:1
	v_fmamk_f32 v5, v3, 0xbc800000, v5
	v_fmamk_f32 v4, v3, 0xbc800000, v4
	v_fmamk_f32 v7, v3, 0xbc800000, v7
	v_fmac_f32_e32 v6, 0xbc800000, v3
	v_pk_mul_f32 v[24:25], v[6:7], v[6:7]
	v_pk_mul_f32 v[30:31], v[4:5], v[4:5]
	s_nop 0
	v_pk_mov_b32 v[32:33], v[30:31], v[24:25] op_sel:[1,0]
	v_mov_b32_e32 v31, v25
	v_pk_add_f32 v[24:25], v[32:33], v[30:31]
	s_nop 0
	v_add_f32_e32 v3, v24, v25
	s_nop 1
	v_add_f32_dpp v3, v3, v3 quad_perm:[1,0,3,2] row_mask:0xf bank_mask:0xf bound_ctrl:1
	s_nop 1
	v_add_f32_dpp v3, v3, v3 quad_perm:[2,3,0,1] row_mask:0xf bank_mask:0xf bound_ctrl:1
	s_nop 1
	v_add_f32_dpp v3, v3, v3 row_half_mirror row_mask:0xf bank_mask:0xf bound_ctrl:1
	s_nop 1
	v_add_f32_dpp v3, v3, v3 row_mirror row_mask:0xf bank_mask:0xf bound_ctrl:1
	v_fmamk_f32 v3, v3, 0x3c800000, v1
	v_mul_f32_e32 v19, 0x4f800000, v3
	v_cmp_gt_f32_e32 vcc, s24, v3
	s_nop 1
	v_cndmask_b32_e32 v3, v3, v19, vcc
	v_sqrt_f32_e32 v19, v3
	s_nop 0
	v_add_u32_e32 v24, -1, v19
	v_add_u32_e32 v25, 1, v19
	v_fma_f32 v30, -v24, v19, v3
	v_fma_f32 v31, -v25, v19, v3
	v_cmp_ge_f32_e64 s[4:5], 0, v30
	s_nop 1
	v_cndmask_b32_e64 v19, v19, v24, s[4:5]
	v_cmp_lt_f32_e64 s[4:5], 0, v31
	s_nop 1
	v_cndmask_b32_e64 v19, v19, v25, s[4:5]
	v_mul_f32_e32 v24, 0x37800000, v19
	v_cndmask_b32_e32 v19, v19, v24, vcc
	v_cmp_class_f32_e32 vcc, v3, v2
	s_nop 1
	v_cndmask_b32_e32 v3, v19, v3, vcc
	v_div_scale_f32 v19, s[4:5], v3, v3, 1.0
	v_rcp_f32_e32 v25, v19
	v_div_scale_f32 v24, vcc, 1.0, v3, 1.0
	v_fma_f32 v30, -v19, v25, 1.0
	v_fmac_f32_e32 v25, v30, v25
	v_mul_f32_e32 v30, v24, v25
	v_fma_f32 v31, -v19, v30, v24
	v_fmac_f32_e32 v30, v31, v25
	v_fma_f32 v19, -v19, v30, v24
	v_div_fmas_f32 v19, v19, v25, v30
	v_div_fixup_f32 v24, v19, v3, 1.0
	v_pk_mul_f32 v[4:5], v[4:5], v[24:25] op_sel_hi:[1,0]
	v_pk_mul_f32 v[6:7], v[6:7], v[24:25] op_sel_hi:[1,0]
	v_pk_fma_f32 v[4:5], v[130:131], v[4:5], v[134:135]
	v_pk_fma_f32 v[6:7], v[132:133], v[6:7], v[136:137]
	s_waitcnt vmcnt(15)
	v_pk_fma_f32 v[4:5], v[18:19], v[26:27], v[4:5] op_sel_hi:[0,1,1]
	v_pk_fma_f32 v[6:7], v[18:19], v[20:21], v[6:7] op_sel_hi:[0,1,1]
	v_pk_mul_f32 v[6:7], v[6:7], v[22:23]
	v_pk_mul_f32 v[4:5], v[4:5], v[28:29]
	s_nop 0
	v_cvt_pk_bf16_f32 v4, v4, v5
	v_cvt_pk_bf16_f32 v5, v6, v7
	global_store_dwordx2 v[16:17], v[4:5], off
	s_ashr_i32 s4, s18, 2
	s_and_b32 s0, s23, 0x300
	v_add_u32_e32 v16, s0, v0
	s_ashr_i32 s5, s4, 31
	s_lshl_b64 s[16:17], s[4:5], 10
	v_ashrrev_i32_e32 v17, 31, v16
	v_lshl_add_u64 v[4:5], s[16:17], 0, v[16:17]
	v_lshl_add_u64 v[8:9], v[4:5], 2, s[6:7]
	v_lshlrev_b64 v[10:11], 1, v[4:5]
	s_waitcnt lgkmcnt(0)
	global_load_dwordx4 v[4:7], v[8:9], off
	s_lshl_b64 s[26:27], s[4:5], 6
	v_ashrrev_i32_e32 v18, 6, v16
	s_add_u32 s16, s19, s26
	v_ashrrev_i32_e32 v19, 31, v18
	s_addc_u32 s17, s20, s27
	v_lshl_add_u64 v[20:21], s[12:13], 0, v[10:11]
	v_lshl_add_u64 v[22:23], s[14:15], 0, v[10:11]
	s_nop 0
	v_lshl_add_u64 v[18:19], v[18:19], 2, s[16:17]
	global_load_dwordx2 v[20:21], v[20:21], off
	s_nop 0
	global_load_dwordx2 v[22:23], v[22:23], off
	s_nop 0
	global_load_dword v18, v[18:19], off
	s_lshl_b64 s[4:5], s[4:5], 12
	s_add_u32 s4, s21, s4
	s_addc_u32 s5, s22, s5
	v_lshl_add_u64 v[16:17], v[16:17], 1, s[4:5]
	s_add_i32 s0, s18, 0x800
	s_add_i32 s23, s23, 0x80000
	s_cmpk_lt_i32 s18, 0x7800
	s_mov_b32 s18, s0
	s_waitcnt vmcnt(18)
	v_mov_b32_e32 v56, v37
	v_mov_b32_e32 v57, v38
	v_mov_b32_e32 v58, v36
	v_mov_b32_e32 v59, v39
	v_pk_add_f32 v[56:57], v[56:57], v[58:59]
	s_waitcnt vmcnt(17)
	v_lshlrev_b32_e32 v58, 16, v52
	v_add_f32_e32 v35, v56, v57
	v_and_b32_e32 v59, 0xffff0000, v52
	v_lshlrev_b32_e32 v52, 16, v53
	v_add_f32_dpp v35, v35, v35 quad_perm:[1,0,3,2] row_mask:0xf bank_mask:0xf bound_ctrl:1
	v_and_b32_e32 v53, 0xffff0000, v53
	s_waitcnt vmcnt(16)
	v_lshlrev_b32_e32 v60, 16, v54
	v_add_f32_dpp v35, v35, v35 quad_perm:[2,3,0,1] row_mask:0xf bank_mask:0xf bound_ctrl:1
	v_and_b32_e32 v61, 0xffff0000, v54
	v_lshlrev_b32_e32 v54, 16, v55
	v_add_f32_dpp v35, v35, v35 row_half_mirror row_mask:0xf bank_mask:0xf bound_ctrl:1
	v_and_b32_e32 v55, 0xffff0000, v55
	s_nop 0
	v_add_f32_dpp v35, v35, v35 row_mirror row_mask:0xf bank_mask:0xf bound_ctrl:1
	v_fmamk_f32 v37, v35, 0xbc800000, v37
	v_fmamk_f32 v36, v35, 0xbc800000, v36
	v_fmamk_f32 v39, v35, 0xbc800000, v39
	v_fmac_f32_e32 v38, 0xbc800000, v35
	v_pk_mul_f32 v[56:57], v[38:39], v[38:39]
	v_pk_mul_f32 v[62:63], v[36:37], v[36:37]
	s_nop 0
	v_pk_mov_b32 v[64:65], v[62:63], v[56:57] op_sel:[1,0]
	v_mov_b32_e32 v63, v57
	v_pk_add_f32 v[56:57], v[64:65], v[62:63]
	s_nop 0
	v_add_f32_e32 v35, v56, v57
	s_nop 1
	v_add_f32_dpp v35, v35, v35 quad_perm:[1,0,3,2] row_mask:0xf bank_mask:0xf bound_ctrl:1
	s_nop 1
	v_add_f32_dpp v35, v35, v35 quad_perm:[2,3,0,1] row_mask:0xf bank_mask:0xf bound_ctrl:1
	s_nop 1
	v_add_f32_dpp v35, v35, v35 row_half_mirror row_mask:0xf bank_mask:0xf bound_ctrl:1
	s_nop 1
	v_add_f32_dpp v35, v35, v35 row_mirror row_mask:0xf bank_mask:0xf bound_ctrl:1
	v_fmamk_f32 v35, v35, 0x3c800000, v1
	v_mul_f32_e32 v51, 0x4f800000, v35
	v_cmp_gt_f32_e32 vcc, s24, v35
	s_nop 1
	v_cndmask_b32_e32 v35, v35, v51, vcc
	v_sqrt_f32_e32 v51, v35
	s_nop 0
	v_add_u32_e32 v56, -1, v51
	v_add_u32_e32 v57, 1, v51
	v_fma_f32 v62, -v56, v51, v35
	v_fma_f32 v63, -v57, v51, v35
	v_cmp_ge_f32_e64 s[4:5], 0, v62
	s_nop 1
	v_cndmask_b32_e64 v51, v51, v56, s[4:5]
	v_cmp_lt_f32_e64 s[4:5], 0, v63
	s_nop 1
	v_cndmask_b32_e64 v51, v51, v57, s[4:5]
	v_mul_f32_e32 v56, 0x37800000, v51
	v_cndmask_b32_e32 v51, v51, v56, vcc
	v_cmp_class_f32_e32 vcc, v35, v2
	s_nop 1
	v_cndmask_b32_e32 v35, v51, v35, vcc
	v_div_scale_f32 v51, s[4:5], v35, v35, 1.0
	v_rcp_f32_e32 v57, v51
	v_div_scale_f32 v56, vcc, 1.0, v35, 1.0
	v_fma_f32 v62, -v51, v57, 1.0
	v_fmac_f32_e32 v57, v62, v57
	v_mul_f32_e32 v62, v56, v57
	v_fma_f32 v63, -v51, v62, v56
	v_fmac_f32_e32 v62, v63, v57
	v_fma_f32 v51, -v51, v62, v56
	v_div_fmas_f32 v51, v51, v57, v62
	v_div_fixup_f32 v56, v51, v35, 1.0
	v_pk_mul_f32 v[36:37], v[36:37], v[56:57] op_sel_hi:[1,0]
	v_pk_mul_f32 v[38:39], v[38:39], v[56:57] op_sel_hi:[1,0]
	v_pk_fma_f32 v[36:37], v[130:131], v[36:37], v[134:135]
	v_pk_fma_f32 v[38:39], v[132:133], v[38:39], v[136:137]
	s_waitcnt vmcnt(15)
	v_pk_fma_f32 v[36:37], v[50:51], v[58:59], v[36:37] op_sel_hi:[0,1,1]
	v_pk_fma_f32 v[38:39], v[50:51], v[52:53], v[38:39] op_sel_hi:[0,1,1]
	v_pk_mul_f32 v[38:39], v[38:39], v[54:55]
	v_pk_mul_f32 v[36:37], v[36:37], v[60:61]
	s_nop 0
	v_cvt_pk_bf16_f32 v36, v36, v37
	v_cvt_pk_bf16_f32 v37, v38, v39
	global_store_dwordx2 v[48:49], v[36:37], off
	s_ashr_i32 s4, s18, 2
	s_and_b32 s0, s23, 0x300
	v_add_u32_e32 v48, s0, v0
	s_ashr_i32 s5, s4, 31
	s_lshl_b64 s[16:17], s[4:5], 10
	v_ashrrev_i32_e32 v49, 31, v48
	v_lshl_add_u64 v[36:37], s[16:17], 0, v[48:49]
	v_lshl_add_u64 v[40:41], v[36:37], 2, s[6:7]
	v_lshlrev_b64 v[42:43], 1, v[36:37]
	s_waitcnt lgkmcnt(0)
	global_load_dwordx4 v[36:39], v[40:41], off
	s_lshl_b64 s[26:27], s[4:5], 6
	v_ashrrev_i32_e32 v50, 6, v48
	s_add_u32 s16, s19, s26
	v_ashrrev_i32_e32 v51, 31, v50
	s_addc_u32 s17, s20, s27
	v_lshl_add_u64 v[52:53], s[12:13], 0, v[42:43]
	v_lshl_add_u64 v[54:55], s[14:15], 0, v[42:43]
	s_nop 0
	v_lshl_add_u64 v[50:51], v[50:51], 2, s[16:17]
	global_load_dwordx2 v[52:53], v[52:53], off
	s_nop 0
	global_load_dwordx2 v[54:55], v[54:55], off
	s_nop 0
	global_load_dword v50, v[50:51], off
	s_lshl_b64 s[4:5], s[4:5], 12
	s_add_u32 s4, s21, s4
	s_addc_u32 s5, s22, s5
	v_lshl_add_u64 v[48:49], v[48:49], 1, s[4:5]
	s_add_i32 s0, s18, 0x800
	s_add_i32 s23, s23, 0x80000
	s_cmpk_lt_i32 s18, 0x7800
	s_mov_b32 s18, s0
	s_waitcnt vmcnt(18)
	v_mov_b32_e32 v88, v69
	v_mov_b32_e32 v89, v70
	v_mov_b32_e32 v90, v68
	v_mov_b32_e32 v91, v71
	v_pk_add_f32 v[88:89], v[88:89], v[90:91]
	s_waitcnt vmcnt(17)
	v_lshlrev_b32_e32 v90, 16, v84
	v_add_f32_e32 v67, v88, v89
	v_and_b32_e32 v91, 0xffff0000, v84
	v_lshlrev_b32_e32 v84, 16, v85
	v_add_f32_dpp v67, v67, v67 quad_perm:[1,0,3,2] row_mask:0xf bank_mask:0xf bound_ctrl:1
	v_and_b32_e32 v85, 0xffff0000, v85
	s_waitcnt vmcnt(16)
	v_lshlrev_b32_e32 v92, 16, v86
	v_add_f32_dpp v67, v67, v67 quad_perm:[2,3,0,1] row_mask:0xf bank_mask:0xf bound_ctrl:1
	v_and_b32_e32 v93, 0xffff0000, v86
	v_lshlrev_b32_e32 v86, 16, v87
	v_add_f32_dpp v67, v67, v67 row_half_mirror row_mask:0xf bank_mask:0xf bound_ctrl:1
	v_and_b32_e32 v87, 0xffff0000, v87
	s_nop 0
	v_add_f32_dpp v67, v67, v67 row_mirror row_mask:0xf bank_mask:0xf bound_ctrl:1
	v_fmamk_f32 v69, v67, 0xbc800000, v69
	v_fmamk_f32 v68, v67, 0xbc800000, v68
	v_fmamk_f32 v71, v67, 0xbc800000, v71
	v_fmac_f32_e32 v70, 0xbc800000, v67
	v_pk_mul_f32 v[88:89], v[70:71], v[70:71]
	v_pk_mul_f32 v[94:95], v[68:69], v[68:69]
	s_nop 0
	v_pk_mov_b32 v[96:97], v[94:95], v[88:89] op_sel:[1,0]
	v_mov_b32_e32 v95, v89
	v_pk_add_f32 v[88:89], v[96:97], v[94:95]
	s_nop 0
	v_add_f32_e32 v67, v88, v89
	s_nop 1
	v_add_f32_dpp v67, v67, v67 quad_perm:[1,0,3,2] row_mask:0xf bank_mask:0xf bound_ctrl:1
	s_nop 1
	v_add_f32_dpp v67, v67, v67 quad_perm:[2,3,0,1] row_mask:0xf bank_mask:0xf bound_ctrl:1
	s_nop 1
	v_add_f32_dpp v67, v67, v67 row_half_mirror row_mask:0xf bank_mask:0xf bound_ctrl:1
	s_nop 1
	v_add_f32_dpp v67, v67, v67 row_mirror row_mask:0xf bank_mask:0xf bound_ctrl:1
	v_fmamk_f32 v67, v67, 0x3c800000, v1
	v_mul_f32_e32 v83, 0x4f800000, v67
	v_cmp_gt_f32_e32 vcc, s24, v67
	s_nop 1
	v_cndmask_b32_e32 v67, v67, v83, vcc
	v_sqrt_f32_e32 v83, v67
	s_nop 0
	v_add_u32_e32 v88, -1, v83
	v_add_u32_e32 v89, 1, v83
	v_fma_f32 v94, -v88, v83, v67
	v_fma_f32 v95, -v89, v83, v67
	v_cmp_ge_f32_e64 s[4:5], 0, v94
	s_nop 1
	v_cndmask_b32_e64 v83, v83, v88, s[4:5]
	v_cmp_lt_f32_e64 s[4:5], 0, v95
	s_nop 1
	v_cndmask_b32_e64 v83, v83, v89, s[4:5]
	v_mul_f32_e32 v88, 0x37800000, v83
	v_cndmask_b32_e32 v83, v83, v88, vcc
	v_cmp_class_f32_e32 vcc, v67, v2
	s_nop 1
	v_cndmask_b32_e32 v67, v83, v67, vcc
	v_div_scale_f32 v83, s[4:5], v67, v67, 1.0
	v_rcp_f32_e32 v89, v83
	v_div_scale_f32 v88, vcc, 1.0, v67, 1.0
	v_fma_f32 v94, -v83, v89, 1.0
	v_fmac_f32_e32 v89, v94, v89
	v_mul_f32_e32 v94, v88, v89
	v_fma_f32 v95, -v83, v94, v88
	v_fmac_f32_e32 v94, v95, v89
	v_fma_f32 v83, -v83, v94, v88
	v_div_fmas_f32 v83, v83, v89, v94
	v_div_fixup_f32 v88, v83, v67, 1.0
	v_pk_mul_f32 v[68:69], v[68:69], v[88:89] op_sel_hi:[1,0]
	v_pk_mul_f32 v[70:71], v[70:71], v[88:89] op_sel_hi:[1,0]
	v_pk_fma_f32 v[68:69], v[130:131], v[68:69], v[134:135]
	v_pk_fma_f32 v[70:71], v[132:133], v[70:71], v[136:137]
	s_waitcnt vmcnt(15)
	v_pk_fma_f32 v[68:69], v[82:83], v[90:91], v[68:69] op_sel_hi:[0,1,1]
	v_pk_fma_f32 v[70:71], v[82:83], v[84:85], v[70:71] op_sel_hi:[0,1,1]
	v_pk_mul_f32 v[70:71], v[70:71], v[86:87]
	v_pk_mul_f32 v[68:69], v[68:69], v[92:93]
	s_nop 0
	v_cvt_pk_bf16_f32 v68, v68, v69
	v_cvt_pk_bf16_f32 v69, v70, v71
	global_store_dwordx2 v[80:81], v[68:69], off
	s_ashr_i32 s4, s18, 2
	s_and_b32 s0, s23, 0x300
	v_add_u32_e32 v80, s0, v0
	s_ashr_i32 s5, s4, 31
	s_lshl_b64 s[16:17], s[4:5], 10
	v_ashrrev_i32_e32 v81, 31, v80
	v_lshl_add_u64 v[68:69], s[16:17], 0, v[80:81]
	v_lshl_add_u64 v[72:73], v[68:69], 2, s[6:7]
	v_lshlrev_b64 v[74:75], 1, v[68:69]
	s_waitcnt lgkmcnt(0)
	global_load_dwordx4 v[68:71], v[72:73], off
	s_lshl_b64 s[26:27], s[4:5], 6
	v_ashrrev_i32_e32 v82, 6, v80
	s_add_u32 s16, s19, s26
	v_ashrrev_i32_e32 v83, 31, v82
	s_addc_u32 s17, s20, s27
	v_lshl_add_u64 v[84:85], s[12:13], 0, v[74:75]
	v_lshl_add_u64 v[86:87], s[14:15], 0, v[74:75]
	s_nop 0
	v_lshl_add_u64 v[82:83], v[82:83], 2, s[16:17]
	global_load_dwordx2 v[84:85], v[84:85], off
	s_nop 0
	global_load_dwordx2 v[86:87], v[86:87], off
	s_nop 0
	global_load_dword v82, v[82:83], off
	s_lshl_b64 s[4:5], s[4:5], 12
	s_add_u32 s4, s21, s4
	s_addc_u32 s5, s22, s5
	v_lshl_add_u64 v[80:81], v[80:81], 1, s[4:5]
	s_add_i32 s0, s18, 0x800
	s_add_i32 s23, s23, 0x80000
	s_cmpk_lt_i32 s18, 0x7800
	s_mov_b32 s18, s0
	s_waitcnt vmcnt(18)
	v_mov_b32_e32 v120, v101
	v_mov_b32_e32 v121, v102
	v_mov_b32_e32 v122, v100
	v_mov_b32_e32 v123, v103
	v_pk_add_f32 v[120:121], v[120:121], v[122:123]
	s_waitcnt vmcnt(17)
	v_lshlrev_b32_e32 v122, 16, v116
	v_add_f32_e32 v99, v120, v121
	v_and_b32_e32 v123, 0xffff0000, v116
	v_lshlrev_b32_e32 v116, 16, v117
	v_add_f32_dpp v99, v99, v99 quad_perm:[1,0,3,2] row_mask:0xf bank_mask:0xf bound_ctrl:1
	v_and_b32_e32 v117, 0xffff0000, v117
	s_waitcnt vmcnt(16)
	v_lshlrev_b32_e32 v124, 16, v118
	v_add_f32_dpp v99, v99, v99 quad_perm:[2,3,0,1] row_mask:0xf bank_mask:0xf bound_ctrl:1
	v_and_b32_e32 v125, 0xffff0000, v118
	v_lshlrev_b32_e32 v118, 16, v119
	v_add_f32_dpp v99, v99, v99 row_half_mirror row_mask:0xf bank_mask:0xf bound_ctrl:1
	v_and_b32_e32 v119, 0xffff0000, v119
	s_nop 0
	v_add_f32_dpp v99, v99, v99 row_mirror row_mask:0xf bank_mask:0xf bound_ctrl:1
	v_fmamk_f32 v101, v99, 0xbc800000, v101
	v_fmamk_f32 v100, v99, 0xbc800000, v100
	v_fmamk_f32 v103, v99, 0xbc800000, v103
	v_fmac_f32_e32 v102, 0xbc800000, v99
	v_pk_mul_f32 v[120:121], v[102:103], v[102:103]
	v_pk_mul_f32 v[126:127], v[100:101], v[100:101]
	s_nop 0
	v_pk_mov_b32 v[128:129], v[126:127], v[120:121] op_sel:[1,0]
	v_mov_b32_e32 v127, v121
	v_pk_add_f32 v[120:121], v[128:129], v[126:127]
	s_nop 0
	v_add_f32_e32 v99, v120, v121
	s_nop 1
	v_add_f32_dpp v99, v99, v99 quad_perm:[1,0,3,2] row_mask:0xf bank_mask:0xf bound_ctrl:1
	s_nop 1
	v_add_f32_dpp v99, v99, v99 quad_perm:[2,3,0,1] row_mask:0xf bank_mask:0xf bound_ctrl:1
	s_nop 1
	v_add_f32_dpp v99, v99, v99 row_half_mirror row_mask:0xf bank_mask:0xf bound_ctrl:1
	s_nop 1
	v_add_f32_dpp v99, v99, v99 row_mirror row_mask:0xf bank_mask:0xf bound_ctrl:1
	v_fmamk_f32 v99, v99, 0x3c800000, v1
	v_mul_f32_e32 v115, 0x4f800000, v99
	v_cmp_gt_f32_e32 vcc, s24, v99
	s_nop 1
	v_cndmask_b32_e32 v99, v99, v115, vcc
	v_sqrt_f32_e32 v115, v99
	s_nop 0
	v_add_u32_e32 v120, -1, v115
	v_add_u32_e32 v121, 1, v115
	v_fma_f32 v126, -v120, v115, v99
	v_fma_f32 v127, -v121, v115, v99
	v_cmp_ge_f32_e64 s[4:5], 0, v126
	s_nop 1
	v_cndmask_b32_e64 v115, v115, v120, s[4:5]
	v_cmp_lt_f32_e64 s[4:5], 0, v127
	s_nop 1
	v_cndmask_b32_e64 v115, v115, v121, s[4:5]
	v_mul_f32_e32 v120, 0x37800000, v115
	v_cndmask_b32_e32 v115, v115, v120, vcc
	v_cmp_class_f32_e32 vcc, v99, v2
	s_nop 1
	v_cndmask_b32_e32 v99, v115, v99, vcc
	v_div_scale_f32 v115, s[4:5], v99, v99, 1.0
	v_rcp_f32_e32 v121, v115
	v_div_scale_f32 v120, vcc, 1.0, v99, 1.0
	v_fma_f32 v126, -v115, v121, 1.0
	v_fmac_f32_e32 v121, v126, v121
	v_mul_f32_e32 v126, v120, v121
	v_fma_f32 v127, -v115, v126, v120
	v_fmac_f32_e32 v126, v127, v121
	v_fma_f32 v115, -v115, v126, v120
	v_div_fmas_f32 v115, v115, v121, v126
	v_div_fixup_f32 v120, v115, v99, 1.0
	v_pk_mul_f32 v[100:101], v[100:101], v[120:121] op_sel_hi:[1,0]
	v_pk_mul_f32 v[102:103], v[102:103], v[120:121] op_sel_hi:[1,0]
	v_pk_fma_f32 v[100:101], v[130:131], v[100:101], v[134:135]
	v_pk_fma_f32 v[102:103], v[132:133], v[102:103], v[136:137]
	s_waitcnt vmcnt(15)
	v_pk_fma_f32 v[100:101], v[114:115], v[122:123], v[100:101] op_sel_hi:[0,1,1]
	v_pk_fma_f32 v[102:103], v[114:115], v[116:117], v[102:103] op_sel_hi:[0,1,1]
	v_pk_mul_f32 v[102:103], v[102:103], v[118:119]
	v_pk_mul_f32 v[100:101], v[100:101], v[124:125]
	s_nop 0
	v_cvt_pk_bf16_f32 v100, v100, v101
	v_cvt_pk_bf16_f32 v101, v102, v103
	global_store_dwordx2 v[112:113], v[100:101], off
	s_ashr_i32 s4, s18, 2
	s_and_b32 s0, s23, 0x300
	v_add_u32_e32 v112, s0, v0
	s_ashr_i32 s5, s4, 31
	s_lshl_b64 s[16:17], s[4:5], 10
	v_ashrrev_i32_e32 v113, 31, v112
	v_lshl_add_u64 v[100:101], s[16:17], 0, v[112:113]
	v_lshl_add_u64 v[104:105], v[100:101], 2, s[6:7]
	v_lshlrev_b64 v[106:107], 1, v[100:101]
	s_waitcnt lgkmcnt(0)
	global_load_dwordx4 v[100:103], v[104:105], off
	s_lshl_b64 s[26:27], s[4:5], 6
	v_ashrrev_i32_e32 v114, 6, v112
	s_add_u32 s16, s19, s26
	v_ashrrev_i32_e32 v115, 31, v114
	s_addc_u32 s17, s20, s27
	v_lshl_add_u64 v[116:117], s[12:13], 0, v[106:107]
	v_lshl_add_u64 v[118:119], s[14:15], 0, v[106:107]
	s_nop 0
	v_lshl_add_u64 v[114:115], v[114:115], 2, s[16:17]
	global_load_dwordx2 v[116:117], v[116:117], off
	s_nop 0
	global_load_dwordx2 v[118:119], v[118:119], off
	s_nop 0
	global_load_dword v114, v[114:115], off
	s_lshl_b64 s[4:5], s[4:5], 12
	s_add_u32 s4, s21, s4
	s_addc_u32 s5, s22, s5
	v_lshl_add_u64 v[112:113], v[112:113], 1, s[4:5]
	s_add_i32 s0, s18, 0x800
	s_add_i32 s23, s23, 0x80000
	s_cmpk_lt_i32 s18, 0x7800
	s_mov_b32 s18, s0
	s_cbranch_scc1 .LBB0_785
	s_waitcnt vmcnt(18)
	v_mov_b32_e32 v24, v5
	v_mov_b32_e32 v25, v6
	v_mov_b32_e32 v26, v4
	v_mov_b32_e32 v27, v7
	v_pk_add_f32 v[24:25], v[24:25], v[26:27]
	s_waitcnt vmcnt(17)
	v_lshlrev_b32_e32 v26, 16, v20
	v_add_f32_e32 v3, v24, v25
	v_and_b32_e32 v27, 0xffff0000, v20
	v_lshlrev_b32_e32 v20, 16, v21
	v_add_f32_dpp v3, v3, v3 quad_perm:[1,0,3,2] row_mask:0xf bank_mask:0xf bound_ctrl:1
	v_and_b32_e32 v21, 0xffff0000, v21
	s_waitcnt vmcnt(16)
	v_lshlrev_b32_e32 v28, 16, v22
	v_add_f32_dpp v3, v3, v3 quad_perm:[2,3,0,1] row_mask:0xf bank_mask:0xf bound_ctrl:1
	v_and_b32_e32 v29, 0xffff0000, v22
	v_lshlrev_b32_e32 v22, 16, v23
	v_add_f32_dpp v3, v3, v3 row_half_mirror row_mask:0xf bank_mask:0xf bound_ctrl:1
	v_and_b32_e32 v23, 0xffff0000, v23
	s_nop 0
	v_add_f32_dpp v3, v3, v3 row_mirror row_mask:0xf bank_mask:0xf bound_ctrl:1
	v_fmamk_f32 v5, v3, 0xbc800000, v5
	v_fmamk_f32 v4, v3, 0xbc800000, v4
	v_fmamk_f32 v7, v3, 0xbc800000, v7
	v_fmac_f32_e32 v6, 0xbc800000, v3
	v_pk_mul_f32 v[24:25], v[6:7], v[6:7]
	v_pk_mul_f32 v[30:31], v[4:5], v[4:5]
	s_nop 0
	v_pk_mov_b32 v[32:33], v[30:31], v[24:25] op_sel:[1,0]
	v_mov_b32_e32 v31, v25
	v_pk_add_f32 v[24:25], v[32:33], v[30:31]
	s_nop 0
	v_add_f32_e32 v3, v24, v25
	s_nop 1
	v_add_f32_dpp v3, v3, v3 quad_perm:[1,0,3,2] row_mask:0xf bank_mask:0xf bound_ctrl:1
	s_nop 1
	v_add_f32_dpp v3, v3, v3 quad_perm:[2,3,0,1] row_mask:0xf bank_mask:0xf bound_ctrl:1
	s_nop 1
	v_add_f32_dpp v3, v3, v3 row_half_mirror row_mask:0xf bank_mask:0xf bound_ctrl:1
	s_nop 1
	v_add_f32_dpp v3, v3, v3 row_mirror row_mask:0xf bank_mask:0xf bound_ctrl:1
	v_fmamk_f32 v3, v3, 0x3c800000, v1
	v_mul_f32_e32 v19, 0x4f800000, v3
	v_cmp_gt_f32_e32 vcc, s24, v3
	s_nop 1
	v_cndmask_b32_e32 v3, v3, v19, vcc
	v_sqrt_f32_e32 v19, v3
	s_nop 0
	v_add_u32_e32 v24, -1, v19
	v_add_u32_e32 v25, 1, v19
	v_fma_f32 v30, -v24, v19, v3
	v_fma_f32 v31, -v25, v19, v3
	v_cmp_ge_f32_e64 s[4:5], 0, v30
	s_nop 1
	v_cndmask_b32_e64 v19, v19, v24, s[4:5]
	v_cmp_lt_f32_e64 s[4:5], 0, v31
	s_nop 1
	v_cndmask_b32_e64 v19, v19, v25, s[4:5]
	v_mul_f32_e32 v24, 0x37800000, v19
	v_cndmask_b32_e32 v19, v19, v24, vcc
	v_cmp_class_f32_e32 vcc, v3, v2
	s_nop 1
	v_cndmask_b32_e32 v3, v19, v3, vcc
	v_div_scale_f32 v19, s[4:5], v3, v3, 1.0
	v_rcp_f32_e32 v25, v19
	v_div_scale_f32 v24, vcc, 1.0, v3, 1.0
	v_fma_f32 v30, -v19, v25, 1.0
	v_fmac_f32_e32 v25, v30, v25
	v_mul_f32_e32 v30, v24, v25
	v_fma_f32 v31, -v19, v30, v24
	v_fmac_f32_e32 v30, v31, v25
	v_fma_f32 v19, -v19, v30, v24
	v_div_fmas_f32 v19, v19, v25, v30
	v_div_fixup_f32 v24, v19, v3, 1.0
	v_pk_mul_f32 v[4:5], v[4:5], v[24:25] op_sel_hi:[1,0]
	v_pk_mul_f32 v[6:7], v[6:7], v[24:25] op_sel_hi:[1,0]
	v_pk_fma_f32 v[4:5], v[130:131], v[4:5], v[134:135]
	v_pk_fma_f32 v[6:7], v[132:133], v[6:7], v[136:137]
	s_waitcnt vmcnt(15)
	v_pk_fma_f32 v[4:5], v[18:19], v[26:27], v[4:5] op_sel_hi:[0,1,1]
	v_pk_fma_f32 v[6:7], v[18:19], v[20:21], v[6:7] op_sel_hi:[0,1,1]
	v_pk_mul_f32 v[6:7], v[6:7], v[22:23]
	v_pk_mul_f32 v[4:5], v[4:5], v[28:29]
	s_nop 0
	v_cvt_pk_bf16_f32 v4, v4, v5
	v_cvt_pk_bf16_f32 v5, v6, v7
	global_store_dwordx2 v[16:17], v[4:5], off
	s_waitcnt vmcnt(14)
	v_mov_b32_e32 v56, v37
	v_mov_b32_e32 v57, v38
	v_mov_b32_e32 v58, v36
	v_mov_b32_e32 v59, v39
	v_pk_add_f32 v[56:57], v[56:57], v[58:59]
	s_waitcnt vmcnt(13)
	v_lshlrev_b32_e32 v58, 16, v52
	v_add_f32_e32 v35, v56, v57
	v_and_b32_e32 v59, 0xffff0000, v52
	v_lshlrev_b32_e32 v52, 16, v53
	v_add_f32_dpp v35, v35, v35 quad_perm:[1,0,3,2] row_mask:0xf bank_mask:0xf bound_ctrl:1
	v_and_b32_e32 v53, 0xffff0000, v53
	s_waitcnt vmcnt(12)
	v_lshlrev_b32_e32 v60, 16, v54
	v_add_f32_dpp v35, v35, v35 quad_perm:[2,3,0,1] row_mask:0xf bank_mask:0xf bound_ctrl:1
	v_and_b32_e32 v61, 0xffff0000, v54
	v_lshlrev_b32_e32 v54, 16, v55
	v_add_f32_dpp v35, v35, v35 row_half_mirror row_mask:0xf bank_mask:0xf bound_ctrl:1
	v_and_b32_e32 v55, 0xffff0000, v55
	s_nop 0
	v_add_f32_dpp v35, v35, v35 row_mirror row_mask:0xf bank_mask:0xf bound_ctrl:1
	v_fmamk_f32 v37, v35, 0xbc800000, v37
	v_fmamk_f32 v36, v35, 0xbc800000, v36
	v_fmamk_f32 v39, v35, 0xbc800000, v39
	v_fmac_f32_e32 v38, 0xbc800000, v35
	v_pk_mul_f32 v[56:57], v[38:39], v[38:39]
	v_pk_mul_f32 v[62:63], v[36:37], v[36:37]
	s_nop 0
	v_pk_mov_b32 v[64:65], v[62:63], v[56:57] op_sel:[1,0]
	v_mov_b32_e32 v63, v57
	v_pk_add_f32 v[56:57], v[64:65], v[62:63]
	s_nop 0
	v_add_f32_e32 v35, v56, v57
	s_nop 1
	v_add_f32_dpp v35, v35, v35 quad_perm:[1,0,3,2] row_mask:0xf bank_mask:0xf bound_ctrl:1
	s_nop 1
	v_add_f32_dpp v35, v35, v35 quad_perm:[2,3,0,1] row_mask:0xf bank_mask:0xf bound_ctrl:1
	s_nop 1
	v_add_f32_dpp v35, v35, v35 row_half_mirror row_mask:0xf bank_mask:0xf bound_ctrl:1
	s_nop 1
	v_add_f32_dpp v35, v35, v35 row_mirror row_mask:0xf bank_mask:0xf bound_ctrl:1
	v_fmamk_f32 v35, v35, 0x3c800000, v1
	v_mul_f32_e32 v51, 0x4f800000, v35
	v_cmp_gt_f32_e32 vcc, s24, v35
	s_nop 1
	v_cndmask_b32_e32 v35, v35, v51, vcc
	v_sqrt_f32_e32 v51, v35
	s_nop 0
	v_add_u32_e32 v56, -1, v51
	v_add_u32_e32 v57, 1, v51
	v_fma_f32 v62, -v56, v51, v35
	v_fma_f32 v63, -v57, v51, v35
	v_cmp_ge_f32_e64 s[4:5], 0, v62
	s_nop 1
	v_cndmask_b32_e64 v51, v51, v56, s[4:5]
	v_cmp_lt_f32_e64 s[4:5], 0, v63
	s_nop 1
	v_cndmask_b32_e64 v51, v51, v57, s[4:5]
	v_mul_f32_e32 v56, 0x37800000, v51
	v_cndmask_b32_e32 v51, v51, v56, vcc
	v_cmp_class_f32_e32 vcc, v35, v2
	s_nop 1
	v_cndmask_b32_e32 v35, v51, v35, vcc
	v_div_scale_f32 v51, s[4:5], v35, v35, 1.0
	v_rcp_f32_e32 v57, v51
	v_div_scale_f32 v56, vcc, 1.0, v35, 1.0
	v_fma_f32 v62, -v51, v57, 1.0
	v_fmac_f32_e32 v57, v62, v57
	v_mul_f32_e32 v62, v56, v57
	v_fma_f32 v63, -v51, v62, v56
	v_fmac_f32_e32 v62, v63, v57
	v_fma_f32 v51, -v51, v62, v56
	v_div_fmas_f32 v51, v51, v57, v62
	v_div_fixup_f32 v56, v51, v35, 1.0
	v_pk_mul_f32 v[36:37], v[36:37], v[56:57] op_sel_hi:[1,0]
	v_pk_mul_f32 v[38:39], v[38:39], v[56:57] op_sel_hi:[1,0]
	v_pk_fma_f32 v[36:37], v[130:131], v[36:37], v[134:135]
	v_pk_fma_f32 v[38:39], v[132:133], v[38:39], v[136:137]
	s_waitcnt vmcnt(11)
	v_pk_fma_f32 v[36:37], v[50:51], v[58:59], v[36:37] op_sel_hi:[0,1,1]
	v_pk_fma_f32 v[38:39], v[50:51], v[52:53], v[38:39] op_sel_hi:[0,1,1]
	v_pk_mul_f32 v[38:39], v[38:39], v[54:55]
	v_pk_mul_f32 v[36:37], v[36:37], v[60:61]
	s_nop 0
	v_cvt_pk_bf16_f32 v36, v36, v37
	v_cvt_pk_bf16_f32 v37, v38, v39
	global_store_dwordx2 v[48:49], v[36:37], off
	s_waitcnt vmcnt(10)
	v_mov_b32_e32 v88, v69
	v_mov_b32_e32 v89, v70
	v_mov_b32_e32 v90, v68
	v_mov_b32_e32 v91, v71
	v_pk_add_f32 v[88:89], v[88:89], v[90:91]
	s_waitcnt vmcnt(9)
	v_lshlrev_b32_e32 v90, 16, v84
	v_add_f32_e32 v67, v88, v89
	v_and_b32_e32 v91, 0xffff0000, v84
	v_lshlrev_b32_e32 v84, 16, v85
	v_add_f32_dpp v67, v67, v67 quad_perm:[1,0,3,2] row_mask:0xf bank_mask:0xf bound_ctrl:1
	v_and_b32_e32 v85, 0xffff0000, v85
	s_waitcnt vmcnt(8)
	v_lshlrev_b32_e32 v92, 16, v86
	v_add_f32_dpp v67, v67, v67 quad_perm:[2,3,0,1] row_mask:0xf bank_mask:0xf bound_ctrl:1
	v_and_b32_e32 v93, 0xffff0000, v86
	v_lshlrev_b32_e32 v86, 16, v87
	v_add_f32_dpp v67, v67, v67 row_half_mirror row_mask:0xf bank_mask:0xf bound_ctrl:1
	v_and_b32_e32 v87, 0xffff0000, v87
	s_nop 0
	v_add_f32_dpp v67, v67, v67 row_mirror row_mask:0xf bank_mask:0xf bound_ctrl:1
	v_fmamk_f32 v69, v67, 0xbc800000, v69
	v_fmamk_f32 v68, v67, 0xbc800000, v68
	v_fmamk_f32 v71, v67, 0xbc800000, v71
	v_fmac_f32_e32 v70, 0xbc800000, v67
	v_pk_mul_f32 v[88:89], v[70:71], v[70:71]
	v_pk_mul_f32 v[94:95], v[68:69], v[68:69]
	s_nop 0
	v_pk_mov_b32 v[96:97], v[94:95], v[88:89] op_sel:[1,0]
	v_mov_b32_e32 v95, v89
	v_pk_add_f32 v[88:89], v[96:97], v[94:95]
	s_nop 0
	v_add_f32_e32 v67, v88, v89
	s_nop 1
	v_add_f32_dpp v67, v67, v67 quad_perm:[1,0,3,2] row_mask:0xf bank_mask:0xf bound_ctrl:1
	s_nop 1
	v_add_f32_dpp v67, v67, v67 quad_perm:[2,3,0,1] row_mask:0xf bank_mask:0xf bound_ctrl:1
	s_nop 1
	v_add_f32_dpp v67, v67, v67 row_half_mirror row_mask:0xf bank_mask:0xf bound_ctrl:1
	s_nop 1
	v_add_f32_dpp v67, v67, v67 row_mirror row_mask:0xf bank_mask:0xf bound_ctrl:1
	v_fmamk_f32 v67, v67, 0x3c800000, v1
	v_mul_f32_e32 v83, 0x4f800000, v67
	v_cmp_gt_f32_e32 vcc, s24, v67
	s_nop 1
	v_cndmask_b32_e32 v67, v67, v83, vcc
	v_sqrt_f32_e32 v83, v67
	s_nop 0
	v_add_u32_e32 v88, -1, v83
	v_add_u32_e32 v89, 1, v83
	v_fma_f32 v94, -v88, v83, v67
	v_fma_f32 v95, -v89, v83, v67
	v_cmp_ge_f32_e64 s[4:5], 0, v94
	s_nop 1
	v_cndmask_b32_e64 v83, v83, v88, s[4:5]
	v_cmp_lt_f32_e64 s[4:5], 0, v95
	s_nop 1
	v_cndmask_b32_e64 v83, v83, v89, s[4:5]
	v_mul_f32_e32 v88, 0x37800000, v83
	v_cndmask_b32_e32 v83, v83, v88, vcc
	v_cmp_class_f32_e32 vcc, v67, v2
	s_nop 1
	v_cndmask_b32_e32 v67, v83, v67, vcc
	v_div_scale_f32 v83, s[4:5], v67, v67, 1.0
	v_rcp_f32_e32 v89, v83
	v_div_scale_f32 v88, vcc, 1.0, v67, 1.0
	v_fma_f32 v94, -v83, v89, 1.0
	v_fmac_f32_e32 v89, v94, v89
	v_mul_f32_e32 v94, v88, v89
	v_fma_f32 v95, -v83, v94, v88
	v_fmac_f32_e32 v94, v95, v89
	v_fma_f32 v83, -v83, v94, v88
	v_div_fmas_f32 v83, v83, v89, v94
	v_div_fixup_f32 v88, v83, v67, 1.0
	v_pk_mul_f32 v[68:69], v[68:69], v[88:89] op_sel_hi:[1,0]
	v_pk_mul_f32 v[70:71], v[70:71], v[88:89] op_sel_hi:[1,0]
	v_pk_fma_f32 v[68:69], v[130:131], v[68:69], v[134:135]
	v_pk_fma_f32 v[70:71], v[132:133], v[70:71], v[136:137]
	s_waitcnt vmcnt(7)
	v_pk_fma_f32 v[68:69], v[82:83], v[90:91], v[68:69] op_sel_hi:[0,1,1]
	v_pk_fma_f32 v[70:71], v[82:83], v[84:85], v[70:71] op_sel_hi:[0,1,1]
	v_pk_mul_f32 v[70:71], v[70:71], v[86:87]
	v_pk_mul_f32 v[68:69], v[68:69], v[92:93]
	s_nop 0
	v_cvt_pk_bf16_f32 v68, v68, v69
	v_cvt_pk_bf16_f32 v69, v70, v71
	global_store_dwordx2 v[80:81], v[68:69], off
	s_waitcnt vmcnt(6)
	v_mov_b32_e32 v120, v101
	v_mov_b32_e32 v121, v102
	v_mov_b32_e32 v122, v100
	v_mov_b32_e32 v123, v103
	v_pk_add_f32 v[120:121], v[120:121], v[122:123]
	s_waitcnt vmcnt(5)
	v_lshlrev_b32_e32 v122, 16, v116
	v_add_f32_e32 v99, v120, v121
	v_and_b32_e32 v123, 0xffff0000, v116
	v_lshlrev_b32_e32 v116, 16, v117
	v_add_f32_dpp v99, v99, v99 quad_perm:[1,0,3,2] row_mask:0xf bank_mask:0xf bound_ctrl:1
	v_and_b32_e32 v117, 0xffff0000, v117
	s_waitcnt vmcnt(4)
	v_lshlrev_b32_e32 v124, 16, v118
	v_add_f32_dpp v99, v99, v99 quad_perm:[2,3,0,1] row_mask:0xf bank_mask:0xf bound_ctrl:1
	v_and_b32_e32 v125, 0xffff0000, v118
	v_lshlrev_b32_e32 v118, 16, v119
	v_add_f32_dpp v99, v99, v99 row_half_mirror row_mask:0xf bank_mask:0xf bound_ctrl:1
	v_and_b32_e32 v119, 0xffff0000, v119
	s_nop 0
	v_add_f32_dpp v99, v99, v99 row_mirror row_mask:0xf bank_mask:0xf bound_ctrl:1
	v_fmamk_f32 v101, v99, 0xbc800000, v101
	v_fmamk_f32 v100, v99, 0xbc800000, v100
	v_fmamk_f32 v103, v99, 0xbc800000, v103
	v_fmac_f32_e32 v102, 0xbc800000, v99
	v_pk_mul_f32 v[120:121], v[102:103], v[102:103]
	v_pk_mul_f32 v[126:127], v[100:101], v[100:101]
	s_nop 0
	v_pk_mov_b32 v[128:129], v[126:127], v[120:121] op_sel:[1,0]
	v_mov_b32_e32 v127, v121
	v_pk_add_f32 v[120:121], v[128:129], v[126:127]
	s_nop 0
	v_add_f32_e32 v99, v120, v121
	s_nop 1
	v_add_f32_dpp v99, v99, v99 quad_perm:[1,0,3,2] row_mask:0xf bank_mask:0xf bound_ctrl:1
	s_nop 1
	v_add_f32_dpp v99, v99, v99 quad_perm:[2,3,0,1] row_mask:0xf bank_mask:0xf bound_ctrl:1
	s_nop 1
	v_add_f32_dpp v99, v99, v99 row_half_mirror row_mask:0xf bank_mask:0xf bound_ctrl:1
	s_nop 1
	v_add_f32_dpp v99, v99, v99 row_mirror row_mask:0xf bank_mask:0xf bound_ctrl:1
	v_fmamk_f32 v99, v99, 0x3c800000, v1
	v_mul_f32_e32 v115, 0x4f800000, v99
	v_cmp_gt_f32_e32 vcc, s24, v99
	s_nop 1
	v_cndmask_b32_e32 v99, v99, v115, vcc
	v_sqrt_f32_e32 v115, v99
	s_nop 0
	v_add_u32_e32 v120, -1, v115
	v_add_u32_e32 v121, 1, v115
	v_fma_f32 v126, -v120, v115, v99
	v_fma_f32 v127, -v121, v115, v99
	v_cmp_ge_f32_e64 s[4:5], 0, v126
	s_nop 1
	v_cndmask_b32_e64 v115, v115, v120, s[4:5]
	v_cmp_lt_f32_e64 s[4:5], 0, v127
	s_nop 1
	v_cndmask_b32_e64 v115, v115, v121, s[4:5]
	v_mul_f32_e32 v120, 0x37800000, v115
	v_cndmask_b32_e32 v115, v115, v120, vcc
	v_cmp_class_f32_e32 vcc, v99, v2
	s_nop 1
	v_cndmask_b32_e32 v99, v115, v99, vcc
	v_div_scale_f32 v115, s[4:5], v99, v99, 1.0
	v_rcp_f32_e32 v121, v115
	v_div_scale_f32 v120, vcc, 1.0, v99, 1.0
	v_fma_f32 v126, -v115, v121, 1.0
	v_fmac_f32_e32 v121, v126, v121
	v_mul_f32_e32 v126, v120, v121
	v_fma_f32 v127, -v115, v126, v120
	v_fmac_f32_e32 v126, v127, v121
	v_fma_f32 v115, -v115, v126, v120
	v_div_fmas_f32 v115, v115, v121, v126
	v_div_fixup_f32 v120, v115, v99, 1.0
	v_pk_mul_f32 v[100:101], v[100:101], v[120:121] op_sel_hi:[1,0]
	v_pk_mul_f32 v[102:103], v[102:103], v[120:121] op_sel_hi:[1,0]
	v_pk_fma_f32 v[100:101], v[130:131], v[100:101], v[134:135]
	v_pk_fma_f32 v[102:103], v[132:133], v[102:103], v[136:137]
	s_waitcnt vmcnt(3)
	v_pk_fma_f32 v[100:101], v[114:115], v[122:123], v[100:101] op_sel_hi:[0,1,1]
	v_pk_fma_f32 v[102:103], v[114:115], v[116:117], v[102:103] op_sel_hi:[0,1,1]
	v_pk_mul_f32 v[102:103], v[102:103], v[118:119]
	v_pk_mul_f32 v[100:101], v[100:101], v[124:125]
	s_nop 0
	v_cvt_pk_bf16_f32 v100, v100, v101
	v_cvt_pk_bf16_f32 v101, v102, v103
	global_store_dwordx2 v[112:113], v[100:101], off
	s_load_dwordx2 s[4:5], s[52:53], 0x188

.LBB0_1877:
	s_or_b64 exec, exec, s[4:5]
	v_mov_b32_e32 v1, s2
	s_waitcnt lgkmcnt(0)
	s_barrier
	v_mbcnt_lo_u32_b32 v0, -1, 0
	v_mbcnt_hi_u32_b32 v0, -1, v0
	v_readlane_b32 s0, v254, 18
	v_readfirstlane_b32 s16, v1
	v_mov_b32_e32 v1, 0
	v_readlane_b32 s1, v254, 19
	s_load_dwordx2 s[6:7], s[0:1], 0x188
	s_lshl_b32 s0, s16, 3
	s_add_i32 s18, s0, s76
	s_cmpk_gt_i32 s18, 0x7fff
	v_readfirstlane_b32 s4, v1
	s_cbranch_scc1 .LBB0_1881
	s_ashr_i32 s0, s4, 31
	s_waitcnt lgkmcnt(0)
	s_add_u32 s1, s6, s4
	v_readlane_b32 s4, v254, 18
	s_addc_u32 s0, s7, s0
	v_readlane_b32 s5, v254, 19
	s_load_dwordx4 s[8:11], s[4:5], 0x130
	s_add_u32 s4, s1, 0x4c480000
	s_addc_u32 s5, s0, 0
	s_add_u32 s12, s1, 0x48480000
	s_addc_u32 s13, s0, 0
	s_add_u32 s14, s1, 0x4a480000
	s_addc_u32 s15, s0, 0
	s_add_u32 s19, s1, 0x4c0000
	s_addc_u32 s20, s0, 0
	s_add_u32 s21, s1, 0x35c80000
	s_addc_u32 s22, s0, 0
	s_lshl_b32 s0, s16, 11
	s_lshl_b32 s1, s76, 8
	v_lshlrev_b32_e32 v0, 2, v0
	s_add_i32 s23, s0, s1
	v_mov_b32_e32 v1, 0x3a27c5ac
	s_mov_b32 s24, 0xf800000
	v_mov_b32_e32 v2, 0x260
	s_waitcnt lgkmcnt(0)
	s_and_b32 s0, s23, 0x300
	v_add_u32_e32 v130, s0, v0
	v_lshlrev_b32_e32 v130, 2, v130
	global_load_dwordx4 v[134:137], v130, s[10:11]
	global_load_dwordx4 v[130:133], v130, s[8:9]
	s_ashr_i32 s6, s18, 2
	s_and_b32 s0, s23, 0x300
	v_add_u32_e32 v16, s0, v0
	s_ashr_i32 s7, s6, 31
	s_lshl_b64 s[0:1], s[6:7], 10
	v_ashrrev_i32_e32 v17, 31, v16
	v_lshl_add_u64 v[4:5], s[0:1], 0, v[16:17]
	v_lshl_add_u64 v[8:9], v[4:5], 2, s[4:5]
	v_lshlrev_b64 v[10:11], 1, v[4:5]
	s_waitcnt lgkmcnt(0)
	global_load_dwordx4 v[4:7], v[8:9], off
	s_lshl_b64 s[16:17], s[6:7], 6
	v_ashrrev_i32_e32 v18, 6, v16
	s_add_u32 s16, s19, s16
	v_ashrrev_i32_e32 v19, 31, v18
	s_addc_u32 s17, s20, s17
	v_lshl_add_u64 v[20:21], s[12:13], 0, v[10:11]
	v_lshl_add_u64 v[22:23], s[14:15], 0, v[10:11]
	s_nop 0
	v_lshl_add_u64 v[18:19], v[18:19], 2, s[16:17]
	global_load_dwordx2 v[20:21], v[20:21], off
	s_nop 0
	global_load_dwordx2 v[22:23], v[22:23], off
	s_nop 0
	global_load_dword v18, v[18:19], off
	s_lshl_b64 s[0:1], s[6:7], 12
	s_add_u32 s0, s21, s0
	s_addc_u32 s1, s22, s1
	s_add_i32 s6, s18, 0x800
	s_add_i32 s23, s23, 0x80000
	s_cmpk_lt_i32 s18, 0x7800
	s_mov_b32 s18, s6
	v_lshl_add_u64 v[16:17], v[16:17], 1, s[0:1]
	s_ashr_i32 s6, s18, 2
	s_and_b32 s0, s23, 0x300
	v_add_u32_e32 v48, s0, v0
	s_ashr_i32 s7, s6, 31
	s_lshl_b64 s[0:1], s[6:7], 10
	v_ashrrev_i32_e32 v49, 31, v48
	v_lshl_add_u64 v[36:37], s[0:1], 0, v[48:49]
	v_lshl_add_u64 v[40:41], v[36:37], 2, s[4:5]
	v_lshlrev_b64 v[42:43], 1, v[36:37]
	s_waitcnt lgkmcnt(0)
	global_load_dwordx4 v[36:39], v[40:41], off
	s_lshl_b64 s[16:17], s[6:7], 6
	v_ashrrev_i32_e32 v50, 6, v48
	s_add_u32 s16, s19, s16
	v_ashrrev_i32_e32 v51, 31, v50
	s_addc_u32 s17, s20, s17
	v_lshl_add_u64 v[52:53], s[12:13], 0, v[42:43]
	v_lshl_add_u64 v[54:55], s[14:15], 0, v[42:43]
	s_nop 0
	v_lshl_add_u64 v[50:51], v[50:51], 2, s[16:17]
	global_load_dwordx2 v[52:53], v[52:53], off
	s_nop 0
	global_load_dwordx2 v[54:55], v[54:55], off
	s_nop 0
	global_load_dword v50, v[50:51], off
	s_lshl_b64 s[0:1], s[6:7], 12
	s_add_u32 s0, s21, s0
	s_addc_u32 s1, s22, s1
	s_add_i32 s6, s18, 0x800
	s_add_i32 s23, s23, 0x80000
	s_cmpk_lt_i32 s18, 0x7800
	s_mov_b32 s18, s6
	v_lshl_add_u64 v[48:49], v[48:49], 1, s[0:1]
	s_ashr_i32 s6, s18, 2
	s_and_b32 s0, s23, 0x300
	v_add_u32_e32 v80, s0, v0
	s_ashr_i32 s7, s6, 31
	s_lshl_b64 s[0:1], s[6:7], 10
	v_ashrrev_i32_e32 v81, 31, v80
	v_lshl_add_u64 v[68:69], s[0:1], 0, v[80:81]
	v_lshl_add_u64 v[72:73], v[68:69], 2, s[4:5]
	v_lshlrev_b64 v[74:75], 1, v[68:69]
	s_waitcnt lgkmcnt(0)
	global_load_dwordx4 v[68:71], v[72:73], off
	s_lshl_b64 s[16:17], s[6:7], 6
	v_ashrrev_i32_e32 v82, 6, v80
	s_add_u32 s16, s19, s16
	v_ashrrev_i32_e32 v83, 31, v82
	s_addc_u32 s17, s20, s17
	v_lshl_add_u64 v[84:85], s[12:13], 0, v[74:75]
	v_lshl_add_u64 v[86:87], s[14:15], 0, v[74:75]
	s_nop 0
	v_lshl_add_u64 v[82:83], v[82:83], 2, s[16:17]
	global_load_dwordx2 v[84:85], v[84:85], off
	s_nop 0
	global_load_dwordx2 v[86:87], v[86:87], off
	s_nop 0
	global_load_dword v82, v[82:83], off
	s_lshl_b64 s[0:1], s[6:7], 12
	s_add_u32 s0, s21, s0
	s_addc_u32 s1, s22, s1
	s_add_i32 s6, s18, 0x800
	s_add_i32 s23, s23, 0x80000
	s_cmpk_lt_i32 s18, 0x7800
	s_mov_b32 s18, s6
	v_lshl_add_u64 v[80:81], v[80:81], 1, s[0:1]
	s_ashr_i32 s6, s18, 2
	s_and_b32 s0, s23, 0x300
	v_add_u32_e32 v112, s0, v0
	s_ashr_i32 s7, s6, 31
	s_lshl_b64 s[0:1], s[6:7], 10
	v_ashrrev_i32_e32 v113, 31, v112
	v_lshl_add_u64 v[100:101], s[0:1], 0, v[112:113]
	v_lshl_add_u64 v[104:105], v[100:101], 2, s[4:5]
	v_lshlrev_b64 v[106:107], 1, v[100:101]
	s_waitcnt lgkmcnt(0)
	global_load_dwordx4 v[100:103], v[104:105], off
	s_lshl_b64 s[16:17], s[6:7], 6
	v_ashrrev_i32_e32 v114, 6, v112
	s_add_u32 s16, s19, s16
	v_ashrrev_i32_e32 v115, 31, v114
	s_addc_u32 s17, s20, s17
	v_lshl_add_u64 v[116:117], s[12:13], 0, v[106:107]
	v_lshl_add_u64 v[118:119], s[14:15], 0, v[106:107]
	s_nop 0
	v_lshl_add_u64 v[114:115], v[114:115], 2, s[16:17]
	global_load_dwordx2 v[116:117], v[116:117], off
	s_nop 0
	global_load_dwordx2 v[118:119], v[118:119], off
	s_nop 0
	global_load_dword v114, v[114:115], off
	s_lshl_b64 s[0:1], s[6:7], 12
	s_add_u32 s0, s21, s0
	s_addc_u32 s1, s22, s1
	s_add_i32 s6, s18, 0x800
	s_add_i32 s23, s23, 0x80000
	s_cmpk_lt_i32 s18, 0x7800
	s_mov_b32 s18, s6
	v_lshl_add_u64 v[112:113], v[112:113], 1, s[0:1]
	s_waitcnt vmcnt(15)
	v_mov_b32_e32 v24, v5
	v_mov_b32_e32 v25, v6
	v_mov_b32_e32 v26, v4
	v_mov_b32_e32 v27, v7
	v_pk_add_f32 v[24:25], v[24:25], v[26:27]
	s_waitcnt vmcnt(14)
	v_lshlrev_b32_e32 v26, 16, v20
	v_add_f32_e32 v3, v24, v25
	v_and_b32_e32 v27, 0xffff0000, v20
	v_lshlrev_b32_e32 v20, 16, v21
	v_add_f32_dpp v3, v3, v3 quad_perm:[1,0,3,2] row_mask:0xf bank_mask:0xf bound_ctrl:1
	v_and_b32_e32 v21, 0xffff0000, v21
	s_waitcnt vmcnt(13)
	v_lshlrev_b32_e32 v28, 16, v22
	v_add_f32_dpp v3, v3, v3 quad_perm:[2,3,0,1] row_mask:0xf bank_mask:0xf bound_ctrl:1
	v_and_b32_e32 v29, 0xffff0000, v22
	v_lshlrev_b32_e32 v22, 16, v23
	v_add_f32_dpp v3, v3, v3 row_half_mirror row_mask:0xf bank_mask:0xf bound_ctrl:1
	v_and_b32_e32 v23, 0xffff0000, v23
	s_nop 0
	v_add_f32_dpp v3, v3, v3 row_mirror row_mask:0xf bank_mask:0xf bound_ctrl:1
	v_fmamk_f32 v5, v3, 0xbc800000, v5
	v_fmamk_f32 v4, v3, 0xbc800000, v4
	v_fmamk_f32 v7, v3, 0xbc800000, v7
	v_fmac_f32_e32 v6, 0xbc800000, v3
	v_pk_mul_f32 v[24:25], v[6:7], v[6:7]
	v_pk_mul_f32 v[30:31], v[4:5], v[4:5]
	s_nop 0
	v_pk_mov_b32 v[32:33], v[30:31], v[24:25] op_sel:[1,0]
	v_mov_b32_e32 v31, v25
	v_pk_add_f32 v[24:25], v[32:33], v[30:31]
	s_nop 0
	v_add_f32_e32 v3, v24, v25
	s_nop 1
	v_add_f32_dpp v3, v3, v3 quad_perm:[1,0,3,2] row_mask:0xf bank_mask:0xf bound_ctrl:1
	s_nop 1
	v_add_f32_dpp v3, v3, v3 quad_perm:[2,3,0,1] row_mask:0xf bank_mask:0xf bound_ctrl:1
	s_nop 1
	v_add_f32_dpp v3, v3, v3 row_half_mirror row_mask:0xf bank_mask:0xf bound_ctrl:1
	s_nop 1
	v_add_f32_dpp v3, v3, v3 row_mirror row_mask:0xf bank_mask:0xf bound_ctrl:1
	v_fmamk_f32 v3, v3, 0x3c800000, v1
	v_mul_f32_e32 v19, 0x4f800000, v3
	v_cmp_gt_f32_e32 vcc, s24, v3
	s_nop 1
	v_cndmask_b32_e32 v3, v3, v19, vcc
	v_sqrt_f32_e32 v19, v3
	s_nop 0
	v_add_u32_e32 v24, -1, v19
	v_add_u32_e32 v25, 1, v19
	v_fma_f32 v30, -v24, v19, v3
	v_fma_f32 v31, -v25, v19, v3
	v_cmp_ge_f32_e64 s[6:7], 0, v30
	s_nop 1
	v_cndmask_b32_e64 v19, v19, v24, s[6:7]
	v_cmp_lt_f32_e64 s[6:7], 0, v31
	s_nop 1
	v_cndmask_b32_e64 v19, v19, v25, s[6:7]
	v_mul_f32_e32 v24, 0x37800000, v19
	v_cndmask_b32_e32 v19, v19, v24, vcc
	v_cmp_class_f32_e32 vcc, v3, v2
	s_nop 1
	v_cndmask_b32_e32 v3, v19, v3, vcc
	v_div_scale_f32 v19, s[0:1], v3, v3, 1.0
	v_rcp_f32_e32 v25, v19
	v_div_scale_f32 v24, vcc, 1.0, v3, 1.0
	v_fma_f32 v30, -v19, v25, 1.0
	v_fmac_f32_e32 v25, v30, v25
	v_mul_f32_e32 v30, v24, v25
	v_fma_f32 v31, -v19, v30, v24
	v_fmac_f32_e32 v30, v31, v25
	v_fma_f32 v19, -v19, v30, v24
	v_div_fmas_f32 v19, v19, v25, v30
	v_div_fixup_f32 v24, v19, v3, 1.0
	v_pk_mul_f32 v[4:5], v[4:5], v[24:25] op_sel_hi:[1,0]
	v_pk_mul_f32 v[6:7], v[6:7], v[24:25] op_sel_hi:[1,0]
	v_pk_fma_f32 v[4:5], v[130:131], v[4:5], v[134:135]
	v_pk_fma_f32 v[6:7], v[132:133], v[6:7], v[136:137]
	s_waitcnt vmcnt(12)
	v_pk_fma_f32 v[4:5], v[18:19], v[26:27], v[4:5] op_sel_hi:[0,1,1]
	v_pk_fma_f32 v[6:7], v[18:19], v[20:21], v[6:7] op_sel_hi:[0,1,1]
	v_pk_mul_f32 v[6:7], v[6:7], v[22:23]
	v_pk_mul_f32 v[4:5], v[4:5], v[28:29]
	s_nop 0
	v_cvt_pk_bf16_f32 v4, v4, v5
	v_cvt_pk_bf16_f32 v5, v6, v7
	global_store_dwordx2 v[16:17], v[4:5], off
	s_ashr_i32 s6, s18, 2
	s_and_b32 s0, s23, 0x300
	v_add_u32_e32 v16, s0, v0
	s_ashr_i32 s7, s6, 31
	s_lshl_b64 s[0:1], s[6:7], 10
	v_ashrrev_i32_e32 v17, 31, v16
	v_lshl_add_u64 v[4:5], s[0:1], 0, v[16:17]
	v_lshl_add_u64 v[8:9], v[4:5], 2, s[4:5]
	v_lshlrev_b64 v[10:11], 1, v[4:5]
	s_waitcnt lgkmcnt(0)
	global_load_dwordx4 v[4:7], v[8:9], off
	s_lshl_b64 s[16:17], s[6:7], 6
	v_ashrrev_i32_e32 v18, 6, v16
	s_add_u32 s16, s19, s16
	v_ashrrev_i32_e32 v19, 31, v18
	s_addc_u32 s17, s20, s17
	v_lshl_add_u64 v[20:21], s[12:13], 0, v[10:11]
	v_lshl_add_u64 v[22:23], s[14:15], 0, v[10:11]
	s_nop 0
	v_lshl_add_u64 v[18:19], v[18:19], 2, s[16:17]
	global_load_dwordx2 v[20:21], v[20:21], off
	s_nop 0
	global_load_dwordx2 v[22:23], v[22:23], off
	s_nop 0
	global_load_dword v18, v[18:19], off
	s_lshl_b64 s[0:1], s[6:7], 12
	s_add_u32 s0, s21, s0
	s_addc_u32 s1, s22, s1
	s_add_i32 s6, s18, 0x800
	s_add_i32 s23, s23, 0x80000
	s_cmpk_lt_i32 s18, 0x7800
	s_mov_b32 s18, s6
	v_lshl_add_u64 v[16:17], v[16:17], 1, s[0:1]
	s_waitcnt vmcnt(16)
	v_mov_b32_e32 v56, v37
	v_mov_b32_e32 v57, v38
	v_mov_b32_e32 v58, v36
	v_mov_b32_e32 v59, v39
	v_pk_add_f32 v[56:57], v[56:57], v[58:59]
	s_waitcnt vmcnt(15)
	v_lshlrev_b32_e32 v58, 16, v52
	v_add_f32_e32 v35, v56, v57
	v_and_b32_e32 v59, 0xffff0000, v52
	v_lshlrev_b32_e32 v52, 16, v53
	v_add_f32_dpp v35, v35, v35 quad_perm:[1,0,3,2] row_mask:0xf bank_mask:0xf bound_ctrl:1
	v_and_b32_e32 v53, 0xffff0000, v53
	s_waitcnt vmcnt(14)
	v_lshlrev_b32_e32 v60, 16, v54
	v_add_f32_dpp v35, v35, v35 quad_perm:[2,3,0,1] row_mask:0xf bank_mask:0xf bound_ctrl:1
	v_and_b32_e32 v61, 0xffff0000, v54
	v_lshlrev_b32_e32 v54, 16, v55
	v_add_f32_dpp v35, v35, v35 row_half_mirror row_mask:0xf bank_mask:0xf bound_ctrl:1
	v_and_b32_e32 v55, 0xffff0000, v55
	s_nop 0
	v_add_f32_dpp v35, v35, v35 row_mirror row_mask:0xf bank_mask:0xf bound_ctrl:1
	v_fmamk_f32 v37, v35, 0xbc800000, v37
	v_fmamk_f32 v36, v35, 0xbc800000, v36
	v_fmamk_f32 v39, v35, 0xbc800000, v39
	v_fmac_f32_e32 v38, 0xbc800000, v35
	v_pk_mul_f32 v[56:57], v[38:39], v[38:39]
	v_pk_mul_f32 v[62:63], v[36:37], v[36:37]
	s_nop 0
	v_pk_mov_b32 v[64:65], v[62:63], v[56:57] op_sel:[1,0]
	v_mov_b32_e32 v63, v57
	v_pk_add_f32 v[56:57], v[64:65], v[62:63]
	s_nop 0
	v_add_f32_e32 v35, v56, v57
	s_nop 1
	v_add_f32_dpp v35, v35, v35 quad_perm:[1,0,3,2] row_mask:0xf bank_mask:0xf bound_ctrl:1
	s_nop 1
	v_add_f32_dpp v35, v35, v35 quad_perm:[2,3,0,1] row_mask:0xf bank_mask:0xf bound_ctrl:1
	s_nop 1
	v_add_f32_dpp v35, v35, v35 row_half_mirror row_mask:0xf bank_mask:0xf bound_ctrl:1
	s_nop 1
	v_add_f32_dpp v35, v35, v35 row_mirror row_mask:0xf bank_mask:0xf bound_ctrl:1
	v_fmamk_f32 v35, v35, 0x3c800000, v1
	v_mul_f32_e32 v51, 0x4f800000, v35
	v_cmp_gt_f32_e32 vcc, s24, v35
	s_nop 1
	v_cndmask_b32_e32 v35, v35, v51, vcc
	v_sqrt_f32_e32 v51, v35
	s_nop 0
	v_add_u32_e32 v56, -1, v51
	v_add_u32_e32 v57, 1, v51
	v_fma_f32 v62, -v56, v51, v35
	v_fma_f32 v63, -v57, v51, v35
	v_cmp_ge_f32_e64 s[6:7], 0, v62
	s_nop 1
	v_cndmask_b32_e64 v51, v51, v56, s[6:7]
	v_cmp_lt_f32_e64 s[6:7], 0, v63
	s_nop 1
	v_cndmask_b32_e64 v51, v51, v57, s[6:7]
	v_mul_f32_e32 v56, 0x37800000, v51
	v_cndmask_b32_e32 v51, v51, v56, vcc
	v_cmp_class_f32_e32 vcc, v35, v2
	s_nop 1
	v_cndmask_b32_e32 v35, v51, v35, vcc
	v_div_scale_f32 v51, s[0:1], v35, v35, 1.0
	v_rcp_f32_e32 v57, v51
	v_div_scale_f32 v56, vcc, 1.0, v35, 1.0
	v_fma_f32 v62, -v51, v57, 1.0
	v_fmac_f32_e32 v57, v62, v57
	v_mul_f32_e32 v62, v56, v57
	v_fma_f32 v63, -v51, v62, v56
	v_fmac_f32_e32 v62, v63, v57
	v_fma_f32 v51, -v51, v62, v56
	v_div_fmas_f32 v51, v51, v57, v62
	v_div_fixup_f32 v56, v51, v35, 1.0
	v_pk_mul_f32 v[36:37], v[36:37], v[56:57] op_sel_hi:[1,0]
	v_pk_mul_f32 v[38:39], v[38:39], v[56:57] op_sel_hi:[1,0]
	v_pk_fma_f32 v[36:37], v[130:131], v[36:37], v[134:135]
	v_pk_fma_f32 v[38:39], v[132:133], v[38:39], v[136:137]
	s_waitcnt vmcnt(13)
	v_pk_fma_f32 v[36:37], v[50:51], v[58:59], v[36:37] op_sel_hi:[0,1,1]
	v_pk_fma_f32 v[38:39], v[50:51], v[52:53], v[38:39] op_sel_hi:[0,1,1]
	v_pk_mul_f32 v[38:39], v[38:39], v[54:55]
	v_pk_mul_f32 v[36:37], v[36:37], v[60:61]
	s_nop 0
	v_cvt_pk_bf16_f32 v36, v36, v37
	v_cvt_pk_bf16_f32 v37, v38, v39
	global_store_dwordx2 v[48:49], v[36:37], off
	s_ashr_i32 s6, s18, 2
	s_and_b32 s0, s23, 0x300
	v_add_u32_e32 v48, s0, v0
	s_ashr_i32 s7, s6, 31
	s_lshl_b64 s[0:1], s[6:7], 10
	v_ashrrev_i32_e32 v49, 31, v48
	v_lshl_add_u64 v[36:37], s[0:1], 0, v[48:49]
	v_lshl_add_u64 v[40:41], v[36:37], 2, s[4:5]
	v_lshlrev_b64 v[42:43], 1, v[36:37]
	s_waitcnt lgkmcnt(0)
	global_load_dwordx4 v[36:39], v[40:41], off
	s_lshl_b64 s[16:17], s[6:7], 6
	v_ashrrev_i32_e32 v50, 6, v48
	s_add_u32 s16, s19, s16
	v_ashrrev_i32_e32 v51, 31, v50
	s_addc_u32 s17, s20, s17
	v_lshl_add_u64 v[52:53], s[12:13], 0, v[42:43]
	v_lshl_add_u64 v[54:55], s[14:15], 0, v[42:43]
	s_nop 0
	v_lshl_add_u64 v[50:51], v[50:51], 2, s[16:17]
	global_load_dwordx2 v[52:53], v[52:53], off
	s_nop 0
	global_load_dwordx2 v[54:55], v[54:55], off
	s_nop 0
	global_load_dword v50, v[50:51], off
	s_lshl_b64 s[0:1], s[6:7], 12
	s_add_u32 s0, s21, s0
	s_addc_u32 s1, s22, s1
	s_add_i32 s6, s18, 0x800
	s_add_i32 s23, s23, 0x80000
	s_cmpk_lt_i32 s18, 0x7800
	s_mov_b32 s18, s6
	v_lshl_add_u64 v[48:49], v[48:49], 1, s[0:1]
	s_waitcnt vmcnt(17)
	v_mov_b32_e32 v88, v69
	v_mov_b32_e32 v89, v70
	v_mov_b32_e32 v90, v68
	v_mov_b32_e32 v91, v71
	v_pk_add_f32 v[88:89], v[88:89], v[90:91]
	s_waitcnt vmcnt(16)
	v_lshlrev_b32_e32 v90, 16, v84
	v_add_f32_e32 v67, v88, v89
	v_and_b32_e32 v91, 0xffff0000, v84
	v_lshlrev_b32_e32 v84, 16, v85
	v_add_f32_dpp v67, v67, v67 quad_perm:[1,0,3,2] row_mask:0xf bank_mask:0xf bound_ctrl:1
	v_and_b32_e32 v85, 0xffff0000, v85
	s_waitcnt vmcnt(15)
	v_lshlrev_b32_e32 v92, 16, v86
	v_add_f32_dpp v67, v67, v67 quad_perm:[2,3,0,1] row_mask:0xf bank_mask:0xf bound_ctrl:1
	v_and_b32_e32 v93, 0xffff0000, v86
	v_lshlrev_b32_e32 v86, 16, v87
	v_add_f32_dpp v67, v67, v67 row_half_mirror row_mask:0xf bank_mask:0xf bound_ctrl:1
	v_and_b32_e32 v87, 0xffff0000, v87
	s_nop 0
	v_add_f32_dpp v67, v67, v67 row_mirror row_mask:0xf bank_mask:0xf bound_ctrl:1
	v_fmamk_f32 v69, v67, 0xbc800000, v69
	v_fmamk_f32 v68, v67, 0xbc800000, v68
	v_fmamk_f32 v71, v67, 0xbc800000, v71
	v_fmac_f32_e32 v70, 0xbc800000, v67
	v_pk_mul_f32 v[88:89], v[70:71], v[70:71]
	v_pk_mul_f32 v[94:95], v[68:69], v[68:69]
	s_nop 0
	v_pk_mov_b32 v[96:97], v[94:95], v[88:89] op_sel:[1,0]
	v_mov_b32_e32 v95, v89
	v_pk_add_f32 v[88:89], v[96:97], v[94:95]
	s_nop 0
	v_add_f32_e32 v67, v88, v89
	s_nop 1
	v_add_f32_dpp v67, v67, v67 quad_perm:[1,0,3,2] row_mask:0xf bank_mask:0xf bound_ctrl:1
	s_nop 1
	v_add_f32_dpp v67, v67, v67 quad_perm:[2,3,0,1] row_mask:0xf bank_mask:0xf bound_ctrl:1
	s_nop 1
	v_add_f32_dpp v67, v67, v67 row_half_mirror row_mask:0xf bank_mask:0xf bound_ctrl:1
	s_nop 1
	v_add_f32_dpp v67, v67, v67 row_mirror row_mask:0xf bank_mask:0xf bound_ctrl:1
	v_fmamk_f32 v67, v67, 0x3c800000, v1
	v_mul_f32_e32 v83, 0x4f800000, v67
	v_cmp_gt_f32_e32 vcc, s24, v67
	s_nop 1
	v_cndmask_b32_e32 v67, v67, v83, vcc
	v_sqrt_f32_e32 v83, v67
	s_nop 0
	v_add_u32_e32 v88, -1, v83
	v_add_u32_e32 v89, 1, v83
	v_fma_f32 v94, -v88, v83, v67
	v_fma_f32 v95, -v89, v83, v67
	v_cmp_ge_f32_e64 s[6:7], 0, v94
	s_nop 1
	v_cndmask_b32_e64 v83, v83, v88, s[6:7]
	v_cmp_lt_f32_e64 s[6:7], 0, v95
	s_nop 1
	v_cndmask_b32_e64 v83, v83, v89, s[6:7]
	v_mul_f32_e32 v88, 0x37800000, v83
	v_cndmask_b32_e32 v83, v83, v88, vcc
	v_cmp_class_f32_e32 vcc, v67, v2
	s_nop 1
	v_cndmask_b32_e32 v67, v83, v67, vcc
	v_div_scale_f32 v83, s[0:1], v67, v67, 1.0
	v_rcp_f32_e32 v89, v83
	v_div_scale_f32 v88, vcc, 1.0, v67, 1.0
	v_fma_f32 v94, -v83, v89, 1.0
	v_fmac_f32_e32 v89, v94, v89
	v_mul_f32_e32 v94, v88, v89
	v_fma_f32 v95, -v83, v94, v88
	v_fmac_f32_e32 v94, v95, v89
	v_fma_f32 v83, -v83, v94, v88
	v_div_fmas_f32 v83, v83, v89, v94
	v_div_fixup_f32 v88, v83, v67, 1.0
	v_pk_mul_f32 v[68:69], v[68:69], v[88:89] op_sel_hi:[1,0]
	v_pk_mul_f32 v[70:71], v[70:71], v[88:89] op_sel_hi:[1,0]
	v_pk_fma_f32 v[68:69], v[130:131], v[68:69], v[134:135]
	v_pk_fma_f32 v[70:71], v[132:133], v[70:71], v[136:137]
	s_waitcnt vmcnt(14)
	v_pk_fma_f32 v[68:69], v[82:83], v[90:91], v[68:69] op_sel_hi:[0,1,1]
	v_pk_fma_f32 v[70:71], v[82:83], v[84:85], v[70:71] op_sel_hi:[0,1,1]
	v_pk_mul_f32 v[70:71], v[70:71], v[86:87]
	v_pk_mul_f32 v[68:69], v[68:69], v[92:93]
	s_nop 0
	v_cvt_pk_bf16_f32 v68, v68, v69
	v_cvt_pk_bf16_f32 v69, v70, v71
	global_store_dwordx2 v[80:81], v[68:69], off
	s_ashr_i32 s6, s18, 2
	s_and_b32 s0, s23, 0x300
	v_add_u32_e32 v80, s0, v0
	s_ashr_i32 s7, s6, 31
	s_lshl_b64 s[0:1], s[6:7], 10
	v_ashrrev_i32_e32 v81, 31, v80
	v_lshl_add_u64 v[68:69], s[0:1], 0, v[80:81]
	v_lshl_add_u64 v[72:73], v[68:69], 2, s[4:5]
	v_lshlrev_b64 v[74:75], 1, v[68:69]
	s_waitcnt lgkmcnt(0)
	global_load_dwordx4 v[68:71], v[72:73], off
	s_lshl_b64 s[16:17], s[6:7], 6
	v_ashrrev_i32_e32 v82, 6, v80
	s_add_u32 s16, s19, s16
	v_ashrrev_i32_e32 v83, 31, v82
	s_addc_u32 s17, s20, s17
	v_lshl_add_u64 v[84:85], s[12:13], 0, v[74:75]
	v_lshl_add_u64 v[86:87], s[14:15], 0, v[74:75]
	s_nop 0
	v_lshl_add_u64 v[82:83], v[82:83], 2, s[16:17]
	global_load_dwordx2 v[84:85], v[84:85], off
	s_nop 0
	global_load_dwordx2 v[86:87], v[86:87], off
	s_nop 0
	global_load_dword v82, v[82:83], off
	s_lshl_b64 s[0:1], s[6:7], 12
	s_add_u32 s0, s21, s0
	s_addc_u32 s1, s22, s1
	s_add_i32 s6, s18, 0x800
	s_add_i32 s23, s23, 0x80000
	s_cmpk_lt_i32 s18, 0x7800
	s_mov_b32 s18, s6
	v_lshl_add_u64 v[80:81], v[80:81], 1, s[0:1]
	s_waitcnt vmcnt(18)
	v_mov_b32_e32 v120, v101
	v_mov_b32_e32 v121, v102
	v_mov_b32_e32 v122, v100
	v_mov_b32_e32 v123, v103
	v_pk_add_f32 v[120:121], v[120:121], v[122:123]
	s_waitcnt vmcnt(17)
	v_lshlrev_b32_e32 v122, 16, v116
	v_add_f32_e32 v99, v120, v121
	v_and_b32_e32 v123, 0xffff0000, v116
	v_lshlrev_b32_e32 v116, 16, v117
	v_add_f32_dpp v99, v99, v99 quad_perm:[1,0,3,2] row_mask:0xf bank_mask:0xf bound_ctrl:1
	v_and_b32_e32 v117, 0xffff0000, v117
	s_waitcnt vmcnt(16)
	v_lshlrev_b32_e32 v124, 16, v118
	v_add_f32_dpp v99, v99, v99 quad_perm:[2,3,0,1] row_mask:0xf bank_mask:0xf bound_ctrl:1
	v_and_b32_e32 v125, 0xffff0000, v118
	v_lshlrev_b32_e32 v118, 16, v119
	v_add_f32_dpp v99, v99, v99 row_half_mirror row_mask:0xf bank_mask:0xf bound_ctrl:1
	v_and_b32_e32 v119, 0xffff0000, v119
	s_nop 0
	v_add_f32_dpp v99, v99, v99 row_mirror row_mask:0xf bank_mask:0xf bound_ctrl:1
	v_fmamk_f32 v101, v99, 0xbc800000, v101
	v_fmamk_f32 v100, v99, 0xbc800000, v100
	v_fmamk_f32 v103, v99, 0xbc800000, v103
	v_fmac_f32_e32 v102, 0xbc800000, v99
	v_pk_mul_f32 v[120:121], v[102:103], v[102:103]
	v_pk_mul_f32 v[126:127], v[100:101], v[100:101]
	s_nop 0
	v_pk_mov_b32 v[128:129], v[126:127], v[120:121] op_sel:[1,0]
	v_mov_b32_e32 v127, v121
	v_pk_add_f32 v[120:121], v[128:129], v[126:127]
	s_nop 0
	v_add_f32_e32 v99, v120, v121
	s_nop 1
	v_add_f32_dpp v99, v99, v99 quad_perm:[1,0,3,2] row_mask:0xf bank_mask:0xf bound_ctrl:1
	s_nop 1
	v_add_f32_dpp v99, v99, v99 quad_perm:[2,3,0,1] row_mask:0xf bank_mask:0xf bound_ctrl:1
	s_nop 1
	v_add_f32_dpp v99, v99, v99 row_half_mirror row_mask:0xf bank_mask:0xf bound_ctrl:1
	s_nop 1
	v_add_f32_dpp v99, v99, v99 row_mirror row_mask:0xf bank_mask:0xf bound_ctrl:1
	v_fmamk_f32 v99, v99, 0x3c800000, v1
	v_mul_f32_e32 v115, 0x4f800000, v99
	v_cmp_gt_f32_e32 vcc, s24, v99
	s_nop 1
	v_cndmask_b32_e32 v99, v99, v115, vcc
	v_sqrt_f32_e32 v115, v99
	s_nop 0
	v_add_u32_e32 v120, -1, v115
	v_add_u32_e32 v121, 1, v115
	v_fma_f32 v126, -v120, v115, v99
	v_fma_f32 v127, -v121, v115, v99
	v_cmp_ge_f32_e64 s[6:7], 0, v126
	s_nop 1
	v_cndmask_b32_e64 v115, v115, v120, s[6:7]
	v_cmp_lt_f32_e64 s[6:7], 0, v127
	s_nop 1
	v_cndmask_b32_e64 v115, v115, v121, s[6:7]
	v_mul_f32_e32 v120, 0x37800000, v115
	v_cndmask_b32_e32 v115, v115, v120, vcc
	v_cmp_class_f32_e32 vcc, v99, v2
	s_nop 1
	v_cndmask_b32_e32 v99, v115, v99, vcc
	v_div_scale_f32 v115, s[0:1], v99, v99, 1.0
	v_rcp_f32_e32 v121, v115
	v_div_scale_f32 v120, vcc, 1.0, v99, 1.0
	v_fma_f32 v126, -v115, v121, 1.0
	v_fmac_f32_e32 v121, v126, v121
	v_mul_f32_e32 v126, v120, v121
	v_fma_f32 v127, -v115, v126, v120
	v_fmac_f32_e32 v126, v127, v121
	v_fma_f32 v115, -v115, v126, v120
	v_div_fmas_f32 v115, v115, v121, v126
	v_div_fixup_f32 v120, v115, v99, 1.0
	v_pk_mul_f32 v[100:101], v[100:101], v[120:121] op_sel_hi:[1,0]
	v_pk_mul_f32 v[102:103], v[102:103], v[120:121] op_sel_hi:[1,0]
	v_pk_fma_f32 v[100:101], v[130:131], v[100:101], v[134:135]
	v_pk_fma_f32 v[102:103], v[132:133], v[102:103], v[136:137]
	s_waitcnt vmcnt(15)
	v_pk_fma_f32 v[100:101], v[114:115], v[122:123], v[100:101] op_sel_hi:[0,1,1]
	v_pk_fma_f32 v[102:103], v[114:115], v[116:117], v[102:103] op_sel_hi:[0,1,1]
	v_pk_mul_f32 v[102:103], v[102:103], v[118:119]
	v_pk_mul_f32 v[100:101], v[100:101], v[124:125]
	s_nop 0
	v_cvt_pk_bf16_f32 v100, v100, v101
	v_cvt_pk_bf16_f32 v101, v102, v103
	global_store_dwordx2 v[112:113], v[100:101], off
	s_ashr_i32 s6, s18, 2
	s_and_b32 s0, s23, 0x300
	v_add_u32_e32 v112, s0, v0
	s_ashr_i32 s7, s6, 31
	s_lshl_b64 s[0:1], s[6:7], 10
	v_ashrrev_i32_e32 v113, 31, v112
	v_lshl_add_u64 v[100:101], s[0:1], 0, v[112:113]
	v_lshl_add_u64 v[104:105], v[100:101], 2, s[4:5]
	v_lshlrev_b64 v[106:107], 1, v[100:101]
	s_waitcnt lgkmcnt(0)
	global_load_dwordx4 v[100:103], v[104:105], off
	s_lshl_b64 s[16:17], s[6:7], 6
	v_ashrrev_i32_e32 v114, 6, v112
	s_add_u32 s16, s19, s16
	v_ashrrev_i32_e32 v115, 31, v114
	s_addc_u32 s17, s20, s17
	v_lshl_add_u64 v[116:117], s[12:13], 0, v[106:107]
	v_lshl_add_u64 v[118:119], s[14:15], 0, v[106:107]
	s_nop 0
	v_lshl_add_u64 v[114:115], v[114:115], 2, s[16:17]
	global_load_dwordx2 v[116:117], v[116:117], off
	s_nop 0
	global_load_dwordx2 v[118:119], v[118:119], off
	s_nop 0
	global_load_dword v114, v[114:115], off
	s_lshl_b64 s[0:1], s[6:7], 12
	s_add_u32 s0, s21, s0
	s_addc_u32 s1, s22, s1
	s_add_i32 s6, s18, 0x800
	s_add_i32 s23, s23, 0x80000
	s_cmpk_lt_i32 s18, 0x7800
	s_mov_b32 s18, s6
	v_lshl_add_u64 v[112:113], v[112:113], 1, s[0:1]
.LBB0_1879:
	s_waitcnt vmcnt(18)
	v_mov_b32_e32 v24, v5
	v_mov_b32_e32 v25, v6
	v_mov_b32_e32 v26, v4
	v_mov_b32_e32 v27, v7
	v_pk_add_f32 v[24:25], v[24:25], v[26:27]
	s_waitcnt vmcnt(17)
	v_lshlrev_b32_e32 v26, 16, v20
	v_add_f32_e32 v3, v24, v25
	v_and_b32_e32 v27, 0xffff0000, v20
	v_lshlrev_b32_e32 v20, 16, v21
	v_add_f32_dpp v3, v3, v3 quad_perm:[1,0,3,2] row_mask:0xf bank_mask:0xf bound_ctrl:1
	v_and_b32_e32 v21, 0xffff0000, v21
	s_waitcnt vmcnt(16)
	v_lshlrev_b32_e32 v28, 16, v22
	v_add_f32_dpp v3, v3, v3 quad_perm:[2,3,0,1] row_mask:0xf bank_mask:0xf bound_ctrl:1
	v_and_b32_e32 v29, 0xffff0000, v22
	v_lshlrev_b32_e32 v22, 16, v23
	v_add_f32_dpp v3, v3, v3 row_half_mirror row_mask:0xf bank_mask:0xf bound_ctrl:1
	v_and_b32_e32 v23, 0xffff0000, v23
	s_nop 0
	v_add_f32_dpp v3, v3, v3 row_mirror row_mask:0xf bank_mask:0xf bound_ctrl:1
	v_fmamk_f32 v5, v3, 0xbc800000, v5
	v_fmamk_f32 v4, v3, 0xbc800000, v4
	v_fmamk_f32 v7, v3, 0xbc800000, v7
	v_fmac_f32_e32 v6, 0xbc800000, v3
	v_pk_mul_f32 v[24:25], v[6:7], v[6:7]
	v_pk_mul_f32 v[30:31], v[4:5], v[4:5]
	s_nop 0
	v_pk_mov_b32 v[32:33], v[30:31], v[24:25] op_sel:[1,0]
	v_mov_b32_e32 v31, v25
	v_pk_add_f32 v[24:25], v[32:33], v[30:31]
	s_nop 0
	v_add_f32_e32 v3, v24, v25
	s_nop 1
	v_add_f32_dpp v3, v3, v3 quad_perm:[1,0,3,2] row_mask:0xf bank_mask:0xf bound_ctrl:1
	s_nop 1
	v_add_f32_dpp v3, v3, v3 quad_perm:[2,3,0,1] row_mask:0xf bank_mask:0xf bound_ctrl:1
	s_nop 1
	v_add_f32_dpp v3, v3, v3 row_half_mirror row_mask:0xf bank_mask:0xf bound_ctrl:1
	s_nop 1
	v_add_f32_dpp v3, v3, v3 row_mirror row_mask:0xf bank_mask:0xf bound_ctrl:1
	v_fmamk_f32 v3, v3, 0x3c800000, v1
	v_mul_f32_e32 v19, 0x4f800000, v3
	v_cmp_gt_f32_e32 vcc, s24, v3
	s_nop 1
	v_cndmask_b32_e32 v3, v3, v19, vcc
	v_sqrt_f32_e32 v19, v3
	s_nop 0
	v_add_u32_e32 v24, -1, v19
	v_add_u32_e32 v25, 1, v19
	v_fma_f32 v30, -v24, v19, v3
	v_fma_f32 v31, -v25, v19, v3
	v_cmp_ge_f32_e64 s[6:7], 0, v30
	s_nop 1
	v_cndmask_b32_e64 v19, v19, v24, s[6:7]
	v_cmp_lt_f32_e64 s[6:7], 0, v31
	s_nop 1
	v_cndmask_b32_e64 v19, v19, v25, s[6:7]
	v_mul_f32_e32 v24, 0x37800000, v19
	v_cndmask_b32_e32 v19, v19, v24, vcc
	v_cmp_class_f32_e32 vcc, v3, v2
	s_nop 1
	v_cndmask_b32_e32 v3, v19, v3, vcc
	v_div_scale_f32 v19, s[0:1], v3, v3, 1.0
	v_rcp_f32_e32 v25, v19
	v_div_scale_f32 v24, vcc, 1.0, v3, 1.0
	v_fma_f32 v30, -v19, v25, 1.0
	v_fmac_f32_e32 v25, v30, v25
	v_mul_f32_e32 v30, v24, v25
	v_fma_f32 v31, -v19, v30, v24
	v_fmac_f32_e32 v30, v31, v25
	v_fma_f32 v19, -v19, v30, v24
	v_div_fmas_f32 v19, v19, v25, v30
	v_div_fixup_f32 v24, v19, v3, 1.0
	v_pk_mul_f32 v[4:5], v[4:5], v[24:25] op_sel_hi:[1,0]
	v_pk_mul_f32 v[6:7], v[6:7], v[24:25] op_sel_hi:[1,0]
	v_pk_fma_f32 v[4:5], v[130:131], v[4:5], v[134:135]
	v_pk_fma_f32 v[6:7], v[132:133], v[6:7], v[136:137]
	s_waitcnt vmcnt(15)
	v_pk_fma_f32 v[4:5], v[18:19], v[26:27], v[4:5] op_sel_hi:[0,1,1]
	v_pk_fma_f32 v[6:7], v[18:19], v[20:21], v[6:7] op_sel_hi:[0,1,1]
	v_pk_mul_f32 v[6:7], v[6:7], v[22:23]
	v_pk_mul_f32 v[4:5], v[4:5], v[28:29]
	s_nop 0
	v_cvt_pk_bf16_f32 v4, v4, v5
	v_cvt_pk_bf16_f32 v5, v6, v7
	global_store_dwordx2 v[16:17], v[4:5], off
	s_ashr_i32 s6, s18, 2
	s_and_b32 s0, s23, 0x300
	v_add_u32_e32 v16, s0, v0
	s_ashr_i32 s7, s6, 31
	s_lshl_b64 s[0:1], s[6:7], 10
	v_ashrrev_i32_e32 v17, 31, v16
	v_lshl_add_u64 v[4:5], s[0:1], 0, v[16:17]
	v_lshl_add_u64 v[8:9], v[4:5], 2, s[4:5]
	v_lshlrev_b64 v[10:11], 1, v[4:5]
	s_waitcnt lgkmcnt(0)
	global_load_dwordx4 v[4:7], v[8:9], off
	s_lshl_b64 s[16:17], s[6:7], 6
	v_ashrrev_i32_e32 v18, 6, v16
	s_add_u32 s16, s19, s16
	v_ashrrev_i32_e32 v19, 31, v18
	s_addc_u32 s17, s20, s17
	v_lshl_add_u64 v[20:21], s[12:13], 0, v[10:11]
	v_lshl_add_u64 v[22:23], s[14:15], 0, v[10:11]
	s_nop 0
	v_lshl_add_u64 v[18:19], v[18:19], 2, s[16:17]
	global_load_dwordx2 v[20:21], v[20:21], off
	s_nop 0
	global_load_dwordx2 v[22:23], v[22:23], off
	s_nop 0
	global_load_dword v18, v[18:19], off
	s_lshl_b64 s[0:1], s[6:7], 12
	s_add_u32 s0, s21, s0
	s_addc_u32 s1, s22, s1
	s_add_i32 s6, s18, 0x800
	s_add_i32 s23, s23, 0x80000
	s_cmpk_lt_i32 s18, 0x7800
	s_mov_b32 s18, s6
	v_lshl_add_u64 v[16:17], v[16:17], 1, s[0:1]
	s_waitcnt vmcnt(18)
	v_mov_b32_e32 v56, v37
	v_mov_b32_e32 v57, v38
	v_mov_b32_e32 v58, v36
	v_mov_b32_e32 v59, v39
	v_pk_add_f32 v[56:57], v[56:57], v[58:59]
	s_waitcnt vmcnt(17)
	v_lshlrev_b32_e32 v58, 16, v52
	v_add_f32_e32 v35, v56, v57
	v_and_b32_e32 v59, 0xffff0000, v52
	v_lshlrev_b32_e32 v52, 16, v53
	v_add_f32_dpp v35, v35, v35 quad_perm:[1,0,3,2] row_mask:0xf bank_mask:0xf bound_ctrl:1
	v_and_b32_e32 v53, 0xffff0000, v53
	s_waitcnt vmcnt(16)
	v_lshlrev_b32_e32 v60, 16, v54
	v_add_f32_dpp v35, v35, v35 quad_perm:[2,3,0,1] row_mask:0xf bank_mask:0xf bound_ctrl:1
	v_and_b32_e32 v61, 0xffff0000, v54
	v_lshlrev_b32_e32 v54, 16, v55
	v_add_f32_dpp v35, v35, v35 row_half_mirror row_mask:0xf bank_mask:0xf bound_ctrl:1
	v_and_b32_e32 v55, 0xffff0000, v55
	s_nop 0
	v_add_f32_dpp v35, v35, v35 row_mirror row_mask:0xf bank_mask:0xf bound_ctrl:1
	v_fmamk_f32 v37, v35, 0xbc800000, v37
	v_fmamk_f32 v36, v35, 0xbc800000, v36
	v_fmamk_f32 v39, v35, 0xbc800000, v39
	v_fmac_f32_e32 v38, 0xbc800000, v35
	v_pk_mul_f32 v[56:57], v[38:39], v[38:39]
	v_pk_mul_f32 v[62:63], v[36:37], v[36:37]
	s_nop 0
	v_pk_mov_b32 v[64:65], v[62:63], v[56:57] op_sel:[1,0]
	v_mov_b32_e32 v63, v57
	v_pk_add_f32 v[56:57], v[64:65], v[62:63]
	s_nop 0
	v_add_f32_e32 v35, v56, v57
	s_nop 1
	v_add_f32_dpp v35, v35, v35 quad_perm:[1,0,3,2] row_mask:0xf bank_mask:0xf bound_ctrl:1
	s_nop 1
	v_add_f32_dpp v35, v35, v35 quad_perm:[2,3,0,1] row_mask:0xf bank_mask:0xf bound_ctrl:1
	s_nop 1
	v_add_f32_dpp v35, v35, v35 row_half_mirror row_mask:0xf bank_mask:0xf bound_ctrl:1
	s_nop 1
	v_add_f32_dpp v35, v35, v35 row_mirror row_mask:0xf bank_mask:0xf bound_ctrl:1
	v_fmamk_f32 v35, v35, 0x3c800000, v1
	v_mul_f32_e32 v51, 0x4f800000, v35
	v_cmp_gt_f32_e32 vcc, s24, v35
	s_nop 1
	v_cndmask_b32_e32 v35, v35, v51, vcc
	v_sqrt_f32_e32 v51, v35
	s_nop 0
	v_add_u32_e32 v56, -1, v51
	v_add_u32_e32 v57, 1, v51
	v_fma_f32 v62, -v56, v51, v35
	v_fma_f32 v63, -v57, v51, v35
	v_cmp_ge_f32_e64 s[6:7], 0, v62
	s_nop 1
	v_cndmask_b32_e64 v51, v51, v56, s[6:7]
	v_cmp_lt_f32_e64 s[6:7], 0, v63
	s_nop 1
	v_cndmask_b32_e64 v51, v51, v57, s[6:7]
	v_mul_f32_e32 v56, 0x37800000, v51
	v_cndmask_b32_e32 v51, v51, v56, vcc
	v_cmp_class_f32_e32 vcc, v35, v2
	s_nop 1
	v_cndmask_b32_e32 v35, v51, v35, vcc
	v_div_scale_f32 v51, s[0:1], v35, v35, 1.0
	v_rcp_f32_e32 v57, v51
	v_div_scale_f32 v56, vcc, 1.0, v35, 1.0
	v_fma_f32 v62, -v51, v57, 1.0
	v_fmac_f32_e32 v57, v62, v57
	v_mul_f32_e32 v62, v56, v57
	v_fma_f32 v63, -v51, v62, v56
	v_fmac_f32_e32 v62, v63, v57
	v_fma_f32 v51, -v51, v62, v56
	v_div_fmas_f32 v51, v51, v57, v62
	v_div_fixup_f32 v56, v51, v35, 1.0
	v_pk_mul_f32 v[36:37], v[36:37], v[56:57] op_sel_hi:[1,0]
	v_pk_mul_f32 v[38:39], v[38:39], v[56:57] op_sel_hi:[1,0]
	v_pk_fma_f32 v[36:37], v[130:131], v[36:37], v[134:135]
	v_pk_fma_f32 v[38:39], v[132:133], v[38:39], v[136:137]
	s_waitcnt vmcnt(15)
	v_pk_fma_f32 v[36:37], v[50:51], v[58:59], v[36:37] op_sel_hi:[0,1,1]
	v_pk_fma_f32 v[38:39], v[50:51], v[52:53], v[38:39] op_sel_hi:[0,1,1]
	v_pk_mul_f32 v[38:39], v[38:39], v[54:55]
	v_pk_mul_f32 v[36:37], v[36:37], v[60:61]
	s_nop 0
	v_cvt_pk_bf16_f32 v36, v36, v37
	v_cvt_pk_bf16_f32 v37, v38, v39
	global_store_dwordx2 v[48:49], v[36:37], off
	s_ashr_i32 s6, s18, 2
	s_and_b32 s0, s23, 0x300
	v_add_u32_e32 v48, s0, v0
	s_ashr_i32 s7, s6, 31
	s_lshl_b64 s[0:1], s[6:7], 10
	v_ashrrev_i32_e32 v49, 31, v48
	v_lshl_add_u64 v[36:37], s[0:1], 0, v[48:49]
	v_lshl_add_u64 v[40:41], v[36:37], 2, s[4:5]
	v_lshlrev_b64 v[42:43], 1, v[36:37]
	s_waitcnt lgkmcnt(0)
	global_load_dwordx4 v[36:39], v[40:41], off
	s_lshl_b64 s[16:17], s[6:7], 6
	v_ashrrev_i32_e32 v50, 6, v48
	s_add_u32 s16, s19, s16
	v_ashrrev_i32_e32 v51, 31, v50
	s_addc_u32 s17, s20, s17
	v_lshl_add_u64 v[52:53], s[12:13], 0, v[42:43]
	v_lshl_add_u64 v[54:55], s[14:15], 0, v[42:43]
	s_nop 0
	v_lshl_add_u64 v[50:51], v[50:51], 2, s[16:17]
	global_load_dwordx2 v[52:53], v[52:53], off
	s_nop 0
	global_load_dwordx2 v[54:55], v[54:55], off
	s_nop 0
	global_load_dword v50, v[50:51], off
	s_lshl_b64 s[0:1], s[6:7], 12
	s_add_u32 s0, s21, s0
	s_addc_u32 s1, s22, s1
	s_add_i32 s6, s18, 0x800
	s_add_i32 s23, s23, 0x80000
	s_cmpk_lt_i32 s18, 0x7800
	s_mov_b32 s18, s6
	v_lshl_add_u64 v[48:49], v[48:49], 1, s[0:1]
	s_waitcnt vmcnt(18)
	v_mov_b32_e32 v88, v69
	v_mov_b32_e32 v89, v70
	v_mov_b32_e32 v90, v68
	v_mov_b32_e32 v91, v71
	v_pk_add_f32 v[88:89], v[88:89], v[90:91]
	s_waitcnt vmcnt(17)
	v_lshlrev_b32_e32 v90, 16, v84
	v_add_f32_e32 v67, v88, v89
	v_and_b32_e32 v91, 0xffff0000, v84
	v_lshlrev_b32_e32 v84, 16, v85
	v_add_f32_dpp v67, v67, v67 quad_perm:[1,0,3,2] row_mask:0xf bank_mask:0xf bound_ctrl:1
	v_and_b32_e32 v85, 0xffff0000, v85
	s_waitcnt vmcnt(16)
	v_lshlrev_b32_e32 v92, 16, v86
	v_add_f32_dpp v67, v67, v67 quad_perm:[2,3,0,1] row_mask:0xf bank_mask:0xf bound_ctrl:1
	v_and_b32_e32 v93, 0xffff0000, v86
	v_lshlrev_b32_e32 v86, 16, v87
	v_add_f32_dpp v67, v67, v67 row_half_mirror row_mask:0xf bank_mask:0xf bound_ctrl:1
	v_and_b32_e32 v87, 0xffff0000, v87
	s_nop 0
	v_add_f32_dpp v67, v67, v67 row_mirror row_mask:0xf bank_mask:0xf bound_ctrl:1
	v_fmamk_f32 v69, v67, 0xbc800000, v69
	v_fmamk_f32 v68, v67, 0xbc800000, v68
	v_fmamk_f32 v71, v67, 0xbc800000, v71
	v_fmac_f32_e32 v70, 0xbc800000, v67
	v_pk_mul_f32 v[88:89], v[70:71], v[70:71]
	v_pk_mul_f32 v[94:95], v[68:69], v[68:69]
	s_nop 0
	v_pk_mov_b32 v[96:97], v[94:95], v[88:89] op_sel:[1,0]
	v_mov_b32_e32 v95, v89
	v_pk_add_f32 v[88:89], v[96:97], v[94:95]
	s_nop 0
	v_add_f32_e32 v67, v88, v89
	s_nop 1
	v_add_f32_dpp v67, v67, v67 quad_perm:[1,0,3,2] row_mask:0xf bank_mask:0xf bound_ctrl:1
	s_nop 1
	v_add_f32_dpp v67, v67, v67 quad_perm:[2,3,0,1] row_mask:0xf bank_mask:0xf bound_ctrl:1
	s_nop 1
	v_add_f32_dpp v67, v67, v67 row_half_mirror row_mask:0xf bank_mask:0xf bound_ctrl:1
	s_nop 1
	v_add_f32_dpp v67, v67, v67 row_mirror row_mask:0xf bank_mask:0xf bound_ctrl:1
	v_fmamk_f32 v67, v67, 0x3c800000, v1
	v_mul_f32_e32 v83, 0x4f800000, v67
	v_cmp_gt_f32_e32 vcc, s24, v67
	s_nop 1
	v_cndmask_b32_e32 v67, v67, v83, vcc
	v_sqrt_f32_e32 v83, v67
	s_nop 0
	v_add_u32_e32 v88, -1, v83
	v_add_u32_e32 v89, 1, v83
	v_fma_f32 v94, -v88, v83, v67
	v_fma_f32 v95, -v89, v83, v67
	v_cmp_ge_f32_e64 s[6:7], 0, v94
	s_nop 1
	v_cndmask_b32_e64 v83, v83, v88, s[6:7]
	v_cmp_lt_f32_e64 s[6:7], 0, v95
	s_nop 1
	v_cndmask_b32_e64 v83, v83, v89, s[6:7]
	v_mul_f32_e32 v88, 0x37800000, v83
	v_cndmask_b32_e32 v83, v83, v88, vcc
	v_cmp_class_f32_e32 vcc, v67, v2
	s_nop 1
	v_cndmask_b32_e32 v67, v83, v67, vcc
	v_div_scale_f32 v83, s[0:1], v67, v67, 1.0
	v_rcp_f32_e32 v89, v83
	v_div_scale_f32 v88, vcc, 1.0, v67, 1.0
	v_fma_f32 v94, -v83, v89, 1.0
	v_fmac_f32_e32 v89, v94, v89
	v_mul_f32_e32 v94, v88, v89
	v_fma_f32 v95, -v83, v94, v88
	v_fmac_f32_e32 v94, v95, v89
	v_fma_f32 v83, -v83, v94, v88
	v_div_fmas_f32 v83, v83, v89, v94
	v_div_fixup_f32 v88, v83, v67, 1.0
	v_pk_mul_f32 v[68:69], v[68:69], v[88:89] op_sel_hi:[1,0]
	v_pk_mul_f32 v[70:71], v[70:71], v[88:89] op_sel_hi:[1,0]
	v_pk_fma_f32 v[68:69], v[130:131], v[68:69], v[134:135]
	v_pk_fma_f32 v[70:71], v[132:133], v[70:71], v[136:137]
	s_waitcnt vmcnt(15)
	v_pk_fma_f32 v[68:69], v[82:83], v[90:91], v[68:69] op_sel_hi:[0,1,1]
	v_pk_fma_f32 v[70:71], v[82:83], v[84:85], v[70:71] op_sel_hi:[0,1,1]
	v_pk_mul_f32 v[70:71], v[70:71], v[86:87]
	v_pk_mul_f32 v[68:69], v[68:69], v[92:93]
	s_nop 0
	v_cvt_pk_bf16_f32 v68, v68, v69
	v_cvt_pk_bf16_f32 v69, v70, v71
	global_store_dwordx2 v[80:81], v[68:69], off
	s_ashr_i32 s6, s18, 2
	s_and_b32 s0, s23, 0x300
	v_add_u32_e32 v80, s0, v0
	s_ashr_i32 s7, s6, 31
	s_lshl_b64 s[0:1], s[6:7], 10
	v_ashrrev_i32_e32 v81, 31, v80
	v_lshl_add_u64 v[68:69], s[0:1], 0, v[80:81]
	v_lshl_add_u64 v[72:73], v[68:69], 2, s[4:5]
	v_lshlrev_b64 v[74:75], 1, v[68:69]
	s_waitcnt lgkmcnt(0)
	global_load_dwordx4 v[68:71], v[72:73], off
	s_lshl_b64 s[16:17], s[6:7], 6
	v_ashrrev_i32_e32 v82, 6, v80
	s_add_u32 s16, s19, s16
	v_ashrrev_i32_e32 v83, 31, v82
	s_addc_u32 s17, s20, s17
	v_lshl_add_u64 v[84:85], s[12:13], 0, v[74:75]
	v_lshl_add_u64 v[86:87], s[14:15], 0, v[74:75]
	s_nop 0
	v_lshl_add_u64 v[82:83], v[82:83], 2, s[16:17]
	global_load_dwordx2 v[84:85], v[84:85], off
	s_nop 0
	global_load_dwordx2 v[86:87], v[86:87], off
	s_nop 0
	global_load_dword v82, v[82:83], off
	s_lshl_b64 s[0:1], s[6:7], 12
	s_add_u32 s0, s21, s0
	s_addc_u32 s1, s22, s1
	s_add_i32 s6, s18, 0x800
	s_add_i32 s23, s23, 0x80000
	s_cmpk_lt_i32 s18, 0x7800
	s_mov_b32 s18, s6
	v_lshl_add_u64 v[80:81], v[80:81], 1, s[0:1]
	s_waitcnt vmcnt(18)
	v_mov_b32_e32 v120, v101
	v_mov_b32_e32 v121, v102
	v_mov_b32_e32 v122, v100
	v_mov_b32_e32 v123, v103
	v_pk_add_f32 v[120:121], v[120:121], v[122:123]
	s_waitcnt vmcnt(17)
	v_lshlrev_b32_e32 v122, 16, v116
	v_add_f32_e32 v99, v120, v121
	v_and_b32_e32 v123, 0xffff0000, v116
	v_lshlrev_b32_e32 v116, 16, v117
	v_add_f32_dpp v99, v99, v99 quad_perm:[1,0,3,2] row_mask:0xf bank_mask:0xf bound_ctrl:1
	v_and_b32_e32 v117, 0xffff0000, v117
	s_waitcnt vmcnt(16)
	v_lshlrev_b32_e32 v124, 16, v118
	v_add_f32_dpp v99, v99, v99 quad_perm:[2,3,0,1] row_mask:0xf bank_mask:0xf bound_ctrl:1
	v_and_b32_e32 v125, 0xffff0000, v118
	v_lshlrev_b32_e32 v118, 16, v119
	v_add_f32_dpp v99, v99, v99 row_half_mirror row_mask:0xf bank_mask:0xf bound_ctrl:1
	v_and_b32_e32 v119, 0xffff0000, v119
	s_nop 0
	v_add_f32_dpp v99, v99, v99 row_mirror row_mask:0xf bank_mask:0xf bound_ctrl:1
	v_fmamk_f32 v101, v99, 0xbc800000, v101
	v_fmamk_f32 v100, v99, 0xbc800000, v100
	v_fmamk_f32 v103, v99, 0xbc800000, v103
	v_fmac_f32_e32 v102, 0xbc800000, v99
	v_pk_mul_f32 v[120:121], v[102:103], v[102:103]
	v_pk_mul_f32 v[126:127], v[100:101], v[100:101]
	s_nop 0
	v_pk_mov_b32 v[128:129], v[126:127], v[120:121] op_sel:[1,0]
	v_mov_b32_e32 v127, v121
	v_pk_add_f32 v[120:121], v[128:129], v[126:127]
	s_nop 0
	v_add_f32_e32 v99, v120, v121
	s_nop 1
	v_add_f32_dpp v99, v99, v99 quad_perm:[1,0,3,2] row_mask:0xf bank_mask:0xf bound_ctrl:1
	s_nop 1
	v_add_f32_dpp v99, v99, v99 quad_perm:[2,3,0,1] row_mask:0xf bank_mask:0xf bound_ctrl:1
	s_nop 1
	v_add_f32_dpp v99, v99, v99 row_half_mirror row_mask:0xf bank_mask:0xf bound_ctrl:1
	s_nop 1
	v_add_f32_dpp v99, v99, v99 row_mirror row_mask:0xf bank_mask:0xf bound_ctrl:1
	v_fmamk_f32 v99, v99, 0x3c800000, v1
	v_mul_f32_e32 v115, 0x4f800000, v99
	v_cmp_gt_f32_e32 vcc, s24, v99
	s_nop 1
	v_cndmask_b32_e32 v99, v99, v115, vcc
	v_sqrt_f32_e32 v115, v99
	s_nop 0
	v_add_u32_e32 v120, -1, v115
	v_add_u32_e32 v121, 1, v115
	v_fma_f32 v126, -v120, v115, v99
	v_fma_f32 v127, -v121, v115, v99
	v_cmp_ge_f32_e64 s[6:7], 0, v126
	s_nop 1
	v_cndmask_b32_e64 v115, v115, v120, s[6:7]
	v_cmp_lt_f32_e64 s[6:7], 0, v127
	s_nop 1
	v_cndmask_b32_e64 v115, v115, v121, s[6:7]
	v_mul_f32_e32 v120, 0x37800000, v115
	v_cndmask_b32_e32 v115, v115, v120, vcc
	v_cmp_class_f32_e32 vcc, v99, v2
	s_nop 1
	v_cndmask_b32_e32 v99, v115, v99, vcc
	v_div_scale_f32 v115, s[0:1], v99, v99, 1.0
	v_rcp_f32_e32 v121, v115
	v_div_scale_f32 v120, vcc, 1.0, v99, 1.0
	v_fma_f32 v126, -v115, v121, 1.0
	v_fmac_f32_e32 v121, v126, v121
	v_mul_f32_e32 v126, v120, v121
	v_fma_f32 v127, -v115, v126, v120
	v_fmac_f32_e32 v126, v127, v121
	v_fma_f32 v115, -v115, v126, v120
	v_div_fmas_f32 v115, v115, v121, v126
	v_div_fixup_f32 v120, v115, v99, 1.0
	v_pk_mul_f32 v[100:101], v[100:101], v[120:121] op_sel_hi:[1,0]
	v_pk_mul_f32 v[102:103], v[102:103], v[120:121] op_sel_hi:[1,0]
	v_pk_fma_f32 v[100:101], v[130:131], v[100:101], v[134:135]
	v_pk_fma_f32 v[102:103], v[132:133], v[102:103], v[136:137]
	s_waitcnt vmcnt(15)
	v_pk_fma_f32 v[100:101], v[114:115], v[122:123], v[100:101] op_sel_hi:[0,1,1]
	v_pk_fma_f32 v[102:103], v[114:115], v[116:117], v[102:103] op_sel_hi:[0,1,1]
	v_pk_mul_f32 v[102:103], v[102:103], v[118:119]
	v_pk_mul_f32 v[100:101], v[100:101], v[124:125]
	s_nop 0
	v_cvt_pk_bf16_f32 v100, v100, v101
	v_cvt_pk_bf16_f32 v101, v102, v103
	global_store_dwordx2 v[112:113], v[100:101], off
	s_ashr_i32 s6, s18, 2
	s_and_b32 s0, s23, 0x300
	v_add_u32_e32 v112, s0, v0
	s_ashr_i32 s7, s6, 31
	s_lshl_b64 s[0:1], s[6:7], 10
	v_ashrrev_i32_e32 v113, 31, v112
	v_lshl_add_u64 v[100:101], s[0:1], 0, v[112:113]
	v_lshl_add_u64 v[104:105], v[100:101], 2, s[4:5]
	v_lshlrev_b64 v[106:107], 1, v[100:101]
	s_waitcnt lgkmcnt(0)
	global_load_dwordx4 v[100:103], v[104:105], off
	s_lshl_b64 s[16:17], s[6:7], 6
	v_ashrrev_i32_e32 v114, 6, v112
	s_add_u32 s16, s19, s16
	v_ashrrev_i32_e32 v115, 31, v114
	s_addc_u32 s17, s20, s17
	v_lshl_add_u64 v[116:117], s[12:13], 0, v[106:107]
	v_lshl_add_u64 v[118:119], s[14:15], 0, v[106:107]
	s_nop 0
	v_lshl_add_u64 v[114:115], v[114:115], 2, s[16:17]
	global_load_dwordx2 v[116:117], v[116:117], off
	s_nop 0
	global_load_dwordx2 v[118:119], v[118:119], off
	s_nop 0
	global_load_dword v114, v[114:115], off
	s_lshl_b64 s[0:1], s[6:7], 12
	s_add_u32 s0, s21, s0
	s_addc_u32 s1, s22, s1
	s_add_i32 s6, s18, 0x800
	s_add_i32 s23, s23, 0x80000
	s_cmpk_lt_i32 s18, 0x7800
	s_mov_b32 s18, s6
	v_lshl_add_u64 v[112:113], v[112:113], 1, s[0:1]
	s_cbranch_scc1 .LBB0_1879
	s_waitcnt vmcnt(18)
	v_mov_b32_e32 v24, v5
	v_mov_b32_e32 v25, v6
	v_mov_b32_e32 v26, v4
	v_mov_b32_e32 v27, v7
	v_pk_add_f32 v[24:25], v[24:25], v[26:27]
	s_waitcnt vmcnt(17)
	v_lshlrev_b32_e32 v26, 16, v20
	v_add_f32_e32 v3, v24, v25
	v_and_b32_e32 v27, 0xffff0000, v20
	v_lshlrev_b32_e32 v20, 16, v21
	v_add_f32_dpp v3, v3, v3 quad_perm:[1,0,3,2] row_mask:0xf bank_mask:0xf bound_ctrl:1
	v_and_b32_e32 v21, 0xffff0000, v21
	s_waitcnt vmcnt(16)
	v_lshlrev_b32_e32 v28, 16, v22
	v_add_f32_dpp v3, v3, v3 quad_perm:[2,3,0,1] row_mask:0xf bank_mask:0xf bound_ctrl:1
	v_and_b32_e32 v29, 0xffff0000, v22
	v_lshlrev_b32_e32 v22, 16, v23
	v_add_f32_dpp v3, v3, v3 row_half_mirror row_mask:0xf bank_mask:0xf bound_ctrl:1
	v_and_b32_e32 v23, 0xffff0000, v23
	s_nop 0
	v_add_f32_dpp v3, v3, v3 row_mirror row_mask:0xf bank_mask:0xf bound_ctrl:1
	v_fmamk_f32 v5, v3, 0xbc800000, v5
	v_fmamk_f32 v4, v3, 0xbc800000, v4
	v_fmamk_f32 v7, v3, 0xbc800000, v7
	v_fmac_f32_e32 v6, 0xbc800000, v3
	v_pk_mul_f32 v[24:25], v[6:7], v[6:7]
	v_pk_mul_f32 v[30:31], v[4:5], v[4:5]
	s_nop 0
	v_pk_mov_b32 v[32:33], v[30:31], v[24:25] op_sel:[1,0]
	v_mov_b32_e32 v31, v25
	v_pk_add_f32 v[24:25], v[32:33], v[30:31]
	s_nop 0
	v_add_f32_e32 v3, v24, v25
	s_nop 1
	v_add_f32_dpp v3, v3, v3 quad_perm:[1,0,3,2] row_mask:0xf bank_mask:0xf bound_ctrl:1
	s_nop 1
	v_add_f32_dpp v3, v3, v3 quad_perm:[2,3,0,1] row_mask:0xf bank_mask:0xf bound_ctrl:1
	s_nop 1
	v_add_f32_dpp v3, v3, v3 row_half_mirror row_mask:0xf bank_mask:0xf bound_ctrl:1
	s_nop 1
	v_add_f32_dpp v3, v3, v3 row_mirror row_mask:0xf bank_mask:0xf bound_ctrl:1
	v_fmamk_f32 v3, v3, 0x3c800000, v1
	v_mul_f32_e32 v19, 0x4f800000, v3
	v_cmp_gt_f32_e32 vcc, s24, v3
	s_nop 1
	v_cndmask_b32_e32 v3, v3, v19, vcc
	v_sqrt_f32_e32 v19, v3
	s_nop 0
	v_add_u32_e32 v24, -1, v19
	v_add_u32_e32 v25, 1, v19
	v_fma_f32 v30, -v24, v19, v3
	v_fma_f32 v31, -v25, v19, v3
	v_cmp_ge_f32_e64 s[6:7], 0, v30
	s_nop 1
	v_cndmask_b32_e64 v19, v19, v24, s[6:7]
	v_cmp_lt_f32_e64 s[6:7], 0, v31
	s_nop 1
	v_cndmask_b32_e64 v19, v19, v25, s[6:7]
	v_mul_f32_e32 v24, 0x37800000, v19
	v_cndmask_b32_e32 v19, v19, v24, vcc
	v_cmp_class_f32_e32 vcc, v3, v2
	s_nop 1
	v_cndmask_b32_e32 v3, v19, v3, vcc
	v_div_scale_f32 v19, s[0:1], v3, v3, 1.0
	v_rcp_f32_e32 v25, v19
	v_div_scale_f32 v24, vcc, 1.0, v3, 1.0
	v_fma_f32 v30, -v19, v25, 1.0
	v_fmac_f32_e32 v25, v30, v25
	v_mul_f32_e32 v30, v24, v25
	v_fma_f32 v31, -v19, v30, v24
	v_fmac_f32_e32 v30, v31, v25
	v_fma_f32 v19, -v19, v30, v24
	v_div_fmas_f32 v19, v19, v25, v30
	v_div_fixup_f32 v24, v19, v3, 1.0
	v_pk_mul_f32 v[4:5], v[4:5], v[24:25] op_sel_hi:[1,0]
	v_pk_mul_f32 v[6:7], v[6:7], v[24:25] op_sel_hi:[1,0]
	v_pk_fma_f32 v[4:5], v[130:131], v[4:5], v[134:135]
	v_pk_fma_f32 v[6:7], v[132:133], v[6:7], v[136:137]
	s_waitcnt vmcnt(15)
	v_pk_fma_f32 v[4:5], v[18:19], v[26:27], v[4:5] op_sel_hi:[0,1,1]
	v_pk_fma_f32 v[6:7], v[18:19], v[20:21], v[6:7] op_sel_hi:[0,1,1]
	v_pk_mul_f32 v[6:7], v[6:7], v[22:23]
	v_pk_mul_f32 v[4:5], v[4:5], v[28:29]
	s_nop 0
	v_cvt_pk_bf16_f32 v4, v4, v5
	v_cvt_pk_bf16_f32 v5, v6, v7
	global_store_dwordx2 v[16:17], v[4:5], off
	s_waitcnt vmcnt(14)
	v_mov_b32_e32 v56, v37
	v_mov_b32_e32 v57, v38
	v_mov_b32_e32 v58, v36
	v_mov_b32_e32 v59, v39
	v_pk_add_f32 v[56:57], v[56:57], v[58:59]
	s_waitcnt vmcnt(13)
	v_lshlrev_b32_e32 v58, 16, v52
	v_add_f32_e32 v35, v56, v57
	v_and_b32_e32 v59, 0xffff0000, v52
	v_lshlrev_b32_e32 v52, 16, v53
	v_add_f32_dpp v35, v35, v35 quad_perm:[1,0,3,2] row_mask:0xf bank_mask:0xf bound_ctrl:1
	v_and_b32_e32 v53, 0xffff0000, v53
	s_waitcnt vmcnt(12)
	v_lshlrev_b32_e32 v60, 16, v54
	v_add_f32_dpp v35, v35, v35 quad_perm:[2,3,0,1] row_mask:0xf bank_mask:0xf bound_ctrl:1
	v_and_b32_e32 v61, 0xffff0000, v54
	v_lshlrev_b32_e32 v54, 16, v55
	v_add_f32_dpp v35, v35, v35 row_half_mirror row_mask:0xf bank_mask:0xf bound_ctrl:1
	v_and_b32_e32 v55, 0xffff0000, v55
	s_nop 0
	v_add_f32_dpp v35, v35, v35 row_mirror row_mask:0xf bank_mask:0xf bound_ctrl:1
	v_fmamk_f32 v37, v35, 0xbc800000, v37
	v_fmamk_f32 v36, v35, 0xbc800000, v36
	v_fmamk_f32 v39, v35, 0xbc800000, v39
	v_fmac_f32_e32 v38, 0xbc800000, v35
	v_pk_mul_f32 v[56:57], v[38:39], v[38:39]
	v_pk_mul_f32 v[62:63], v[36:37], v[36:37]
	s_nop 0
	v_pk_mov_b32 v[64:65], v[62:63], v[56:57] op_sel:[1,0]
	v_mov_b32_e32 v63, v57
	v_pk_add_f32 v[56:57], v[64:65], v[62:63]
	s_nop 0
	v_add_f32_e32 v35, v56, v57
	s_nop 1
	v_add_f32_dpp v35, v35, v35 quad_perm:[1,0,3,2] row_mask:0xf bank_mask:0xf bound_ctrl:1
	s_nop 1
	v_add_f32_dpp v35, v35, v35 quad_perm:[2,3,0,1] row_mask:0xf bank_mask:0xf bound_ctrl:1
	s_nop 1
	v_add_f32_dpp v35, v35, v35 row_half_mirror row_mask:0xf bank_mask:0xf bound_ctrl:1
	s_nop 1
	v_add_f32_dpp v35, v35, v35 row_mirror row_mask:0xf bank_mask:0xf bound_ctrl:1
	v_fmamk_f32 v35, v35, 0x3c800000, v1
	v_mul_f32_e32 v51, 0x4f800000, v35
	v_cmp_gt_f32_e32 vcc, s24, v35
	s_nop 1
	v_cndmask_b32_e32 v35, v35, v51, vcc
	v_sqrt_f32_e32 v51, v35
	s_nop 0
	v_add_u32_e32 v56, -1, v51
	v_add_u32_e32 v57, 1, v51
	v_fma_f32 v62, -v56, v51, v35
	v_fma_f32 v63, -v57, v51, v35
	v_cmp_ge_f32_e64 s[6:7], 0, v62
	s_nop 1
	v_cndmask_b32_e64 v51, v51, v56, s[6:7]
	v_cmp_lt_f32_e64 s[6:7], 0, v63
	s_nop 1
	v_cndmask_b32_e64 v51, v51, v57, s[6:7]
	v_mul_f32_e32 v56, 0x37800000, v51
	v_cndmask_b32_e32 v51, v51, v56, vcc
	v_cmp_class_f32_e32 vcc, v35, v2
	s_nop 1
	v_cndmask_b32_e32 v35, v51, v35, vcc
	v_div_scale_f32 v51, s[0:1], v35, v35, 1.0
	v_rcp_f32_e32 v57, v51
	v_div_scale_f32 v56, vcc, 1.0, v35, 1.0
	v_fma_f32 v62, -v51, v57, 1.0
	v_fmac_f32_e32 v57, v62, v57
	v_mul_f32_e32 v62, v56, v57
	v_fma_f32 v63, -v51, v62, v56
	v_fmac_f32_e32 v62, v63, v57
	v_fma_f32 v51, -v51, v62, v56
	v_div_fmas_f32 v51, v51, v57, v62
	v_div_fixup_f32 v56, v51, v35, 1.0
	v_pk_mul_f32 v[36:37], v[36:37], v[56:57] op_sel_hi:[1,0]
	v_pk_mul_f32 v[38:39], v[38:39], v[56:57] op_sel_hi:[1,0]
	v_pk_fma_f32 v[36:37], v[130:131], v[36:37], v[134:135]
	v_pk_fma_f32 v[38:39], v[132:133], v[38:39], v[136:137]
	s_waitcnt vmcnt(11)
	v_pk_fma_f32 v[36:37], v[50:51], v[58:59], v[36:37] op_sel_hi:[0,1,1]
	v_pk_fma_f32 v[38:39], v[50:51], v[52:53], v[38:39] op_sel_hi:[0,1,1]
	v_pk_mul_f32 v[38:39], v[38:39], v[54:55]
	v_pk_mul_f32 v[36:37], v[36:37], v[60:61]
	s_nop 0
	v_cvt_pk_bf16_f32 v36, v36, v37
	v_cvt_pk_bf16_f32 v37, v38, v39
	global_store_dwordx2 v[48:49], v[36:37], off
	s_waitcnt vmcnt(10)
	v_mov_b32_e32 v88, v69
	v_mov_b32_e32 v89, v70
	v_mov_b32_e32 v90, v68
	v_mov_b32_e32 v91, v71
	v_pk_add_f32 v[88:89], v[88:89], v[90:91]
	s_waitcnt vmcnt(9)
	v_lshlrev_b32_e32 v90, 16, v84
	v_add_f32_e32 v67, v88, v89
	v_and_b32_e32 v91, 0xffff0000, v84
	v_lshlrev_b32_e32 v84, 16, v85
	v_add_f32_dpp v67, v67, v67 quad_perm:[1,0,3,2] row_mask:0xf bank_mask:0xf bound_ctrl:1
	v_and_b32_e32 v85, 0xffff0000, v85
	s_waitcnt vmcnt(8)
	v_lshlrev_b32_e32 v92, 16, v86
	v_add_f32_dpp v67, v67, v67 quad_perm:[2,3,0,1] row_mask:0xf bank_mask:0xf bound_ctrl:1
	v_and_b32_e32 v93, 0xffff0000, v86
	v_lshlrev_b32_e32 v86, 16, v87
	v_add_f32_dpp v67, v67, v67 row_half_mirror row_mask:0xf bank_mask:0xf bound_ctrl:1
	v_and_b32_e32 v87, 0xffff0000, v87
	s_nop 0
	v_add_f32_dpp v67, v67, v67 row_mirror row_mask:0xf bank_mask:0xf bound_ctrl:1
	v_fmamk_f32 v69, v67, 0xbc800000, v69
	v_fmamk_f32 v68, v67, 0xbc800000, v68
	v_fmamk_f32 v71, v67, 0xbc800000, v71
	v_fmac_f32_e32 v70, 0xbc800000, v67
	v_pk_mul_f32 v[88:89], v[70:71], v[70:71]
	v_pk_mul_f32 v[94:95], v[68:69], v[68:69]
	s_nop 0
	v_pk_mov_b32 v[96:97], v[94:95], v[88:89] op_sel:[1,0]
	v_mov_b32_e32 v95, v89
	v_pk_add_f32 v[88:89], v[96:97], v[94:95]
	s_nop 0
	v_add_f32_e32 v67, v88, v89
	s_nop 1
	v_add_f32_dpp v67, v67, v67 quad_perm:[1,0,3,2] row_mask:0xf bank_mask:0xf bound_ctrl:1
	s_nop 1
	v_add_f32_dpp v67, v67, v67 quad_perm:[2,3,0,1] row_mask:0xf bank_mask:0xf bound_ctrl:1
	s_nop 1
	v_add_f32_dpp v67, v67, v67 row_half_mirror row_mask:0xf bank_mask:0xf bound_ctrl:1
	s_nop 1
	v_add_f32_dpp v67, v67, v67 row_mirror row_mask:0xf bank_mask:0xf bound_ctrl:1
	v_fmamk_f32 v67, v67, 0x3c800000, v1
	v_mul_f32_e32 v83, 0x4f800000, v67
	v_cmp_gt_f32_e32 vcc, s24, v67
	s_nop 1
	v_cndmask_b32_e32 v67, v67, v83, vcc
	v_sqrt_f32_e32 v83, v67
	s_nop 0
	v_add_u32_e32 v88, -1, v83
	v_add_u32_e32 v89, 1, v83
	v_fma_f32 v94, -v88, v83, v67
	v_fma_f32 v95, -v89, v83, v67
	v_cmp_ge_f32_e64 s[6:7], 0, v94
	s_nop 1
	v_cndmask_b32_e64 v83, v83, v88, s[6:7]
	v_cmp_lt_f32_e64 s[6:7], 0, v95
	s_nop 1
	v_cndmask_b32_e64 v83, v83, v89, s[6:7]
	v_mul_f32_e32 v88, 0x37800000, v83
	v_cndmask_b32_e32 v83, v83, v88, vcc
	v_cmp_class_f32_e32 vcc, v67, v2
	s_nop 1
	v_cndmask_b32_e32 v67, v83, v67, vcc
	v_div_scale_f32 v83, s[0:1], v67, v67, 1.0
	v_rcp_f32_e32 v89, v83
	v_div_scale_f32 v88, vcc, 1.0, v67, 1.0
	v_fma_f32 v94, -v83, v89, 1.0
	v_fmac_f32_e32 v89, v94, v89
	v_mul_f32_e32 v94, v88, v89
	v_fma_f32 v95, -v83, v94, v88
	v_fmac_f32_e32 v94, v95, v89
	v_fma_f32 v83, -v83, v94, v88
	v_div_fmas_f32 v83, v83, v89, v94
	v_div_fixup_f32 v88, v83, v67, 1.0
	v_pk_mul_f32 v[68:69], v[68:69], v[88:89] op_sel_hi:[1,0]
	v_pk_mul_f32 v[70:71], v[70:71], v[88:89] op_sel_hi:[1,0]
	v_pk_fma_f32 v[68:69], v[130:131], v[68:69], v[134:135]
	v_pk_fma_f32 v[70:71], v[132:133], v[70:71], v[136:137]
	s_waitcnt vmcnt(7)
	v_pk_fma_f32 v[68:69], v[82:83], v[90:91], v[68:69] op_sel_hi:[0,1,1]
	v_pk_fma_f32 v[70:71], v[82:83], v[84:85], v[70:71] op_sel_hi:[0,1,1]
	v_pk_mul_f32 v[70:71], v[70:71], v[86:87]
	v_pk_mul_f32 v[68:69], v[68:69], v[92:93]
	s_nop 0
	v_cvt_pk_bf16_f32 v68, v68, v69
	v_cvt_pk_bf16_f32 v69, v70, v71
	global_store_dwordx2 v[80:81], v[68:69], off
	s_waitcnt vmcnt(6)
	v_mov_b32_e32 v120, v101
	v_mov_b32_e32 v121, v102
	v_mov_b32_e32 v122, v100
	v_mov_b32_e32 v123, v103
	v_pk_add_f32 v[120:121], v[120:121], v[122:123]
	s_waitcnt vmcnt(5)
	v_lshlrev_b32_e32 v122, 16, v116
	v_add_f32_e32 v99, v120, v121
	v_and_b32_e32 v123, 0xffff0000, v116
	v_lshlrev_b32_e32 v116, 16, v117
	v_add_f32_dpp v99, v99, v99 quad_perm:[1,0,3,2] row_mask:0xf bank_mask:0xf bound_ctrl:1
	v_and_b32_e32 v117, 0xffff0000, v117
	s_waitcnt vmcnt(4)
	v_lshlrev_b32_e32 v124, 16, v118
	v_add_f32_dpp v99, v99, v99 quad_perm:[2,3,0,1] row_mask:0xf bank_mask:0xf bound_ctrl:1
	v_and_b32_e32 v125, 0xffff0000, v118
	v_lshlrev_b32_e32 v118, 16, v119
	v_add_f32_dpp v99, v99, v99 row_half_mirror row_mask:0xf bank_mask:0xf bound_ctrl:1
	v_and_b32_e32 v119, 0xffff0000, v119
	s_nop 0
	v_add_f32_dpp v99, v99, v99 row_mirror row_mask:0xf bank_mask:0xf bound_ctrl:1
	v_fmamk_f32 v101, v99, 0xbc800000, v101
	v_fmamk_f32 v100, v99, 0xbc800000, v100
	v_fmamk_f32 v103, v99, 0xbc800000, v103
	v_fmac_f32_e32 v102, 0xbc800000, v99
	v_pk_mul_f32 v[120:121], v[102:103], v[102:103]
	v_pk_mul_f32 v[126:127], v[100:101], v[100:101]
	s_nop 0
	v_pk_mov_b32 v[128:129], v[126:127], v[120:121] op_sel:[1,0]
	v_mov_b32_e32 v127, v121
	v_pk_add_f32 v[120:121], v[128:129], v[126:127]
	s_nop 0
	v_add_f32_e32 v99, v120, v121
	s_nop 1
	v_add_f32_dpp v99, v99, v99 quad_perm:[1,0,3,2] row_mask:0xf bank_mask:0xf bound_ctrl:1
	s_nop 1
	v_add_f32_dpp v99, v99, v99 quad_perm:[2,3,0,1] row_mask:0xf bank_mask:0xf bound_ctrl:1
	s_nop 1
	v_add_f32_dpp v99, v99, v99 row_half_mirror row_mask:0xf bank_mask:0xf bound_ctrl:1
	s_nop 1
	v_add_f32_dpp v99, v99, v99 row_mirror row_mask:0xf bank_mask:0xf bound_ctrl:1
	v_fmamk_f32 v99, v99, 0x3c800000, v1
	v_mul_f32_e32 v115, 0x4f800000, v99
	v_cmp_gt_f32_e32 vcc, s24, v99
	s_nop 1
	v_cndmask_b32_e32 v99, v99, v115, vcc
	v_sqrt_f32_e32 v115, v99
	s_nop 0
	v_add_u32_e32 v120, -1, v115
	v_add_u32_e32 v121, 1, v115
	v_fma_f32 v126, -v120, v115, v99
	v_fma_f32 v127, -v121, v115, v99
	v_cmp_ge_f32_e64 s[6:7], 0, v126
	s_nop 1
	v_cndmask_b32_e64 v115, v115, v120, s[6:7]
	v_cmp_lt_f32_e64 s[6:7], 0, v127
	s_nop 1
	v_cndmask_b32_e64 v115, v115, v121, s[6:7]
	v_mul_f32_e32 v120, 0x37800000, v115
	v_cndmask_b32_e32 v115, v115, v120, vcc
	v_cmp_class_f32_e32 vcc, v99, v2
	s_nop 1
	v_cndmask_b32_e32 v99, v115, v99, vcc
	v_div_scale_f32 v115, s[0:1], v99, v99, 1.0
	v_rcp_f32_e32 v121, v115
	v_div_scale_f32 v120, vcc, 1.0, v99, 1.0
	v_fma_f32 v126, -v115, v121, 1.0
	v_fmac_f32_e32 v121, v126, v121
	v_mul_f32_e32 v126, v120, v121
	v_fma_f32 v127, -v115, v126, v120
	v_fmac_f32_e32 v126, v127, v121
	v_fma_f32 v115, -v115, v126, v120
	v_div_fmas_f32 v115, v115, v121, v126
	v_div_fixup_f32 v120, v115, v99, 1.0
	v_pk_mul_f32 v[100:101], v[100:101], v[120:121] op_sel_hi:[1,0]
	v_pk_mul_f32 v[102:103], v[102:103], v[120:121] op_sel_hi:[1,0]
	v_pk_fma_f32 v[100:101], v[130:131], v[100:101], v[134:135]
	v_pk_fma_f32 v[102:103], v[132:133], v[102:103], v[136:137]
	s_waitcnt vmcnt(3)
	v_pk_fma_f32 v[100:101], v[114:115], v[122:123], v[100:101] op_sel_hi:[0,1,1]
	v_pk_fma_f32 v[102:103], v[114:115], v[116:117], v[102:103] op_sel_hi:[0,1,1]
	v_pk_mul_f32 v[102:103], v[102:103], v[118:119]
	v_pk_mul_f32 v[100:101], v[100:101], v[124:125]
	s_nop 0
	v_cvt_pk_bf16_f32 v100, v100, v101
	v_cvt_pk_bf16_f32 v101, v102, v103
	global_store_dwordx2 v[112:113], v[100:101], off
	v_readlane_b32 s0, v254, 18
	v_readlane_b32 s1, v254, 19
	s_load_dwordx2 s[6:7], s[0:1], 0x188

.LBB0_2446:
	s_or_b64 exec, exec, s[4:5]
	s_waitcnt lgkmcnt(0)
	v_mov_b32_e32 v0, s2
	s_barrier
	v_mbcnt_lo_u32_b32 v4, -1, 0
	v_mbcnt_hi_u32_b32 v4, -1, v4
	s_mov_b32 s8, 0
	v_readfirstlane_b32 s16, v0
	v_mov_b32_e32 v0, 0
	s_load_dwordx4 s[4:7], s[48:49], 0x178
	s_load_dwordx2 s[0:1], s[48:49], 0x188
	v_readfirstlane_b32 s2, v0
	s_ashr_i32 s3, s2, 31
	v_ashrrev_i32_e32 v5, 31, v4
	v_lshlrev_b64 v[0:1], 4, v[4:5]
	s_waitcnt lgkmcnt(0)
	s_add_u32 s2, s0, s2
	s_addc_u32 s3, s1, s3
	v_lshl_add_u64 v[2:3], s[2:3], 0, v[0:1]
	s_mov_b64 s[0:1], 0x2bc80000
	s_add_u32 s9, s2, 0x460000
	v_lshl_add_u64 v[6:7], v[2:3], 0, s[0:1]
	v_lshl_add_u64 v[2:3], v[4:5], 3, s[2:3]
	s_mov_b64 s[0:1], 0x48a80000
	s_addc_u32 s10, s3, 0
	v_lshl_add_u64 v[8:9], v[2:3], 0, s[0:1]
	v_lshl_add_u64 v[10:11], s[4:5], 0, v[0:1]
	s_mov_b64 s[0:1], 0x1000
	s_add_u32 s11, s2, 0x470000
	v_lshl_add_u64 v[12:13], v[10:11], 0, s[0:1]
	s_mov_b64 s[0:1], 0x1400
	s_addc_u32 s12, s3, 0
	v_lshl_add_u64 v[14:15], v[10:11], 0, s[0:1]
	s_mov_b64 s[0:1], 0x1800
	s_add_u32 s13, s2, 0x480000
	v_lshl_add_u64 v[16:17], v[10:11], 0, s[0:1]
	s_mov_b64 s[0:1], 0x1c00
	s_addc_u32 s14, s3, 0
	s_lshl_b32 s15, s16, 5
	v_lshlrev_b32_e32 v2, 2, v4
	v_lshl_add_u64 v[18:19], v[10:11], 0, s[0:1]
	s_lshl_b32 s0, s16, 6
	v_readlane_b32 s1, v254, 22
	v_mov_b32_e32 v24, 0
	s_add_i32 s15, s15, s76
	v_xor_b32_e32 v25, 64, v2
	v_xor_b32_e32 v26, 0x80, v2
	v_lshl_add_u64 v[20:21], s[6:7], 0, v[0:1]
	s_add_i32 s4, s0, s1
	s_add_i32 s16, 0, 0x27c40
	s_mov_b64 s[6:7], 0x40a000
	s_movk_i32 s17, 0x1000
	s_mov_b32 s18, 0x40b000
	v_mov_b32_e32 v27, 0x358637bd
	s_mov_b32 s19, 0xf800000
	v_mov_b32_e32 v28, 0x260
	s_add_i32 s0, s4, 0
	s_ashr_i32 s1, s0, 31
	s_lshl_b64 s[22:23], s[0:1], 2
	s_add_u32 s20, s9, s22
	s_addc_u32 s21, s10, s23
	global_load_dwordx2 v[212:213], v24, s[20:21]
	s_add_u32 s20, s11, s22
	s_addc_u32 s21, s12, s23
	global_load_dwordx2 v[214:215], v24, s[20:21]
	s_add_u32 s20, s13, s22
	s_addc_u32 s21, s14, s23
	global_load_dwordx2 v[216:217], v24, s[20:21]
	s_add_i32 s0, s4, 16
	s_ashr_i32 s1, s0, 31
	s_lshl_b64 s[22:23], s[0:1], 2
	s_add_u32 s20, s9, s22
	s_addc_u32 s21, s10, s23
	global_load_dwordx2 v[218:219], v24, s[20:21]
	s_add_u32 s20, s11, s22
	s_addc_u32 s21, s12, s23
	global_load_dwordx2 v[220:221], v24, s[20:21]
	s_add_u32 s20, s13, s22
	s_addc_u32 s21, s14, s23
	global_load_dwordx2 v[222:223], v24, s[20:21]
	s_add_i32 s0, s4, 32
	s_ashr_i32 s1, s0, 31
	s_lshl_b64 s[22:23], s[0:1], 2
	s_add_u32 s20, s9, s22
	s_addc_u32 s21, s10, s23
	global_load_dwordx2 v[224:225], v24, s[20:21]
	s_add_u32 s20, s11, s22
	s_addc_u32 s21, s12, s23
	global_load_dwordx2 v[226:227], v24, s[20:21]
	s_add_u32 s20, s13, s22
	s_addc_u32 s21, s14, s23
	global_load_dwordx2 v[228:229], v24, s[20:21]
	s_add_i32 s0, s4, 48
	s_ashr_i32 s1, s0, 31
	s_lshl_b64 s[22:23], s[0:1], 2
	s_add_u32 s20, s9, s22
	s_addc_u32 s21, s10, s23
	global_load_dwordx2 v[230:231], v24, s[20:21]
	s_add_u32 s20, s11, s22
	s_addc_u32 s21, s12, s23
	global_load_dwordx2 v[232:233], v24, s[20:21]
	s_add_u32 s20, s13, s22
	s_addc_u32 s21, s14, s23
	global_load_dwordx2 v[234:235], v24, s[20:21]
	global_load_dwordx4 v[176:179], v[10:11], off
	global_load_dwordx4 v[180:183], v[10:11], off offset:1024
	global_load_dwordx4 v[184:187], v[10:11], off offset:2048
	global_load_dwordx4 v[188:191], v[10:11], off offset:3072
	global_load_dwordx4 v[192:195], v[12:13], off
	global_load_dwordx4 v[196:199], v[14:15], off
	global_load_dwordx4 v[200:203], v[16:17], off
	global_load_dwordx4 v[204:207], v[18:19], off
	s_waitcnt vmcnt(0)
.LBB0_2447:
	s_add_i32 s0, s15, s8
	s_ashr_i32 s1, s0, 31
	s_lshr_b32 s5, s1, 21
	s_add_i32 s5, s0, s5
	s_ashr_i32 s5, s5, 11
	s_add_i32 s5, s5, 4
	s_mul_hi_i32 s21, s5, 0xc000
	s_mul_i32 s5, s5, 0xc000
	s_add_u32 s20, s2, s5
	s_addc_u32 s21, s3, s21
	s_ashr_i32 s5, s4, 31
	s_lshl_b64 s[22:23], s[4:5], 2
	v_lshl_add_u64 v[22:23], v[4:5], 4, s[20:21]
	s_add_u32 s20, s9, s22
	v_lshl_add_u64 v[62:63], v[22:23], 0, s[6:7]
	v_add_co_u32_e32 v22, vcc, s18, v22
	s_nop 0
	v_addc_co_u32_e32 v23, vcc, 0, v23, vcc
	s_addc_u32 s21, s10, s23
	global_load_dwordx4 v[30:33], v[62:63], off offset:1024
	global_load_dwordx4 v[34:37], v[62:63], off offset:2048
	global_load_dwordx4 v[38:41], v[62:63], off offset:3072
	global_load_dwordx4 v[42:45], v[22:23], off offset:-4096
	global_load_dwordx4 v[46:49], v[22:23], off
	global_load_dwordx4 v[50:53], v[22:23], off offset:1024
	global_load_dwordx4 v[54:57], v[22:23], off offset:2048
	global_load_dwordx4 v[58:61], v[22:23], off offset:3072
	v_mov_b64_e32 v[94:95], v[212:213]
	v_mov_b32_e32 v29, v214
	v_mov_b32_e32 v97, v215
	v_mov_b32_e32 v96, v216
	v_mov_b32_e32 v98, v217
	v_mov_b64_e32 v[212:213], v[218:219]
	v_mov_b64_e32 v[214:215], v[220:221]
	v_mov_b64_e32 v[216:217], v[222:223]
	v_mov_b64_e32 v[218:219], v[224:225]
	v_mov_b64_e32 v[220:221], v[226:227]
	v_mov_b64_e32 v[222:223], v[228:229]
	v_mov_b64_e32 v[224:225], v[230:231]
	v_mov_b64_e32 v[226:227], v[232:233]
	v_mov_b64_e32 v[228:229], v[234:235]
	s_add_u32 s20, s11, s22
	s_addc_u32 s21, s12, s23
	s_add_i32 s24, s4, 1
	s_ashr_i32 s25, s24, 31
	s_lshl_b64 s[20:21], s[24:25], 2
	s_add_u32 s24, s11, s20
	s_addc_u32 s25, s12, s21
	s_add_u32 s22, s13, s22
	s_addc_u32 s23, s14, s23
	s_add_u32 s20, s13, s20
	s_addc_u32 s21, s14, s21
	s_lshl_b64 s[0:1], s[0:1], 13
	v_lshl_add_u64 v[78:79], v[6:7], 0, s[0:1]
	v_add_co_u32_e32 v100, vcc, s17, v78
	v_addc_co_u32_e32 v101, vcc, 0, v79, vcc
	global_load_dwordx4 v[62:65], v[78:79], off
	global_load_dwordx4 v[66:69], v[78:79], off offset:1024
	global_load_dwordx4 v[70:73], v[78:79], off offset:2048
	global_load_dwordx4 v[74:77], v[78:79], off offset:3072
	s_nop 0
	global_load_dwordx4 v[78:81], v[100:101], off
	global_load_dwordx4 v[82:85], v[100:101], off offset:1024
	global_load_dwordx4 v[86:89], v[100:101], off offset:2048
	global_load_dwordx4 v[90:93], v[100:101], off offset:3072
	v_lshl_add_u64 v[22:23], v[20:21], 0, s[0:1]
	s_add_i32 s8, s8, 8
	s_add_i32 s4, s4, 16
	s_cmp_lg_u32 s8, 32
	v_lshlrev_b32_e32 v94, 2, v94
	v_lshlrev_b32_e32 v95, 2, v95
	v_add_u32_e32 v94, s16, v94
	v_add_u32_e32 v95, s16, v95
	ds_read_b32 v94, v94
	ds_read_b32 v95, v95
	s_waitcnt lgkmcnt(1)
	v_lshlrev_b32_e32 v94, 8, v94
	s_waitcnt lgkmcnt(0)
	v_lshlrev_b32_e32 v95, 8, v95
	v_add_u32_e32 v94, v94, v29
	v_add_u32_e32 v100, v95, v97
	v_ashrrev_i32_e32 v95, 31, v94
	v_ashrrev_i32_e32 v101, 31, v100
	v_lshlrev_b64 v[94:95], 12, v[94:95]
	v_lshlrev_b64 v[100:101], 12, v[100:101]
	v_lshl_add_u64 v[94:95], v[8:9], 0, v[94:95]
	v_lshl_add_u64 v[100:101], v[8:9], 0, v[100:101]
	global_load_dwordx2 v[102:103], v[94:95], off
	global_load_dwordx2 v[104:105], v[100:101], off
	global_load_dwordx2 v[106:107], v[94:95], off offset:512
	global_load_dwordx2 v[108:109], v[100:101], off offset:512
	global_load_dwordx2 v[110:111], v[94:95], off offset:1024
	global_load_dwordx2 v[112:113], v[100:101], off offset:1024
	global_load_dwordx2 v[114:115], v[94:95], off offset:1536
	global_load_dwordx2 v[116:117], v[100:101], off offset:1536
	global_load_dwordx2 v[118:119], v[94:95], off offset:2048
	global_load_dwordx2 v[120:121], v[100:101], off offset:2048
	global_load_dwordx2 v[122:123], v[94:95], off offset:2560
	global_load_dwordx2 v[124:125], v[100:101], off offset:2560
	global_load_dwordx2 v[126:127], v[94:95], off offset:3072
	global_load_dwordx2 v[128:129], v[100:101], off offset:3072
	s_nop 0
	global_load_dwordx2 v[94:95], v[94:95], off offset:3584
	s_nop 0
	global_load_dwordx2 v[100:101], v[100:101], off offset:3584
	s_waitcnt vmcnt(15)
	v_lshlrev_b32_e32 v130, 16, v102
	s_waitcnt vmcnt(14)
	v_lshlrev_b32_e32 v132, 16, v104
	v_and_b32_e32 v133, 0xffff0000, v104
	v_lshlrev_b32_e32 v104, 16, v105
	v_and_b32_e32 v105, 0xffff0000, v105
	s_waitcnt vmcnt(12)
	v_lshlrev_b32_e32 v136, 16, v108
	v_and_b32_e32 v137, 0xffff0000, v108
	v_lshlrev_b32_e32 v108, 16, v109
	v_and_b32_e32 v109, 0xffff0000, v109
	v_and_b32_e32 v131, 0xffff0000, v102
	v_lshlrev_b32_e32 v102, 16, v103
	v_and_b32_e32 v103, 0xffff0000, v103
	v_lshlrev_b32_e32 v134, 16, v106
	v_and_b32_e32 v135, 0xffff0000, v106
	v_lshlrev_b32_e32 v106, 16, v107
	v_and_b32_e32 v107, 0xffff0000, v107
	s_waitcnt vmcnt(10)
	v_lshlrev_b32_e32 v140, 16, v112
	v_and_b32_e32 v141, 0xffff0000, v112
	v_lshlrev_b32_e32 v112, 16, v113
	v_and_b32_e32 v113, 0xffff0000, v113
	v_pk_mul_f32 v[104:105], v[98:99], v[104:105] op_sel_hi:[0,1]
	v_pk_mul_f32 v[132:133], v[98:99], v[132:133] op_sel_hi:[0,1]
	v_pk_mul_f32 v[108:109], v[98:99], v[108:109] op_sel_hi:[0,1]
	v_pk_mul_f32 v[136:137], v[98:99], v[136:137] op_sel_hi:[0,1]
	v_lshlrev_b32_e32 v138, 16, v110
	v_and_b32_e32 v139, 0xffff0000, v110
	v_lshlrev_b32_e32 v110, 16, v111
	v_and_b32_e32 v111, 0xffff0000, v111
	v_pk_mul_f32 v[140:141], v[98:99], v[140:141] op_sel_hi:[0,1]
	v_pk_mul_f32 v[112:113], v[98:99], v[112:113] op_sel_hi:[0,1]
	v_pk_fma_f32 v[130:131], v[96:97], v[130:131], v[132:133] op_sel_hi:[0,1,1]
	v_pk_fma_f32 v[102:103], v[96:97], v[102:103], v[104:105] op_sel_hi:[0,1,1]
	v_pk_fma_f32 v[104:105], v[96:97], v[134:135], v[136:137] op_sel_hi:[0,1,1]
	v_pk_fma_f32 v[106:107], v[96:97], v[106:107], v[108:109] op_sel_hi:[0,1,1]
	s_waitcnt vmcnt(8)
	v_lshlrev_b32_e32 v144, 16, v116
	v_and_b32_e32 v145, 0xffff0000, v116
	v_lshlrev_b32_e32 v116, 16, v117
	v_and_b32_e32 v117, 0xffff0000, v117
	s_waitcnt vmcnt(4)
	v_lshlrev_b32_e32 v152, 16, v124
	v_and_b32_e32 v153, 0xffff0000, v124
	v_lshlrev_b32_e32 v124, 16, v125
	v_and_b32_e32 v125, 0xffff0000, v125
	s_waitcnt vmcnt(2)
	v_lshlrev_b32_e32 v156, 16, v128
	v_and_b32_e32 v157, 0xffff0000, v128
	v_pk_fma_f32 v[108:109], v[96:97], v[110:111], v[112:113] op_sel_hi:[0,1,1]
	v_pk_fma_f32 v[110:111], v[96:97], v[138:139], v[140:141] op_sel_hi:[0,1,1]
	v_pk_fma_f32 v[44:45], v[44:45], v[102:103], v[64:65]
	v_pk_fma_f32 v[42:43], v[42:43], v[130:131], v[62:63]
	v_pk_fma_f32 v[32:33], v[32:33], v[106:107], v[68:69]
	v_pk_fma_f32 v[30:31], v[30:31], v[104:105], v[66:67]
	v_lshlrev_b32_e32 v142, 16, v114
	v_and_b32_e32 v143, 0xffff0000, v114
	v_lshlrev_b32_e32 v114, 16, v115
	v_and_b32_e32 v115, 0xffff0000, v115
	v_lshlrev_b32_e32 v148, 16, v120
	v_and_b32_e32 v149, 0xffff0000, v120
	v_lshlrev_b32_e32 v120, 16, v121
	v_and_b32_e32 v121, 0xffff0000, v121
	v_lshlrev_b32_e32 v150, 16, v122
	v_and_b32_e32 v151, 0xffff0000, v122
	v_lshlrev_b32_e32 v122, 16, v123
	v_and_b32_e32 v123, 0xffff0000, v123
	v_lshlrev_b32_e32 v154, 16, v126
	v_and_b32_e32 v155, 0xffff0000, v126
	v_pk_mul_f32 v[116:117], v[98:99], v[116:117] op_sel_hi:[0,1]
	v_pk_mul_f32 v[144:145], v[98:99], v[144:145] op_sel_hi:[0,1]
	v_pk_mul_f32 v[124:125], v[98:99], v[124:125] op_sel_hi:[0,1]
	v_pk_mul_f32 v[156:157], v[98:99], v[156:157] op_sel_hi:[0,1]
	v_pk_fma_f32 v[34:35], v[34:35], v[110:111], v[70:71]
	v_pk_fma_f32 v[36:37], v[36:37], v[108:109], v[72:73]
	v_mov_b32_e32 v64, v43
	v_mov_b32_e32 v65, v31
	v_mov_b32_e32 v68, v45
	v_mov_b32_e32 v69, v33
	v_lshlrev_b32_e32 v146, 16, v118
	v_and_b32_e32 v147, 0xffff0000, v118
	v_lshlrev_b32_e32 v118, 16, v119
	v_and_b32_e32 v119, 0xffff0000, v119
	v_lshlrev_b32_e32 v128, 16, v129
	v_and_b32_e32 v129, 0xffff0000, v129
	v_pk_mul_f32 v[120:121], v[98:99], v[120:121] op_sel_hi:[0,1]
	v_pk_mul_f32 v[148:149], v[98:99], v[148:149] op_sel_hi:[0,1]
	v_pk_fma_f32 v[112:113], v[96:97], v[142:143], v[144:145] op_sel_hi:[0,1,1]
	v_pk_fma_f32 v[114:115], v[96:97], v[114:115], v[116:117] op_sel_hi:[0,1,1]
	v_pk_fma_f32 v[122:123], v[96:97], v[122:123], v[124:125] op_sel_hi:[0,1,1]
	v_pk_fma_f32 v[124:125], v[96:97], v[154:155], v[156:157] op_sel_hi:[0,1,1]
	v_mov_b32_e32 v62, v42
	v_mov_b32_e32 v63, v30
	v_mov_b32_e32 v66, v44
	v_mov_b32_e32 v67, v32
	v_pk_mul_f32 v[70:71], v[36:37], v[36:37]
	v_pk_mul_f32 v[72:73], v[34:35], v[34:35]
	v_pk_mul_f32 v[64:65], v[64:65], v[64:65]
	v_pk_mul_f32 v[68:69], v[68:69], v[68:69]
	v_lshlrev_b32_e32 v126, 16, v127
	v_and_b32_e32 v127, 0xffff0000, v127
	v_pk_mul_f32 v[152:153], v[98:99], v[152:153] op_sel_hi:[0,1]
	v_pk_mul_f32 v[128:129], v[98:99], v[128:129] op_sel_hi:[0,1]
	v_pk_fma_f32 v[116:117], v[96:97], v[146:147], v[148:149] op_sel_hi:[0,1,1]
	v_pk_fma_f32 v[118:119], v[96:97], v[118:119], v[120:121] op_sel_hi:[0,1,1]
	v_pk_fma_f32 v[40:41], v[40:41], v[114:115], v[76:77]
	v_pk_fma_f32 v[38:39], v[38:39], v[112:113], v[74:75]
	v_pk_fma_f32 v[54:55], v[54:55], v[124:125], v[86:87]
	v_pk_mov_b32 v[86:87], v[72:73], v[70:71] op_sel:[1,0]
	v_mov_b32_e32 v73, v71
	v_pk_fma_f32 v[62:63], v[62:63], v[62:63], v[64:65]
	v_pk_fma_f32 v[64:65], v[66:67], v[66:67], v[68:69]
	v_pk_fma_f32 v[120:121], v[96:97], v[150:151], v[152:153] op_sel_hi:[0,1,1]
	v_pk_fma_f32 v[126:127], v[96:97], v[126:127], v[128:129] op_sel_hi:[0,1,1]
	v_pk_fma_f32 v[48:49], v[48:49], v[118:119], v[80:81]
	v_pk_fma_f32 v[46:47], v[46:47], v[116:117], v[78:79]
	v_mul_f32_e32 v74, v39, v39
	v_mul_f32_e32 v76, v41, v41
	v_pk_add_f32 v[66:67], v[86:87], v[72:73]
	v_pk_add_f32 v[62:63], v[62:63], v[64:65]
	s_waitcnt vmcnt(0)
	v_lshlrev_b32_e32 v160, 16, v100
	v_and_b32_e32 v161, 0xffff0000, v100
	v_lshlrev_b32_e32 v100, 16, v101
	v_and_b32_e32 v101, 0xffff0000, v101
	v_pk_fma_f32 v[52:53], v[52:53], v[122:123], v[84:85]
	v_pk_fma_f32 v[50:51], v[50:51], v[120:121], v[82:83]
	v_pk_fma_f32 v[56:57], v[56:57], v[126:127], v[88:89]
	v_mul_f32_e32 v29, v46, v46
	v_mul_f32_e32 v85, v47, v47
	v_mul_f32_e32 v88, v48, v48
	v_mul_f32_e32 v89, v49, v49
	v_pk_fma_f32 v[70:71], v[38:39], v[38:39], v[74:75] op_sel_hi:[1,1,0]
	v_pk_fma_f32 v[74:75], v[40:41], v[40:41], v[76:77] op_sel_hi:[1,1,0]
	v_pk_add_f32 v[64:65], v[66:67], v[66:67] op_sel:[0,1] op_sel_hi:[1,0]
	v_pk_add_f32 v[62:63], v[62:63], v[62:63] op_sel:[0,1] op_sel_hi:[1,0]
	v_lshlrev_b32_e32 v158, 16, v94
	v_and_b32_e32 v159, 0xffff0000, v94
	v_lshlrev_b32_e32 v94, 16, v95
	v_and_b32_e32 v95, 0xffff0000, v95
	v_pk_mul_f32 v[100:101], v[98:99], v[100:101] op_sel_hi:[0,1]
	v_pk_mul_f32 v[98:99], v[98:99], v[160:161] op_sel_hi:[0,1]
	v_pk_mul_f32 v[78:79], v[52:53], v[52:53]
	v_pk_mul_f32 v[80:81], v[50:51], v[50:51]
	v_mov_b32_e32 v71, v88
	v_mov_b32_e32 v75, v89
	v_mov_b32_e32 v65, v85
	v_mov_b32_e32 v63, v29
	v_pk_fma_f32 v[98:99], v[96:97], v[158:159], v[98:99] op_sel_hi:[0,1,1]
	v_pk_fma_f32 v[94:95], v[96:97], v[94:95], v[100:101] op_sel_hi:[0,1,1]
	v_pk_mov_b32 v[76:77], v[80:81], v[78:79] op_sel:[1,0]
	v_mov_b32_e32 v81, v79
	v_pk_add_f32 v[66:67], v[70:71], v[74:75]
	v_pk_add_f32 v[62:63], v[62:63], v[64:65]
	v_pk_fma_f32 v[60:61], v[60:61], v[94:95], v[92:93]
	v_pk_fma_f32 v[58:59], v[58:59], v[98:99], v[90:91]
	v_mul_f32_e32 v82, v55, v55
	v_mul_f32_e32 v84, v57, v57
	v_pk_add_f32 v[68:69], v[76:77], v[80:81]
	v_pk_add_f32 v[62:63], v[62:63], v[66:67]
	v_mul_f32_e32 v90, v58, v58
	v_mul_f32_e32 v91, v59, v59
	v_mul_f32_e32 v92, v60, v60
	v_mul_f32_e32 v93, v61, v61
	v_pk_fma_f32 v[78:79], v[54:55], v[54:55], v[82:83] op_sel_hi:[1,1,0]
	v_pk_fma_f32 v[82:83], v[56:57], v[56:57], v[84:85] op_sel_hi:[1,1,0]
	v_pk_add_f32 v[68:69], v[68:69], v[68:69] op_sel:[0,1] op_sel_hi:[1,0]
	v_pk_add_f32 v[62:63], v[62:63], v[62:63] op_sel:[0,1] op_sel_hi:[1,0]
	v_mov_b32_e32 v79, v92
	v_mov_b32_e32 v83, v93
	v_mov_b32_e32 v69, v91
	v_mov_b32_e32 v63, v90
	v_pk_add_f32 v[70:71], v[78:79], v[82:83]
	v_pk_add_f32 v[62:63], v[62:63], v[68:69]
	s_nop 0
	v_pk_add_f32 v[62:63], v[62:63], v[70:71]
	s_nop 0
	v_add_f32_e32 v29, v62, v63
	s_nop 1
	v_add_f32_dpp v29, v29, v29 quad_perm:[1,0,3,2] row_mask:0xf bank_mask:0xf bound_ctrl:1
	s_nop 1
	v_add_f32_dpp v29, v29, v29 quad_perm:[2,3,0,1] row_mask:0xf bank_mask:0xf bound_ctrl:1
	s_nop 1
	v_add_f32_dpp v29, v29, v29 row_half_mirror row_mask:0xf bank_mask:0xf bound_ctrl:1
	s_nop 1
	v_add_f32_dpp v29, v29, v29 row_mirror row_mask:0xf bank_mask:0xf bound_ctrl:1
	ds_bpermute_b32 v62, v25, v29
	s_waitcnt lgkmcnt(0)
	v_add_f32_e32 v29, v29, v62
	ds_bpermute_b32 v62, v26, v29
	s_waitcnt lgkmcnt(0)
	v_add_f32_e32 v29, v29, v62
	v_fmamk_f32 v29, v29, 0x3a000000, v27
	v_mul_f32_e32 v62, 0x4f800000, v29
	v_cmp_gt_f32_e32 vcc, s19, v29
	s_nop 1
	v_cndmask_b32_e32 v29, v29, v62, vcc
	v_sqrt_f32_e32 v62, v29
	s_nop 0
	v_add_u32_e32 v63, -1, v62
	v_add_u32_e32 v64, 1, v62
	v_fma_f32 v65, -v63, v62, v29
	v_fma_f32 v66, -v64, v62, v29
	v_cmp_ge_f32_e64 s[0:1], 0, v65
	s_nop 1
	v_cndmask_b32_e64 v62, v62, v63, s[0:1]
	v_cmp_lt_f32_e64 s[0:1], 0, v66
	s_nop 1
	v_cndmask_b32_e64 v62, v62, v64, s[0:1]
	v_mul_f32_e32 v63, 0x37800000, v62
	v_cndmask_b32_e32 v62, v62, v63, vcc
	v_cmp_class_f32_e32 vcc, v29, v28
	s_nop 1
	v_cndmask_b32_e32 v29, v62, v29, vcc
	v_div_scale_f32 v62, s[0:1], v29, v29, 1.0
	v_rcp_f32_e32 v64, v62
	v_div_scale_f32 v63, vcc, 1.0, v29, 1.0
	v_fma_f32 v65, -v62, v64, 1.0
	v_fmac_f32_e32 v64, v65, v64
	v_mul_f32_e32 v65, v63, v64
	v_fma_f32 v66, -v62, v65, v63
	v_fmac_f32_e32 v65, v66, v64
	v_fma_f32 v62, -v62, v65, v63
	v_div_fmas_f32 v62, v62, v64, v65
	v_div_fixup_f32 v62, v62, v29, 1.0
	v_pk_mul_f32 v[42:43], v[42:43], v[62:63] op_sel_hi:[1,0]
	v_pk_mul_f32 v[44:45], v[44:45], v[62:63] op_sel_hi:[1,0]
	v_pk_mul_f32 v[0:1], v[176:177], v[42:43]
	v_pk_mul_f32 v[2:3], v[178:179], v[44:45]
	global_store_dwordx4 v[22:23], v[0:3], off
	v_pk_mul_f32 v[32:33], v[32:33], v[62:63] op_sel_hi:[1,0]
	v_pk_mul_f32 v[30:31], v[30:31], v[62:63] op_sel_hi:[1,0]
	v_pk_mul_f32 v[210:211], v[182:183], v[32:33]
	v_pk_mul_f32 v[208:209], v[180:181], v[30:31]
	global_store_dwordx4 v[22:23], v[208:211], off offset:1024
	v_pk_mul_f32 v[30:31], v[36:37], v[62:63] op_sel_hi:[1,0]
	v_pk_mul_f32 v[32:33], v[34:35], v[62:63] op_sel_hi:[1,0]
	v_pk_mul_f32 v[2:3], v[186:187], v[30:31]
	v_pk_mul_f32 v[0:1], v[184:185], v[32:33]
	global_store_dwordx4 v[22:23], v[0:3], off offset:2048
	v_pk_mul_f32 v[30:31], v[40:41], v[62:63] op_sel_hi:[1,0]
	v_pk_mul_f32 v[32:33], v[38:39], v[62:63] op_sel_hi:[1,0]
	v_pk_mul_f32 v[210:211], v[190:191], v[30:31]
	v_pk_mul_f32 v[208:209], v[188:189], v[32:33]
	global_store_dwordx4 v[22:23], v[208:211], off offset:3072
	v_add_co_u32_e32 v22, vcc, s17, v22
	v_pk_mul_f32 v[30:31], v[48:49], v[62:63] op_sel_hi:[1,0]
	v_pk_mul_f32 v[32:33], v[46:47], v[62:63] op_sel_hi:[1,0]
	v_addc_co_u32_e32 v23, vcc, 0, v23, vcc
	v_pk_mul_f32 v[0:1], v[192:193], v[32:33]
	v_pk_mul_f32 v[2:3], v[194:195], v[30:31]
	global_store_dwordx4 v[22:23], v[0:3], off
	v_pk_mul_f32 v[30:31], v[52:53], v[62:63] op_sel_hi:[1,0]
	v_pk_mul_f32 v[32:33], v[50:51], v[62:63] op_sel_hi:[1,0]
	v_pk_mul_f32 v[210:211], v[198:199], v[30:31]
	v_pk_mul_f32 v[208:209], v[196:197], v[32:33]
	global_store_dwordx4 v[22:23], v[208:211], off offset:1024
	v_pk_mul_f32 v[30:31], v[56:57], v[62:63] op_sel_hi:[1,0]
	v_pk_mul_f32 v[32:33], v[54:55], v[62:63] op_sel_hi:[1,0]
	v_pk_mul_f32 v[2:3], v[202:203], v[30:31]
	v_pk_mul_f32 v[0:1], v[200:201], v[32:33]
	global_store_dwordx4 v[22:23], v[0:3], off offset:2048
	v_pk_mul_f32 v[30:31], v[60:61], v[62:63] op_sel_hi:[1,0]
	v_pk_mul_f32 v[32:33], v[58:59], v[62:63] op_sel_hi:[1,0]
	v_pk_mul_f32 v[210:211], v[206:207], v[30:31]
	v_pk_mul_f32 v[208:209], v[204:205], v[32:33]
	global_store_dwordx4 v[22:23], v[208:211], off offset:3072
	s_cbranch_scc1 .LBB0_2447
	s_endpgm
